# first K-iteration (segments 1-2) peeled with C=0 MFMAs: no accumulator zeroing per unit
# speedup vs baseline: 1.0242x; 1.0023x over previous
.LBB0_294:
	s_andn2_b64 vcc, exec, s[8:9]
	s_waitcnt lgkmcnt(0)
	s_cbranch_vccnz .Lzs_0
	s_add_i32 s14, s71, 0x80
	s_addk_i32 s70, 0x100
	s_mov_b32 s71, 0
	ds_read_b128 v[160:163], v144
	ds_read_b128 v[164:167], v145
	ds_read_b128 v[168:171], v140
	ds_read_b128 v[172:175], v141
	ds_read_b128 v[176:179], v146
	ds_read_b128 v[180:183], v147
	ds_read_b128 v[184:187], v148
	ds_read_b128 v[188:191], v149
	s_add_i32 s72, s14, 0x80
	s_cmp_eq_u32 s54, s71
	s_cselect_b32 s73, s13, s70
	s_cselect_b32 s72, s15, s72
	v_add_u32_e32 v159, s14, v157
	s_add_i32 m0, s22, 0xc000
	ds_read_b128 v[192:195], v158
	ds_read_b128 v[196:199], v158 offset:1024
	ds_read_b128 v[200:203], v158 offset:2048
	ds_read_b128 v[204:207], v158 offset:3072
	ds_read_b128 v[214:217], v158 offset:4096
	ds_read_b128 v[218:221], v158 offset:5120
	ds_read_b128 v[222:225], v158 offset:6144
	ds_read_b128 v[226:229], v158 offset:7168
	global_load_lds_dwordx4 v159, s[4:5]
	v_add_u32_e32 v159, s14, v156
	s_add_i32 m0, s22, 0xe000
	s_nop 0
	global_load_lds_dwordx4 v159, s[4:5]
	s_waitcnt vmcnt(8)
	s_waitcnt lgkmcnt(0)
	s_barrier
	s_setprio 1
	s_waitcnt lgkmcnt(0)
	v_mfma_f32_16x16x32_bf16 v[122:125], v[168:171], v[192:195], 0
	v_mfma_f32_16x16x32_bf16 v[126:129], v[164:167], v[192:195], 0
	v_mfma_f32_16x16x32_bf16 v[110:113], v[168:171], v[200:203], 0
	v_mfma_f32_16x16x32_bf16 v[106:109], v[164:167], v[200:203], 0
	v_mfma_f32_16x16x32_bf16 v[94:97], v[168:171], v[214:217], 0
	v_mfma_f32_16x16x32_bf16 v[90:93], v[164:167], v[214:217], 0
	v_mfma_f32_16x16x32_bf16 v[78:81], v[168:171], v[222:225], 0
	v_mfma_f32_16x16x32_bf16 v[74:77], v[164:167], v[222:225], 0
	v_mfma_f32_16x16x32_bf16 v[122:125], v[160:163], v[196:199], v[122:125]
	v_mfma_f32_16x16x32_bf16 v[126:129], v[176:179], v[196:199], v[126:129]
	v_mfma_f32_16x16x32_bf16 v[110:113], v[160:163], v[204:207], v[110:113]
	v_mfma_f32_16x16x32_bf16 v[106:109], v[176:179], v[204:207], v[106:109]
	v_mfma_f32_16x16x32_bf16 v[94:97], v[160:163], v[218:221], v[94:97]
	v_mfma_f32_16x16x32_bf16 v[90:93], v[176:179], v[218:221], v[90:93]
	v_mfma_f32_16x16x32_bf16 v[78:81], v[160:163], v[226:229], v[78:81]
	v_mfma_f32_16x16x32_bf16 v[74:77], v[176:179], v[226:229], v[74:77]
	s_setprio 0
	s_setprio 1
	v_mfma_f32_16x16x32_bf16 v[118:121], v[172:175], v[192:195], 0
	v_mfma_f32_16x16x32_bf16 v[114:117], v[184:187], v[192:195], 0
	v_mfma_f32_16x16x32_bf16 v[102:105], v[172:175], v[200:203], 0
	v_mfma_f32_16x16x32_bf16 v[98:101], v[184:187], v[200:203], 0
	v_mfma_f32_16x16x32_bf16 v[86:89], v[172:175], v[214:217], 0
	v_mfma_f32_16x16x32_bf16 v[82:85], v[184:187], v[214:217], 0
	v_mfma_f32_16x16x32_bf16 v[70:73], v[172:175], v[222:225], 0
	v_mfma_f32_16x16x32_bf16 v[66:69], v[184:187], v[222:225], 0
	v_mfma_f32_16x16x32_bf16 v[118:121], v[180:183], v[196:199], v[118:121]
	v_mfma_f32_16x16x32_bf16 v[114:117], v[188:191], v[196:199], v[114:117]
	v_mfma_f32_16x16x32_bf16 v[102:105], v[180:183], v[204:207], v[102:105]
	v_mfma_f32_16x16x32_bf16 v[98:101], v[188:191], v[204:207], v[98:101]
	v_mfma_f32_16x16x32_bf16 v[86:89], v[180:183], v[218:221], v[86:89]
	v_mfma_f32_16x16x32_bf16 v[82:85], v[188:191], v[218:221], v[82:85]
	v_mfma_f32_16x16x32_bf16 v[70:73], v[180:183], v[226:229], v[70:73]
	v_mfma_f32_16x16x32_bf16 v[66:69], v[188:191], v[226:229], v[66:69]
	s_setprio 0
	s_barrier
	s_mov_b32 m0, s23
	v_add_u32_e32 v159, s73, v134
	ds_read_b128 v[192:195], v158 offset:16384
	ds_read_b128 v[196:199], v158 offset:17408
	ds_read_b128 v[200:203], v158 offset:18432
	ds_read_b128 v[204:207], v158 offset:19456
	ds_read_b128 v[214:217], v158 offset:20480
	ds_read_b128 v[218:221], v158 offset:21504
	ds_read_b128 v[222:225], v158 offset:22528
	ds_read_b128 v[226:229], v158 offset:23552
	global_load_lds_dwordx4 v159, s[20:21]
	v_add_u32_e32 v159, s17, v159
	s_mov_b32 m0, s28
	s_nop 0
	global_load_lds_dwordx4 v159, s[20:21]
	v_add_u32_e32 v159, s73, v135
	s_mov_b32 m0, s29
	s_nop 0
	global_load_lds_dwordx4 v159, s[20:21]
	v_add_u32_e32 v159, s17, v159
	s_mov_b32 m0, s30
	s_nop 0
	global_load_lds_dwordx4 v159, s[20:21]
	v_add_u32_e32 v159, s72, v1
	s_mov_b32 m0, s22
	s_nop 0
	global_load_lds_dwordx4 v159, s[4:5]
	v_add_u32_e32 v159, s16, v159
	s_mov_b32 m0, s31
	s_nop 0
	global_load_lds_dwordx4 v159, s[4:5]
	s_waitcnt vmcnt(8)
	s_waitcnt lgkmcnt(0)
	s_barrier
	s_setprio 1
	s_waitcnt lgkmcnt(0)
	v_mfma_f32_16x16x32_bf16 v[62:65], v[168:171], v[192:195], 0
	v_mfma_f32_16x16x32_bf16 v[58:61], v[164:167], v[192:195], 0
	v_mfma_f32_16x16x32_bf16 v[46:49], v[168:171], v[200:203], 0
	v_mfma_f32_16x16x32_bf16 v[42:45], v[164:167], v[200:203], 0
	v_mfma_f32_16x16x32_bf16 v[30:33], v[168:171], v[214:217], 0
	v_mfma_f32_16x16x32_bf16 v[26:29], v[164:167], v[214:217], 0
	v_mfma_f32_16x16x32_bf16 v[14:17], v[168:171], v[222:225], 0
	v_mfma_f32_16x16x32_bf16 v[10:13], v[164:167], v[222:225], 0
	v_mfma_f32_16x16x32_bf16 v[62:65], v[160:163], v[196:199], v[62:65]
	v_mfma_f32_16x16x32_bf16 v[58:61], v[176:179], v[196:199], v[58:61]
	v_mfma_f32_16x16x32_bf16 v[46:49], v[160:163], v[204:207], v[46:49]
	v_mfma_f32_16x16x32_bf16 v[42:45], v[176:179], v[204:207], v[42:45]
	v_mfma_f32_16x16x32_bf16 v[30:33], v[160:163], v[218:221], v[30:33]
	v_mfma_f32_16x16x32_bf16 v[26:29], v[176:179], v[218:221], v[26:29]
	v_mfma_f32_16x16x32_bf16 v[14:17], v[160:163], v[226:229], v[14:17]
	v_mfma_f32_16x16x32_bf16 v[10:13], v[176:179], v[226:229], v[10:13]
	s_setprio 0
	s_setprio 1
	v_mfma_f32_16x16x32_bf16 v[54:57], v[172:175], v[192:195], 0
	v_mfma_f32_16x16x32_bf16 v[50:53], v[184:187], v[192:195], 0
	v_mfma_f32_16x16x32_bf16 v[38:41], v[172:175], v[200:203], 0
	v_mfma_f32_16x16x32_bf16 v[34:37], v[184:187], v[200:203], 0
	v_mfma_f32_16x16x32_bf16 v[22:25], v[172:175], v[214:217], 0
	v_mfma_f32_16x16x32_bf16 v[18:21], v[184:187], v[214:217], 0
	v_mfma_f32_16x16x32_bf16 v[6:9], v[172:175], v[222:225], 0
	v_mfma_f32_16x16x32_bf16 v[2:5], v[184:187], v[222:225], 0
	v_mfma_f32_16x16x32_bf16 v[54:57], v[180:183], v[196:199], v[54:57]
	v_mfma_f32_16x16x32_bf16 v[50:53], v[188:191], v[196:199], v[50:53]
	v_mfma_f32_16x16x32_bf16 v[38:41], v[180:183], v[204:207], v[38:41]
	v_mfma_f32_16x16x32_bf16 v[34:37], v[188:191], v[204:207], v[34:37]
	v_mfma_f32_16x16x32_bf16 v[22:25], v[180:183], v[218:221], v[22:25]
	v_mfma_f32_16x16x32_bf16 v[18:21], v[188:191], v[218:221], v[18:21]
	v_mfma_f32_16x16x32_bf16 v[6:9], v[180:183], v[226:229], v[6:9]
	v_mfma_f32_16x16x32_bf16 v[2:5], v[188:191], v[226:229], v[2:5]
	s_setprio 0
	s_barrier
	s_branch .Lmid_0

.Lmid_0:
	ds_read_b128 v[160:163], v150
	ds_read_b128 v[164:167], v151
	ds_read_b128 v[168:171], v142
	ds_read_b128 v[172:175], v143
	ds_read_b128 v[176:179], v152
	ds_read_b128 v[180:183], v153
	ds_read_b128 v[184:187], v154
	ds_read_b128 v[188:191], v155
	s_mov_b32 m0, s35
	v_add_u32_e32 v159, s72, v136
	ds_read_b128 v[192:195], v158 offset:32768
	ds_read_b128 v[196:199], v158 offset:33792
	ds_read_b128 v[200:203], v158 offset:34816
	ds_read_b128 v[204:207], v158 offset:35840
	ds_read_b128 v[214:217], v158 offset:36864
	ds_read_b128 v[218:221], v158 offset:37888
	ds_read_b128 v[222:225], v158 offset:38912
	ds_read_b128 v[226:229], v158 offset:39936
	global_load_lds_dwordx4 v159, s[4:5]
	v_add_u32_e32 v159, s16, v159
	s_mov_b32 m0, s44
	s_nop 0
	global_load_lds_dwordx4 v159, s[4:5]
	s_waitcnt vmcnt(8)
	s_waitcnt lgkmcnt(0)
	s_barrier
	s_setprio 1
	s_waitcnt lgkmcnt(0)
	v_mfma_f32_16x16x32_bf16 v[122:125], v[168:171], v[192:195], v[122:125]
	v_mfma_f32_16x16x32_bf16 v[126:129], v[164:167], v[192:195], v[126:129]
	v_mfma_f32_16x16x32_bf16 v[110:113], v[168:171], v[200:203], v[110:113]
	v_mfma_f32_16x16x32_bf16 v[106:109], v[164:167], v[200:203], v[106:109]
	v_mfma_f32_16x16x32_bf16 v[94:97], v[168:171], v[214:217], v[94:97]
	v_mfma_f32_16x16x32_bf16 v[90:93], v[164:167], v[214:217], v[90:93]
	v_mfma_f32_16x16x32_bf16 v[78:81], v[168:171], v[222:225], v[78:81]
	v_mfma_f32_16x16x32_bf16 v[74:77], v[164:167], v[222:225], v[74:77]
	v_mfma_f32_16x16x32_bf16 v[122:125], v[160:163], v[196:199], v[122:125]
	v_mfma_f32_16x16x32_bf16 v[126:129], v[176:179], v[196:199], v[126:129]
	v_mfma_f32_16x16x32_bf16 v[110:113], v[160:163], v[204:207], v[110:113]
	v_mfma_f32_16x16x32_bf16 v[106:109], v[176:179], v[204:207], v[106:109]
	v_mfma_f32_16x16x32_bf16 v[94:97], v[160:163], v[218:221], v[94:97]
	v_mfma_f32_16x16x32_bf16 v[90:93], v[176:179], v[218:221], v[90:93]
	v_mfma_f32_16x16x32_bf16 v[78:81], v[160:163], v[226:229], v[78:81]
	v_mfma_f32_16x16x32_bf16 v[74:77], v[176:179], v[226:229], v[74:77]
	s_setprio 0
	s_setprio 1
	v_mfma_f32_16x16x32_bf16 v[118:121], v[172:175], v[192:195], v[118:121]
	v_mfma_f32_16x16x32_bf16 v[114:117], v[184:187], v[192:195], v[114:117]
	v_mfma_f32_16x16x32_bf16 v[102:105], v[172:175], v[200:203], v[102:105]
	v_mfma_f32_16x16x32_bf16 v[98:101], v[184:187], v[200:203], v[98:101]
	v_mfma_f32_16x16x32_bf16 v[86:89], v[172:175], v[214:217], v[86:89]
	v_mfma_f32_16x16x32_bf16 v[82:85], v[184:187], v[214:217], v[82:85]
	v_mfma_f32_16x16x32_bf16 v[70:73], v[172:175], v[222:225], v[70:73]
	v_mfma_f32_16x16x32_bf16 v[66:69], v[184:187], v[222:225], v[66:69]
	v_mfma_f32_16x16x32_bf16 v[118:121], v[180:183], v[196:199], v[118:121]
	v_mfma_f32_16x16x32_bf16 v[114:117], v[188:191], v[196:199], v[114:117]
	v_mfma_f32_16x16x32_bf16 v[102:105], v[180:183], v[204:207], v[102:105]
	v_mfma_f32_16x16x32_bf16 v[98:101], v[188:191], v[204:207], v[98:101]
	v_mfma_f32_16x16x32_bf16 v[86:89], v[180:183], v[218:221], v[86:89]
	v_mfma_f32_16x16x32_bf16 v[82:85], v[188:191], v[218:221], v[82:85]
	v_mfma_f32_16x16x32_bf16 v[70:73], v[180:183], v[226:229], v[70:73]
	v_mfma_f32_16x16x32_bf16 v[66:69], v[188:191], v[226:229], v[66:69]
	s_setprio 0
	s_barrier
	s_addk_i32 s73, 0x80
	s_mov_b32 m0, s46
	v_add_u32_e32 v159, s73, v134
	ds_read_b128 v[192:195], v158 offset:49152
	ds_read_b128 v[196:199], v158 offset:50176
	ds_read_b128 v[200:203], v158 offset:51200
	ds_read_b128 v[204:207], v158 offset:52224
	ds_read_b128 v[214:217], v158 offset:53248
	ds_read_b128 v[218:221], v158 offset:54272
	ds_read_b128 v[222:225], v158 offset:55296
	ds_read_b128 v[226:229], v158 offset:56320
	global_load_lds_dwordx4 v159, s[20:21]
	v_add_u32_e32 v159, s17, v159
	s_mov_b32 m0, s47
	s_nop 0
	global_load_lds_dwordx4 v159, s[20:21]
	v_add_u32_e32 v159, s73, v135
	s_mov_b32 m0, s50
	s_nop 0
	global_load_lds_dwordx4 v159, s[20:21]
	v_add_u32_e32 v159, s17, v159
	s_mov_b32 m0, s51
	s_nop 0
	global_load_lds_dwordx4 v159, s[20:21]
	v_add_u32_e32 v159, s72, v137
	s_mov_b32 m0, s48
	s_nop 0
	global_load_lds_dwordx4 v159, s[4:5]
	v_add_u32_e32 v159, s16, v159
	s_mov_b32 m0, s49
	s_nop 0
	global_load_lds_dwordx4 v159, s[4:5]
	s_waitcnt vmcnt(8)
	s_waitcnt lgkmcnt(0)
	s_barrier
	s_setprio 1
	s_waitcnt lgkmcnt(0)
	v_mfma_f32_16x16x32_bf16 v[62:65], v[168:171], v[192:195], v[62:65]
	v_mfma_f32_16x16x32_bf16 v[58:61], v[164:167], v[192:195], v[58:61]
	v_mfma_f32_16x16x32_bf16 v[46:49], v[168:171], v[200:203], v[46:49]
	v_mfma_f32_16x16x32_bf16 v[42:45], v[164:167], v[200:203], v[42:45]
	v_mfma_f32_16x16x32_bf16 v[30:33], v[168:171], v[214:217], v[30:33]
	v_mfma_f32_16x16x32_bf16 v[26:29], v[164:167], v[214:217], v[26:29]
	v_mfma_f32_16x16x32_bf16 v[14:17], v[168:171], v[222:225], v[14:17]
	v_mfma_f32_16x16x32_bf16 v[10:13], v[164:167], v[222:225], v[10:13]
	v_mfma_f32_16x16x32_bf16 v[62:65], v[160:163], v[196:199], v[62:65]
	v_mfma_f32_16x16x32_bf16 v[58:61], v[176:179], v[196:199], v[58:61]
	v_mfma_f32_16x16x32_bf16 v[46:49], v[160:163], v[204:207], v[46:49]
	v_mfma_f32_16x16x32_bf16 v[42:45], v[176:179], v[204:207], v[42:45]
	v_mfma_f32_16x16x32_bf16 v[30:33], v[160:163], v[218:221], v[30:33]
	v_mfma_f32_16x16x32_bf16 v[26:29], v[176:179], v[218:221], v[26:29]
	v_mfma_f32_16x16x32_bf16 v[14:17], v[160:163], v[226:229], v[14:17]
	v_mfma_f32_16x16x32_bf16 v[10:13], v[176:179], v[226:229], v[10:13]
	s_setprio 0
	s_setprio 1
	v_mfma_f32_16x16x32_bf16 v[54:57], v[172:175], v[192:195], v[54:57]
	v_mfma_f32_16x16x32_bf16 v[50:53], v[184:187], v[192:195], v[50:53]
	v_mfma_f32_16x16x32_bf16 v[38:41], v[172:175], v[200:203], v[38:41]
	v_mfma_f32_16x16x32_bf16 v[34:37], v[184:187], v[200:203], v[34:37]
	v_mfma_f32_16x16x32_bf16 v[22:25], v[172:175], v[214:217], v[22:25]
	v_mfma_f32_16x16x32_bf16 v[18:21], v[184:187], v[214:217], v[18:21]
	v_mfma_f32_16x16x32_bf16 v[6:9], v[172:175], v[222:225], v[6:9]
	v_mfma_f32_16x16x32_bf16 v[2:5], v[184:187], v[222:225], v[2:5]
	v_mfma_f32_16x16x32_bf16 v[54:57], v[180:183], v[196:199], v[54:57]
	v_mfma_f32_16x16x32_bf16 v[50:53], v[188:191], v[196:199], v[50:53]
	v_mfma_f32_16x16x32_bf16 v[38:41], v[180:183], v[204:207], v[38:41]
	v_mfma_f32_16x16x32_bf16 v[34:37], v[188:191], v[204:207], v[34:37]
	v_mfma_f32_16x16x32_bf16 v[22:25], v[180:183], v[218:221], v[22:25]
	v_mfma_f32_16x16x32_bf16 v[18:21], v[188:191], v[218:221], v[18:21]
	v_mfma_f32_16x16x32_bf16 v[6:9], v[180:183], v[226:229], v[6:9]
	v_mfma_f32_16x16x32_bf16 v[2:5], v[188:191], v[226:229], v[2:5]
	s_setprio 0
	s_barrier
	s_add_i32 s71, s71, 2
	s_addk_i32 s14, 0x100
	s_addk_i32 s70, 0x100
	s_cmp_ge_i32 s71, s52
	s_cbranch_scc0 .LBB0_296

.LBB0_601:
	s_andn2_b64 vcc, exec, s[10:11]
	s_cbranch_vccnz .Lzs_1
	s_add_i32 s16, s74, 0x80
	s_addk_i32 s73, 0x100
	s_mov_b32 s74, 0
	ds_read_b128 v[164:167], v147
	ds_read_b128 v[168:171], v148
	ds_read_b128 v[172:175], v143
	ds_read_b128 v[176:179], v144
	ds_read_b128 v[180:183], v149
	ds_read_b128 v[184:187], v150
	ds_read_b128 v[188:191], v151
	ds_read_b128 v[192:195], v152
	s_add_i32 s75, s16, 0x80
	s_cmp_eq_u32 s59, s74
	s_cselect_b32 s76, s17, s73
	s_cselect_b32 s75, s72, s75
	v_add_u32_e32 v134, s16, v160
	s_add_i32 m0, s28, 0xc000
	ds_read_b128 v[196:199], v161
	ds_read_b128 v[200:203], v161 offset:1024
	ds_read_b128 v[204:207], v161 offset:2048
	ds_read_b128 v[214:217], v161 offset:3072
	ds_read_b128 v[218:221], v161 offset:4096
	ds_read_b128 v[222:225], v161 offset:5120
	ds_read_b128 v[226:229], v161 offset:6144
	ds_read_b128 v[230:233], v161 offset:7168
	global_load_lds_dwordx4 v134, s[4:5]
	v_add_u32_e32 v134, s16, v159
	s_add_i32 m0, s28, 0xe000
	s_nop 0
	global_load_lds_dwordx4 v134, s[4:5]
	s_waitcnt vmcnt(8)
	s_waitcnt lgkmcnt(0)
	s_barrier
	s_setprio 1
	s_waitcnt lgkmcnt(0)
	v_mfma_f32_16x16x32_bf16 v[126:129], v[172:175], v[196:199], 0
	v_mfma_f32_16x16x32_bf16 v[122:125], v[168:171], v[196:199], 0
	v_mfma_f32_16x16x32_bf16 v[110:113], v[172:175], v[204:207], 0
	v_mfma_f32_16x16x32_bf16 v[106:109], v[168:171], v[204:207], 0
	v_mfma_f32_16x16x32_bf16 v[94:97], v[172:175], v[218:221], 0
	v_mfma_f32_16x16x32_bf16 v[90:93], v[168:171], v[218:221], 0
	v_mfma_f32_16x16x32_bf16 v[78:81], v[172:175], v[226:229], 0
	v_mfma_f32_16x16x32_bf16 v[74:77], v[168:171], v[226:229], 0
	v_mfma_f32_16x16x32_bf16 v[126:129], v[164:167], v[200:203], v[126:129]
	v_mfma_f32_16x16x32_bf16 v[122:125], v[180:183], v[200:203], v[122:125]
	v_mfma_f32_16x16x32_bf16 v[110:113], v[164:167], v[214:217], v[110:113]
	v_mfma_f32_16x16x32_bf16 v[106:109], v[180:183], v[214:217], v[106:109]
	v_mfma_f32_16x16x32_bf16 v[94:97], v[164:167], v[222:225], v[94:97]
	v_mfma_f32_16x16x32_bf16 v[90:93], v[180:183], v[222:225], v[90:93]
	v_mfma_f32_16x16x32_bf16 v[78:81], v[164:167], v[230:233], v[78:81]
	v_mfma_f32_16x16x32_bf16 v[74:77], v[180:183], v[230:233], v[74:77]
	s_setprio 0
	s_setprio 1
	v_mfma_f32_16x16x32_bf16 v[118:121], v[176:179], v[196:199], 0
	v_mfma_f32_16x16x32_bf16 v[114:117], v[188:191], v[196:199], 0
	v_mfma_f32_16x16x32_bf16 v[102:105], v[176:179], v[204:207], 0
	v_mfma_f32_16x16x32_bf16 v[98:101], v[188:191], v[204:207], 0
	v_mfma_f32_16x16x32_bf16 v[86:89], v[176:179], v[218:221], 0
	v_mfma_f32_16x16x32_bf16 v[82:85], v[188:191], v[218:221], 0
	v_mfma_f32_16x16x32_bf16 v[70:73], v[176:179], v[226:229], 0
	v_mfma_f32_16x16x32_bf16 v[66:69], v[188:191], v[226:229], 0
	v_mfma_f32_16x16x32_bf16 v[118:121], v[184:187], v[200:203], v[118:121]
	v_mfma_f32_16x16x32_bf16 v[114:117], v[192:195], v[200:203], v[114:117]
	v_mfma_f32_16x16x32_bf16 v[102:105], v[184:187], v[214:217], v[102:105]
	v_mfma_f32_16x16x32_bf16 v[98:101], v[192:195], v[214:217], v[98:101]
	v_mfma_f32_16x16x32_bf16 v[86:89], v[184:187], v[222:225], v[86:89]
	v_mfma_f32_16x16x32_bf16 v[82:85], v[192:195], v[222:225], v[82:85]
	v_mfma_f32_16x16x32_bf16 v[70:73], v[184:187], v[230:233], v[70:73]
	v_mfma_f32_16x16x32_bf16 v[66:69], v[192:195], v[230:233], v[66:69]
	s_setprio 0
	s_barrier
	s_mov_b32 m0, s29
	v_add_u32_e32 v134, s76, v135
	ds_read_b128 v[196:199], v161 offset:16384
	ds_read_b128 v[200:203], v161 offset:17408
	ds_read_b128 v[204:207], v161 offset:18432
	ds_read_b128 v[214:217], v161 offset:19456
	ds_read_b128 v[218:221], v161 offset:20480
	ds_read_b128 v[222:225], v161 offset:21504
	ds_read_b128 v[226:229], v161 offset:22528
	ds_read_b128 v[230:233], v161 offset:23552
	global_load_lds_dwordx4 v134, s[6:7]
	v_add_u32_e32 v134, s23, v134
	s_mov_b32 m0, s30
	s_nop 0
	global_load_lds_dwordx4 v134, s[6:7]
	v_add_u32_e32 v134, s76, v138
	s_mov_b32 m0, s31
	s_nop 0
	global_load_lds_dwordx4 v134, s[6:7]
	v_add_u32_e32 v134, s23, v134
	s_mov_b32 m0, s35
	s_nop 0
	global_load_lds_dwordx4 v134, s[6:7]
	v_add_u32_e32 v134, s75, v1
	s_mov_b32 m0, s28
	s_nop 0
	global_load_lds_dwordx4 v134, s[4:5]
	v_add_u32_e32 v134, s22, v134
	s_mov_b32 m0, s44
	s_nop 0
	global_load_lds_dwordx4 v134, s[4:5]
	s_waitcnt vmcnt(8)
	s_waitcnt lgkmcnt(0)
	s_barrier
	s_setprio 1
	s_waitcnt lgkmcnt(0)
	v_mfma_f32_16x16x32_bf16 v[62:65], v[172:175], v[196:199], 0
	v_mfma_f32_16x16x32_bf16 v[58:61], v[168:171], v[196:199], 0
	v_mfma_f32_16x16x32_bf16 v[46:49], v[172:175], v[204:207], 0
	v_mfma_f32_16x16x32_bf16 v[42:45], v[168:171], v[204:207], 0
	v_mfma_f32_16x16x32_bf16 v[30:33], v[172:175], v[218:221], 0
	v_mfma_f32_16x16x32_bf16 v[26:29], v[168:171], v[218:221], 0
	v_mfma_f32_16x16x32_bf16 v[14:17], v[172:175], v[226:229], 0
	v_mfma_f32_16x16x32_bf16 v[10:13], v[168:171], v[226:229], 0
	v_mfma_f32_16x16x32_bf16 v[62:65], v[164:167], v[200:203], v[62:65]
	v_mfma_f32_16x16x32_bf16 v[58:61], v[180:183], v[200:203], v[58:61]
	v_mfma_f32_16x16x32_bf16 v[46:49], v[164:167], v[214:217], v[46:49]
	v_mfma_f32_16x16x32_bf16 v[42:45], v[180:183], v[214:217], v[42:45]
	v_mfma_f32_16x16x32_bf16 v[30:33], v[164:167], v[222:225], v[30:33]
	v_mfma_f32_16x16x32_bf16 v[26:29], v[180:183], v[222:225], v[26:29]
	v_mfma_f32_16x16x32_bf16 v[14:17], v[164:167], v[230:233], v[14:17]
	v_mfma_f32_16x16x32_bf16 v[10:13], v[180:183], v[230:233], v[10:13]
	s_setprio 0
	s_setprio 1
	v_mfma_f32_16x16x32_bf16 v[54:57], v[176:179], v[196:199], 0
	v_mfma_f32_16x16x32_bf16 v[50:53], v[188:191], v[196:199], 0
	v_mfma_f32_16x16x32_bf16 v[38:41], v[176:179], v[204:207], 0
	v_mfma_f32_16x16x32_bf16 v[34:37], v[188:191], v[204:207], 0
	v_mfma_f32_16x16x32_bf16 v[22:25], v[176:179], v[218:221], 0
	v_mfma_f32_16x16x32_bf16 v[18:21], v[188:191], v[218:221], 0
	v_mfma_f32_16x16x32_bf16 v[6:9], v[176:179], v[226:229], 0
	v_mfma_f32_16x16x32_bf16 v[2:5], v[188:191], v[226:229], 0
	v_mfma_f32_16x16x32_bf16 v[54:57], v[184:187], v[200:203], v[54:57]
	v_mfma_f32_16x16x32_bf16 v[50:53], v[192:195], v[200:203], v[50:53]
	v_mfma_f32_16x16x32_bf16 v[38:41], v[184:187], v[214:217], v[38:41]
	v_mfma_f32_16x16x32_bf16 v[34:37], v[192:195], v[214:217], v[34:37]
	v_mfma_f32_16x16x32_bf16 v[22:25], v[184:187], v[222:225], v[22:25]
	v_mfma_f32_16x16x32_bf16 v[18:21], v[192:195], v[222:225], v[18:21]
	v_mfma_f32_16x16x32_bf16 v[6:9], v[184:187], v[230:233], v[6:9]
	v_mfma_f32_16x16x32_bf16 v[2:5], v[192:195], v[230:233], v[2:5]
	s_setprio 0
	s_barrier
	s_branch .Lmid_1

.Lmid_1:
	ds_read_b128 v[164:167], v153
	ds_read_b128 v[168:171], v154
	ds_read_b128 v[172:175], v145
	ds_read_b128 v[176:179], v146
	ds_read_b128 v[180:183], v155
	ds_read_b128 v[184:187], v156
	ds_read_b128 v[188:191], v157
	ds_read_b128 v[192:195], v158
	s_mov_b32 m0, s45
	v_add_u32_e32 v134, s75, v139
	ds_read_b128 v[196:199], v161 offset:32768
	ds_read_b128 v[200:203], v161 offset:33792
	ds_read_b128 v[204:207], v161 offset:34816
	ds_read_b128 v[214:217], v161 offset:35840
	ds_read_b128 v[218:221], v161 offset:36864
	ds_read_b128 v[222:225], v161 offset:37888
	ds_read_b128 v[226:229], v161 offset:38912
	ds_read_b128 v[230:233], v161 offset:39936
	global_load_lds_dwordx4 v134, s[4:5]
	v_add_u32_e32 v134, s22, v134
	s_mov_b32 m0, s46
	s_nop 0
	global_load_lds_dwordx4 v134, s[4:5]
	s_waitcnt vmcnt(8)
	s_waitcnt lgkmcnt(0)
	s_barrier
	s_setprio 1
	s_waitcnt lgkmcnt(0)
	v_mfma_f32_16x16x32_bf16 v[126:129], v[172:175], v[196:199], v[126:129]
	v_mfma_f32_16x16x32_bf16 v[122:125], v[168:171], v[196:199], v[122:125]
	v_mfma_f32_16x16x32_bf16 v[110:113], v[172:175], v[204:207], v[110:113]
	v_mfma_f32_16x16x32_bf16 v[106:109], v[168:171], v[204:207], v[106:109]
	v_mfma_f32_16x16x32_bf16 v[94:97], v[172:175], v[218:221], v[94:97]
	v_mfma_f32_16x16x32_bf16 v[90:93], v[168:171], v[218:221], v[90:93]
	v_mfma_f32_16x16x32_bf16 v[78:81], v[172:175], v[226:229], v[78:81]
	v_mfma_f32_16x16x32_bf16 v[74:77], v[168:171], v[226:229], v[74:77]
	v_mfma_f32_16x16x32_bf16 v[126:129], v[164:167], v[200:203], v[126:129]
	v_mfma_f32_16x16x32_bf16 v[122:125], v[180:183], v[200:203], v[122:125]
	v_mfma_f32_16x16x32_bf16 v[110:113], v[164:167], v[214:217], v[110:113]
	v_mfma_f32_16x16x32_bf16 v[106:109], v[180:183], v[214:217], v[106:109]
	v_mfma_f32_16x16x32_bf16 v[94:97], v[164:167], v[222:225], v[94:97]
	v_mfma_f32_16x16x32_bf16 v[90:93], v[180:183], v[222:225], v[90:93]
	v_mfma_f32_16x16x32_bf16 v[78:81], v[164:167], v[230:233], v[78:81]
	v_mfma_f32_16x16x32_bf16 v[74:77], v[180:183], v[230:233], v[74:77]
	s_setprio 0
	s_setprio 1
	v_mfma_f32_16x16x32_bf16 v[118:121], v[176:179], v[196:199], v[118:121]
	v_mfma_f32_16x16x32_bf16 v[114:117], v[188:191], v[196:199], v[114:117]
	v_mfma_f32_16x16x32_bf16 v[102:105], v[176:179], v[204:207], v[102:105]
	v_mfma_f32_16x16x32_bf16 v[98:101], v[188:191], v[204:207], v[98:101]
	v_mfma_f32_16x16x32_bf16 v[86:89], v[176:179], v[218:221], v[86:89]
	v_mfma_f32_16x16x32_bf16 v[82:85], v[188:191], v[218:221], v[82:85]
	v_mfma_f32_16x16x32_bf16 v[70:73], v[176:179], v[226:229], v[70:73]
	v_mfma_f32_16x16x32_bf16 v[66:69], v[188:191], v[226:229], v[66:69]
	v_mfma_f32_16x16x32_bf16 v[118:121], v[184:187], v[200:203], v[118:121]
	v_mfma_f32_16x16x32_bf16 v[114:117], v[192:195], v[200:203], v[114:117]
	v_mfma_f32_16x16x32_bf16 v[102:105], v[184:187], v[214:217], v[102:105]
	v_mfma_f32_16x16x32_bf16 v[98:101], v[192:195], v[214:217], v[98:101]
	v_mfma_f32_16x16x32_bf16 v[86:89], v[184:187], v[222:225], v[86:89]
	v_mfma_f32_16x16x32_bf16 v[82:85], v[192:195], v[222:225], v[82:85]
	v_mfma_f32_16x16x32_bf16 v[70:73], v[184:187], v[230:233], v[70:73]
	v_mfma_f32_16x16x32_bf16 v[66:69], v[192:195], v[230:233], v[66:69]
	s_setprio 0
	s_barrier
	s_addk_i32 s76, 0x80
	s_mov_b32 m0, s48
	v_add_u32_e32 v134, s76, v135
	ds_read_b128 v[196:199], v161 offset:49152
	ds_read_b128 v[200:203], v161 offset:50176
	ds_read_b128 v[204:207], v161 offset:51200
	ds_read_b128 v[214:217], v161 offset:52224
	ds_read_b128 v[218:221], v161 offset:53248
	ds_read_b128 v[222:225], v161 offset:54272
	ds_read_b128 v[226:229], v161 offset:55296
	ds_read_b128 v[230:233], v161 offset:56320
	global_load_lds_dwordx4 v134, s[6:7]
	v_add_u32_e32 v134, s23, v134
	s_mov_b32 m0, s49
	s_nop 0
	global_load_lds_dwordx4 v134, s[6:7]
	v_add_u32_e32 v134, s76, v138
	s_mov_b32 m0, s52
	s_nop 0
	global_load_lds_dwordx4 v134, s[6:7]
	v_add_u32_e32 v134, s23, v134
	s_mov_b32 m0, s53
	s_nop 0
	global_load_lds_dwordx4 v134, s[6:7]
	v_add_u32_e32 v134, s75, v140
	s_mov_b32 m0, s50
	s_nop 0
	global_load_lds_dwordx4 v134, s[4:5]
	v_add_u32_e32 v134, s22, v134
	s_mov_b32 m0, s51
	s_nop 0
	global_load_lds_dwordx4 v134, s[4:5]
	s_waitcnt vmcnt(8)
	s_waitcnt lgkmcnt(0)
	s_barrier
	s_setprio 1
	s_waitcnt lgkmcnt(0)
	v_mfma_f32_16x16x32_bf16 v[62:65], v[172:175], v[196:199], v[62:65]
	v_mfma_f32_16x16x32_bf16 v[58:61], v[168:171], v[196:199], v[58:61]
	v_mfma_f32_16x16x32_bf16 v[46:49], v[172:175], v[204:207], v[46:49]
	v_mfma_f32_16x16x32_bf16 v[42:45], v[168:171], v[204:207], v[42:45]
	v_mfma_f32_16x16x32_bf16 v[30:33], v[172:175], v[218:221], v[30:33]
	v_mfma_f32_16x16x32_bf16 v[26:29], v[168:171], v[218:221], v[26:29]
	v_mfma_f32_16x16x32_bf16 v[14:17], v[172:175], v[226:229], v[14:17]
	v_mfma_f32_16x16x32_bf16 v[10:13], v[168:171], v[226:229], v[10:13]
	v_mfma_f32_16x16x32_bf16 v[62:65], v[164:167], v[200:203], v[62:65]
	v_mfma_f32_16x16x32_bf16 v[58:61], v[180:183], v[200:203], v[58:61]
	v_mfma_f32_16x16x32_bf16 v[46:49], v[164:167], v[214:217], v[46:49]
	v_mfma_f32_16x16x32_bf16 v[42:45], v[180:183], v[214:217], v[42:45]
	v_mfma_f32_16x16x32_bf16 v[30:33], v[164:167], v[222:225], v[30:33]
	v_mfma_f32_16x16x32_bf16 v[26:29], v[180:183], v[222:225], v[26:29]
	v_mfma_f32_16x16x32_bf16 v[14:17], v[164:167], v[230:233], v[14:17]
	v_mfma_f32_16x16x32_bf16 v[10:13], v[180:183], v[230:233], v[10:13]
	s_setprio 0
	s_setprio 1
	v_mfma_f32_16x16x32_bf16 v[54:57], v[176:179], v[196:199], v[54:57]
	v_mfma_f32_16x16x32_bf16 v[50:53], v[188:191], v[196:199], v[50:53]
	v_mfma_f32_16x16x32_bf16 v[38:41], v[176:179], v[204:207], v[38:41]
	v_mfma_f32_16x16x32_bf16 v[34:37], v[188:191], v[204:207], v[34:37]
	v_mfma_f32_16x16x32_bf16 v[22:25], v[176:179], v[218:221], v[22:25]
	v_mfma_f32_16x16x32_bf16 v[18:21], v[188:191], v[218:221], v[18:21]
	v_mfma_f32_16x16x32_bf16 v[6:9], v[176:179], v[226:229], v[6:9]
	v_mfma_f32_16x16x32_bf16 v[2:5], v[188:191], v[226:229], v[2:5]
	v_mfma_f32_16x16x32_bf16 v[54:57], v[184:187], v[200:203], v[54:57]
	v_mfma_f32_16x16x32_bf16 v[50:53], v[192:195], v[200:203], v[50:53]
	v_mfma_f32_16x16x32_bf16 v[38:41], v[184:187], v[214:217], v[38:41]
	v_mfma_f32_16x16x32_bf16 v[34:37], v[192:195], v[214:217], v[34:37]
	v_mfma_f32_16x16x32_bf16 v[22:25], v[184:187], v[222:225], v[22:25]
	v_mfma_f32_16x16x32_bf16 v[18:21], v[192:195], v[222:225], v[18:21]
	v_mfma_f32_16x16x32_bf16 v[6:9], v[184:187], v[230:233], v[6:9]
	v_mfma_f32_16x16x32_bf16 v[2:5], v[192:195], v[230:233], v[2:5]
	s_setprio 0
	s_barrier
	s_add_i32 s74, s74, 2
	s_addk_i32 s16, 0x100
	s_addk_i32 s73, 0x100
	s_cmp_ge_i32 s74, s54
	s_cbranch_scc0 .LBB0_603

.LBB0_618:
	s_andn2_b64 vcc, exec, s[10:11]
	s_cbranch_vccnz .Lzs_2
	s_add_i32 s16, s72, 0x80
	s_addk_i32 s71, 0x100
	s_mov_b32 s72, 0
	ds_read_b128 v[160:163], v144
	ds_read_b128 v[164:167], v145
	ds_read_b128 v[168:171], v140
	ds_read_b128 v[172:175], v141
	ds_read_b128 v[176:179], v146
	ds_read_b128 v[180:183], v147
	ds_read_b128 v[184:187], v148
	ds_read_b128 v[188:191], v149
	s_add_i32 s73, s16, 0x80
	s_cmp_eq_u32 s20, s72
	s_cselect_b32 s74, s15, s71
	s_cselect_b32 s73, s17, s73
	v_add_u32_e32 v159, s16, v157
	s_add_i32 m0, s28, 0xc000
	ds_read_b128 v[192:195], v158
	ds_read_b128 v[196:199], v158 offset:1024
	ds_read_b128 v[200:203], v158 offset:2048
	ds_read_b128 v[204:207], v158 offset:3072
	ds_read_b128 v[214:217], v158 offset:4096
	ds_read_b128 v[218:221], v158 offset:5120
	ds_read_b128 v[222:225], v158 offset:6144
	ds_read_b128 v[226:229], v158 offset:7168
	global_load_lds_dwordx4 v159, s[4:5]
	v_add_u32_e32 v159, s16, v156
	s_add_i32 m0, s28, 0xe000
	s_nop 0
	global_load_lds_dwordx4 v159, s[4:5]
	s_waitcnt vmcnt(8)
	s_waitcnt lgkmcnt(0)
	s_barrier
	s_setprio 1
	s_waitcnt lgkmcnt(0)
	v_mfma_f32_16x16x32_bf16 v[122:125], v[168:171], v[192:195], 0
	v_mfma_f32_16x16x32_bf16 v[126:129], v[164:167], v[192:195], 0
	v_mfma_f32_16x16x32_bf16 v[110:113], v[168:171], v[200:203], 0
	v_mfma_f32_16x16x32_bf16 v[106:109], v[164:167], v[200:203], 0
	v_mfma_f32_16x16x32_bf16 v[94:97], v[168:171], v[214:217], 0
	v_mfma_f32_16x16x32_bf16 v[90:93], v[164:167], v[214:217], 0
	v_mfma_f32_16x16x32_bf16 v[78:81], v[168:171], v[222:225], 0
	v_mfma_f32_16x16x32_bf16 v[74:77], v[164:167], v[222:225], 0
	v_mfma_f32_16x16x32_bf16 v[122:125], v[160:163], v[196:199], v[122:125]
	v_mfma_f32_16x16x32_bf16 v[126:129], v[176:179], v[196:199], v[126:129]
	v_mfma_f32_16x16x32_bf16 v[110:113], v[160:163], v[204:207], v[110:113]
	v_mfma_f32_16x16x32_bf16 v[106:109], v[176:179], v[204:207], v[106:109]
	v_mfma_f32_16x16x32_bf16 v[94:97], v[160:163], v[218:221], v[94:97]
	v_mfma_f32_16x16x32_bf16 v[90:93], v[176:179], v[218:221], v[90:93]
	v_mfma_f32_16x16x32_bf16 v[78:81], v[160:163], v[226:229], v[78:81]
	v_mfma_f32_16x16x32_bf16 v[74:77], v[176:179], v[226:229], v[74:77]
	s_setprio 0
	s_setprio 1
	v_mfma_f32_16x16x32_bf16 v[118:121], v[172:175], v[192:195], 0
	v_mfma_f32_16x16x32_bf16 v[114:117], v[184:187], v[192:195], 0
	v_mfma_f32_16x16x32_bf16 v[102:105], v[172:175], v[200:203], 0
	v_mfma_f32_16x16x32_bf16 v[98:101], v[184:187], v[200:203], 0
	v_mfma_f32_16x16x32_bf16 v[86:89], v[172:175], v[214:217], 0
	v_mfma_f32_16x16x32_bf16 v[82:85], v[184:187], v[214:217], 0
	v_mfma_f32_16x16x32_bf16 v[70:73], v[172:175], v[222:225], 0
	v_mfma_f32_16x16x32_bf16 v[66:69], v[184:187], v[222:225], 0
	v_mfma_f32_16x16x32_bf16 v[118:121], v[180:183], v[196:199], v[118:121]
	v_mfma_f32_16x16x32_bf16 v[114:117], v[188:191], v[196:199], v[114:117]
	v_mfma_f32_16x16x32_bf16 v[102:105], v[180:183], v[204:207], v[102:105]
	v_mfma_f32_16x16x32_bf16 v[98:101], v[188:191], v[204:207], v[98:101]
	v_mfma_f32_16x16x32_bf16 v[86:89], v[180:183], v[218:221], v[86:89]
	v_mfma_f32_16x16x32_bf16 v[82:85], v[188:191], v[218:221], v[82:85]
	v_mfma_f32_16x16x32_bf16 v[70:73], v[180:183], v[226:229], v[70:73]
	v_mfma_f32_16x16x32_bf16 v[66:69], v[188:191], v[226:229], v[66:69]
	s_setprio 0
	s_barrier
	s_mov_b32 m0, s29
	v_add_u32_e32 v159, s74, v134
	ds_read_b128 v[192:195], v158 offset:16384
	ds_read_b128 v[196:199], v158 offset:17408
	ds_read_b128 v[200:203], v158 offset:18432
	ds_read_b128 v[204:207], v158 offset:19456
	ds_read_b128 v[214:217], v158 offset:20480
	ds_read_b128 v[218:221], v158 offset:21504
	ds_read_b128 v[222:225], v158 offset:22528
	ds_read_b128 v[226:229], v158 offset:23552
	global_load_lds_dwordx4 v159, s[6:7]
	v_add_u32_e32 v159, s23, v159
	s_mov_b32 m0, s30
	s_nop 0
	global_load_lds_dwordx4 v159, s[6:7]
	v_add_u32_e32 v159, s74, v135
	s_mov_b32 m0, s31
	s_nop 0
	global_load_lds_dwordx4 v159, s[6:7]
	v_add_u32_e32 v159, s23, v159
	s_mov_b32 m0, s35
	s_nop 0
	global_load_lds_dwordx4 v159, s[6:7]
	v_add_u32_e32 v159, s73, v1
	s_mov_b32 m0, s28
	s_nop 0
	global_load_lds_dwordx4 v159, s[4:5]
	v_add_u32_e32 v159, s22, v159
	s_mov_b32 m0, s44
	s_nop 0
	global_load_lds_dwordx4 v159, s[4:5]
	s_waitcnt vmcnt(8)
	s_waitcnt lgkmcnt(0)
	s_barrier
	s_setprio 1
	s_waitcnt lgkmcnt(0)
	v_mfma_f32_16x16x32_bf16 v[62:65], v[168:171], v[192:195], 0
	v_mfma_f32_16x16x32_bf16 v[58:61], v[164:167], v[192:195], 0
	v_mfma_f32_16x16x32_bf16 v[46:49], v[168:171], v[200:203], 0
	v_mfma_f32_16x16x32_bf16 v[42:45], v[164:167], v[200:203], 0
	v_mfma_f32_16x16x32_bf16 v[30:33], v[168:171], v[214:217], 0
	v_mfma_f32_16x16x32_bf16 v[26:29], v[164:167], v[214:217], 0
	v_mfma_f32_16x16x32_bf16 v[14:17], v[168:171], v[222:225], 0
	v_mfma_f32_16x16x32_bf16 v[10:13], v[164:167], v[222:225], 0
	v_mfma_f32_16x16x32_bf16 v[62:65], v[160:163], v[196:199], v[62:65]
	v_mfma_f32_16x16x32_bf16 v[58:61], v[176:179], v[196:199], v[58:61]
	v_mfma_f32_16x16x32_bf16 v[46:49], v[160:163], v[204:207], v[46:49]
	v_mfma_f32_16x16x32_bf16 v[42:45], v[176:179], v[204:207], v[42:45]
	v_mfma_f32_16x16x32_bf16 v[30:33], v[160:163], v[218:221], v[30:33]
	v_mfma_f32_16x16x32_bf16 v[26:29], v[176:179], v[218:221], v[26:29]
	v_mfma_f32_16x16x32_bf16 v[14:17], v[160:163], v[226:229], v[14:17]
	v_mfma_f32_16x16x32_bf16 v[10:13], v[176:179], v[226:229], v[10:13]
	s_setprio 0
	s_setprio 1
	v_mfma_f32_16x16x32_bf16 v[54:57], v[172:175], v[192:195], 0
	v_mfma_f32_16x16x32_bf16 v[50:53], v[184:187], v[192:195], 0
	v_mfma_f32_16x16x32_bf16 v[38:41], v[172:175], v[200:203], 0
	v_mfma_f32_16x16x32_bf16 v[34:37], v[184:187], v[200:203], 0
	v_mfma_f32_16x16x32_bf16 v[22:25], v[172:175], v[214:217], 0
	v_mfma_f32_16x16x32_bf16 v[18:21], v[184:187], v[214:217], 0
	v_mfma_f32_16x16x32_bf16 v[6:9], v[172:175], v[222:225], 0
	v_mfma_f32_16x16x32_bf16 v[2:5], v[184:187], v[222:225], 0
	v_mfma_f32_16x16x32_bf16 v[54:57], v[180:183], v[196:199], v[54:57]
	v_mfma_f32_16x16x32_bf16 v[50:53], v[188:191], v[196:199], v[50:53]
	v_mfma_f32_16x16x32_bf16 v[38:41], v[180:183], v[204:207], v[38:41]
	v_mfma_f32_16x16x32_bf16 v[34:37], v[188:191], v[204:207], v[34:37]
	v_mfma_f32_16x16x32_bf16 v[22:25], v[180:183], v[218:221], v[22:25]
	v_mfma_f32_16x16x32_bf16 v[18:21], v[188:191], v[218:221], v[18:21]
	v_mfma_f32_16x16x32_bf16 v[6:9], v[180:183], v[226:229], v[6:9]
	v_mfma_f32_16x16x32_bf16 v[2:5], v[188:191], v[226:229], v[2:5]
	s_setprio 0
	s_barrier
	s_branch .Lmid_2

.Lmid_2:
	ds_read_b128 v[160:163], v150
	ds_read_b128 v[164:167], v151
	ds_read_b128 v[168:171], v142
	ds_read_b128 v[172:175], v143
	ds_read_b128 v[176:179], v152
	ds_read_b128 v[180:183], v153
	ds_read_b128 v[184:187], v154
	ds_read_b128 v[188:191], v155
	s_mov_b32 m0, s45
	v_add_u32_e32 v159, s73, v136
	ds_read_b128 v[192:195], v158 offset:32768
	ds_read_b128 v[196:199], v158 offset:33792
	ds_read_b128 v[200:203], v158 offset:34816
	ds_read_b128 v[204:207], v158 offset:35840
	ds_read_b128 v[214:217], v158 offset:36864
	ds_read_b128 v[218:221], v158 offset:37888
	ds_read_b128 v[222:225], v158 offset:38912
	ds_read_b128 v[226:229], v158 offset:39936
	global_load_lds_dwordx4 v159, s[4:5]
	v_add_u32_e32 v159, s22, v159
	s_mov_b32 m0, s46
	s_nop 0
	global_load_lds_dwordx4 v159, s[4:5]
	s_waitcnt vmcnt(8)
	s_waitcnt lgkmcnt(0)
	s_barrier
	s_setprio 1
	s_waitcnt lgkmcnt(0)
	v_mfma_f32_16x16x32_bf16 v[122:125], v[168:171], v[192:195], v[122:125]
	v_mfma_f32_16x16x32_bf16 v[126:129], v[164:167], v[192:195], v[126:129]
	v_mfma_f32_16x16x32_bf16 v[110:113], v[168:171], v[200:203], v[110:113]
	v_mfma_f32_16x16x32_bf16 v[106:109], v[164:167], v[200:203], v[106:109]
	v_mfma_f32_16x16x32_bf16 v[94:97], v[168:171], v[214:217], v[94:97]
	v_mfma_f32_16x16x32_bf16 v[90:93], v[164:167], v[214:217], v[90:93]
	v_mfma_f32_16x16x32_bf16 v[78:81], v[168:171], v[222:225], v[78:81]
	v_mfma_f32_16x16x32_bf16 v[74:77], v[164:167], v[222:225], v[74:77]
	v_mfma_f32_16x16x32_bf16 v[122:125], v[160:163], v[196:199], v[122:125]
	v_mfma_f32_16x16x32_bf16 v[126:129], v[176:179], v[196:199], v[126:129]
	v_mfma_f32_16x16x32_bf16 v[110:113], v[160:163], v[204:207], v[110:113]
	v_mfma_f32_16x16x32_bf16 v[106:109], v[176:179], v[204:207], v[106:109]
	v_mfma_f32_16x16x32_bf16 v[94:97], v[160:163], v[218:221], v[94:97]
	v_mfma_f32_16x16x32_bf16 v[90:93], v[176:179], v[218:221], v[90:93]
	v_mfma_f32_16x16x32_bf16 v[78:81], v[160:163], v[226:229], v[78:81]
	v_mfma_f32_16x16x32_bf16 v[74:77], v[176:179], v[226:229], v[74:77]
	s_setprio 0
	s_setprio 1
	v_mfma_f32_16x16x32_bf16 v[118:121], v[172:175], v[192:195], v[118:121]
	v_mfma_f32_16x16x32_bf16 v[114:117], v[184:187], v[192:195], v[114:117]
	v_mfma_f32_16x16x32_bf16 v[102:105], v[172:175], v[200:203], v[102:105]
	v_mfma_f32_16x16x32_bf16 v[98:101], v[184:187], v[200:203], v[98:101]
	v_mfma_f32_16x16x32_bf16 v[86:89], v[172:175], v[214:217], v[86:89]
	v_mfma_f32_16x16x32_bf16 v[82:85], v[184:187], v[214:217], v[82:85]
	v_mfma_f32_16x16x32_bf16 v[70:73], v[172:175], v[222:225], v[70:73]
	v_mfma_f32_16x16x32_bf16 v[66:69], v[184:187], v[222:225], v[66:69]
	v_mfma_f32_16x16x32_bf16 v[118:121], v[180:183], v[196:199], v[118:121]
	v_mfma_f32_16x16x32_bf16 v[114:117], v[188:191], v[196:199], v[114:117]
	v_mfma_f32_16x16x32_bf16 v[102:105], v[180:183], v[204:207], v[102:105]
	v_mfma_f32_16x16x32_bf16 v[98:101], v[188:191], v[204:207], v[98:101]
	v_mfma_f32_16x16x32_bf16 v[86:89], v[180:183], v[218:221], v[86:89]
	v_mfma_f32_16x16x32_bf16 v[82:85], v[188:191], v[218:221], v[82:85]
	v_mfma_f32_16x16x32_bf16 v[70:73], v[180:183], v[226:229], v[70:73]
	v_mfma_f32_16x16x32_bf16 v[66:69], v[188:191], v[226:229], v[66:69]
	s_setprio 0
	s_barrier
	s_addk_i32 s74, 0x80
	s_mov_b32 m0, s49
	v_add_u32_e32 v159, s74, v134
	ds_read_b128 v[192:195], v158 offset:49152
	ds_read_b128 v[196:199], v158 offset:50176
	ds_read_b128 v[200:203], v158 offset:51200
	ds_read_b128 v[204:207], v158 offset:52224
	ds_read_b128 v[214:217], v158 offset:53248
	ds_read_b128 v[218:221], v158 offset:54272
	ds_read_b128 v[222:225], v158 offset:55296
	ds_read_b128 v[226:229], v158 offset:56320
	global_load_lds_dwordx4 v159, s[6:7]
	v_add_u32_e32 v159, s23, v159
	s_mov_b32 m0, s50
	s_nop 0
	global_load_lds_dwordx4 v159, s[6:7]
	v_add_u32_e32 v159, s74, v135
	s_mov_b32 m0, s53
	s_nop 0
	global_load_lds_dwordx4 v159, s[6:7]
	v_add_u32_e32 v159, s23, v159
	s_mov_b32 m0, s54
	s_nop 0
	global_load_lds_dwordx4 v159, s[6:7]
	v_add_u32_e32 v159, s73, v137
	s_mov_b32 m0, s51
	s_nop 0
	global_load_lds_dwordx4 v159, s[4:5]
	v_add_u32_e32 v159, s22, v159
	s_mov_b32 m0, s52
	s_nop 0
	global_load_lds_dwordx4 v159, s[4:5]
	s_waitcnt vmcnt(8)
	s_waitcnt lgkmcnt(0)
	s_barrier
	s_setprio 1
	s_waitcnt lgkmcnt(0)
	v_mfma_f32_16x16x32_bf16 v[62:65], v[168:171], v[192:195], v[62:65]
	v_mfma_f32_16x16x32_bf16 v[58:61], v[164:167], v[192:195], v[58:61]
	v_mfma_f32_16x16x32_bf16 v[46:49], v[168:171], v[200:203], v[46:49]
	v_mfma_f32_16x16x32_bf16 v[42:45], v[164:167], v[200:203], v[42:45]
	v_mfma_f32_16x16x32_bf16 v[30:33], v[168:171], v[214:217], v[30:33]
	v_mfma_f32_16x16x32_bf16 v[26:29], v[164:167], v[214:217], v[26:29]
	v_mfma_f32_16x16x32_bf16 v[14:17], v[168:171], v[222:225], v[14:17]
	v_mfma_f32_16x16x32_bf16 v[10:13], v[164:167], v[222:225], v[10:13]
	v_mfma_f32_16x16x32_bf16 v[62:65], v[160:163], v[196:199], v[62:65]
	v_mfma_f32_16x16x32_bf16 v[58:61], v[176:179], v[196:199], v[58:61]
	v_mfma_f32_16x16x32_bf16 v[46:49], v[160:163], v[204:207], v[46:49]
	v_mfma_f32_16x16x32_bf16 v[42:45], v[176:179], v[204:207], v[42:45]
	v_mfma_f32_16x16x32_bf16 v[30:33], v[160:163], v[218:221], v[30:33]
	v_mfma_f32_16x16x32_bf16 v[26:29], v[176:179], v[218:221], v[26:29]
	v_mfma_f32_16x16x32_bf16 v[14:17], v[160:163], v[226:229], v[14:17]
	v_mfma_f32_16x16x32_bf16 v[10:13], v[176:179], v[226:229], v[10:13]
	s_setprio 0
	s_setprio 1
	v_mfma_f32_16x16x32_bf16 v[54:57], v[172:175], v[192:195], v[54:57]
	v_mfma_f32_16x16x32_bf16 v[50:53], v[184:187], v[192:195], v[50:53]
	v_mfma_f32_16x16x32_bf16 v[38:41], v[172:175], v[200:203], v[38:41]
	v_mfma_f32_16x16x32_bf16 v[34:37], v[184:187], v[200:203], v[34:37]
	v_mfma_f32_16x16x32_bf16 v[22:25], v[172:175], v[214:217], v[22:25]
	v_mfma_f32_16x16x32_bf16 v[18:21], v[184:187], v[214:217], v[18:21]
	v_mfma_f32_16x16x32_bf16 v[6:9], v[172:175], v[222:225], v[6:9]
	v_mfma_f32_16x16x32_bf16 v[2:5], v[184:187], v[222:225], v[2:5]
	v_mfma_f32_16x16x32_bf16 v[54:57], v[180:183], v[196:199], v[54:57]
	v_mfma_f32_16x16x32_bf16 v[50:53], v[188:191], v[196:199], v[50:53]
	v_mfma_f32_16x16x32_bf16 v[38:41], v[180:183], v[204:207], v[38:41]
	v_mfma_f32_16x16x32_bf16 v[34:37], v[188:191], v[204:207], v[34:37]
	v_mfma_f32_16x16x32_bf16 v[22:25], v[180:183], v[218:221], v[22:25]
	v_mfma_f32_16x16x32_bf16 v[18:21], v[188:191], v[218:221], v[18:21]
	v_mfma_f32_16x16x32_bf16 v[6:9], v[180:183], v[226:229], v[6:9]
	v_mfma_f32_16x16x32_bf16 v[2:5], v[188:191], v[226:229], v[2:5]
	s_setprio 0
	s_barrier
	s_add_i32 s72, s72, 2
	s_addk_i32 s16, 0x100
	s_addk_i32 s71, 0x100
	s_cmp_ge_i32 s72, s55
	s_cbranch_scc0 .LBB0_620

.LBB0_635:
	s_andn2_b64 vcc, exec, s[20:21]
	s_cbranch_vccnz .Lzs_3
	s_add_i32 s28, s79, 0x80
	s_add_i32 s79, s75, 0x100
	s_mov_b32 s80, 0
	ds_read_b128 v[130:133], v188
	ds_read_b128 v[134:137], v189
	ds_read_b128 v[138:141], v184
	ds_read_b128 v[142:145], v185
	ds_read_b128 v[146:149], v190
	ds_read_b128 v[150:153], v191
	ds_read_b128 v[154:157], v192
	ds_read_b128 v[158:161], v193
	s_add_i32 s75, s28, 0x80
	s_cmp_eq_u32 s66, s80
	s_cselect_b32 s81, s25, s79
	s_cselect_b32 s75, s29, s75
	v_add_u32_e32 v203, s28, v201
	s_add_i32 m0, s46, 0xc000
	ds_read_b128 v[162:165], v202
	ds_read_b128 v[166:169], v202 offset:1024
	ds_read_b128 v[170:173], v202 offset:2048
	ds_read_b128 v[204:207], v202 offset:3072
	ds_read_b128 v[214:217], v202 offset:4096
	ds_read_b128 v[218:221], v202 offset:5120
	ds_read_b128 v[222:225], v202 offset:6144
	ds_read_b128 v[226:229], v202 offset:7168
	global_load_lds_dwordx4 v203, s[4:5]
	v_add_u32_e32 v203, s28, v200
	s_add_i32 m0, s46, 0xe000
	s_nop 0
	global_load_lds_dwordx4 v203, s[4:5]
	s_waitcnt vmcnt(8)
	s_waitcnt lgkmcnt(0)
	s_barrier
	s_setprio 1
	s_waitcnt lgkmcnt(0)
	v_mfma_f32_16x16x32_bf16 v[126:129], v[138:141], v[162:165], 0
	v_mfma_f32_16x16x32_bf16 v[118:121], v[134:137], v[162:165], 0
	v_mfma_f32_16x16x32_bf16 v[110:113], v[138:141], v[170:173], 0
	v_mfma_f32_16x16x32_bf16 v[102:105], v[134:137], v[170:173], 0
	v_mfma_f32_16x16x32_bf16 v[94:97], v[138:141], v[214:217], 0
	v_mfma_f32_16x16x32_bf16 v[86:89], v[134:137], v[214:217], 0
	v_mfma_f32_16x16x32_bf16 v[78:81], v[138:141], v[222:225], 0
	v_mfma_f32_16x16x32_bf16 v[70:73], v[134:137], v[222:225], 0
	v_mfma_f32_16x16x32_bf16 v[126:129], v[130:133], v[166:169], v[126:129]
	v_mfma_f32_16x16x32_bf16 v[118:121], v[146:149], v[166:169], v[118:121]
	v_mfma_f32_16x16x32_bf16 v[110:113], v[130:133], v[204:207], v[110:113]
	v_mfma_f32_16x16x32_bf16 v[102:105], v[146:149], v[204:207], v[102:105]
	v_mfma_f32_16x16x32_bf16 v[94:97], v[130:133], v[218:221], v[94:97]
	v_mfma_f32_16x16x32_bf16 v[86:89], v[146:149], v[218:221], v[86:89]
	v_mfma_f32_16x16x32_bf16 v[78:81], v[130:133], v[226:229], v[78:81]
	v_mfma_f32_16x16x32_bf16 v[70:73], v[146:149], v[226:229], v[70:73]
	s_setprio 0
	s_setprio 1
	v_mfma_f32_16x16x32_bf16 v[122:125], v[142:145], v[162:165], 0
	v_mfma_f32_16x16x32_bf16 v[114:117], v[154:157], v[162:165], 0
	v_mfma_f32_16x16x32_bf16 v[106:109], v[142:145], v[170:173], 0
	v_mfma_f32_16x16x32_bf16 v[98:101], v[154:157], v[170:173], 0
	v_mfma_f32_16x16x32_bf16 v[90:93], v[142:145], v[214:217], 0
	v_mfma_f32_16x16x32_bf16 v[82:85], v[154:157], v[214:217], 0
	v_mfma_f32_16x16x32_bf16 v[74:77], v[142:145], v[222:225], 0
	v_mfma_f32_16x16x32_bf16 v[66:69], v[154:157], v[222:225], 0
	v_mfma_f32_16x16x32_bf16 v[122:125], v[150:153], v[166:169], v[122:125]
	v_mfma_f32_16x16x32_bf16 v[114:117], v[158:161], v[166:169], v[114:117]
	v_mfma_f32_16x16x32_bf16 v[106:109], v[150:153], v[204:207], v[106:109]
	v_mfma_f32_16x16x32_bf16 v[98:101], v[158:161], v[204:207], v[98:101]
	v_mfma_f32_16x16x32_bf16 v[90:93], v[150:153], v[218:221], v[90:93]
	v_mfma_f32_16x16x32_bf16 v[82:85], v[158:161], v[218:221], v[82:85]
	v_mfma_f32_16x16x32_bf16 v[74:77], v[150:153], v[226:229], v[74:77]
	v_mfma_f32_16x16x32_bf16 v[66:69], v[158:161], v[226:229], v[66:69]
	s_setprio 0
	s_barrier
	s_mov_b32 m0, s47
	v_add_u32_e32 v203, s81, v178
	ds_read_b128 v[162:165], v202 offset:16384
	ds_read_b128 v[166:169], v202 offset:17408
	ds_read_b128 v[170:173], v202 offset:18432
	ds_read_b128 v[204:207], v202 offset:19456
	ds_read_b128 v[214:217], v202 offset:20480
	ds_read_b128 v[218:221], v202 offset:21504
	ds_read_b128 v[222:225], v202 offset:22528
	ds_read_b128 v[226:229], v202 offset:23552
	global_load_lds_dwordx4 v203, s[6:7]
	v_add_u32_e32 v203, s35, v203
	s_mov_b32 m0, s48
	s_nop 0
	global_load_lds_dwordx4 v203, s[6:7]
	v_add_u32_e32 v203, s81, v179
	s_mov_b32 m0, s49
	s_nop 0
	global_load_lds_dwordx4 v203, s[6:7]
	v_add_u32_e32 v203, s35, v203
	s_mov_b32 m0, s50
	s_nop 0
	global_load_lds_dwordx4 v203, s[6:7]
	v_add_u32_e32 v203, s75, v1
	s_mov_b32 m0, s46
	s_nop 0
	global_load_lds_dwordx4 v203, s[4:5]
	v_add_u32_e32 v203, s31, v203
	s_mov_b32 m0, s51
	s_nop 0
	global_load_lds_dwordx4 v203, s[4:5]
	s_waitcnt vmcnt(8)
	s_waitcnt lgkmcnt(0)
	s_barrier
	s_setprio 1
	s_waitcnt lgkmcnt(0)
	v_mfma_f32_16x16x32_bf16 v[62:65], v[138:141], v[162:165], 0
	v_mfma_f32_16x16x32_bf16 v[54:57], v[134:137], v[162:165], 0
	v_mfma_f32_16x16x32_bf16 v[46:49], v[138:141], v[170:173], 0
	v_mfma_f32_16x16x32_bf16 v[38:41], v[134:137], v[170:173], 0
	v_mfma_f32_16x16x32_bf16 v[30:33], v[138:141], v[214:217], 0
	v_mfma_f32_16x16x32_bf16 v[22:25], v[134:137], v[214:217], 0
	v_mfma_f32_16x16x32_bf16 v[14:17], v[138:141], v[222:225], 0
	v_mfma_f32_16x16x32_bf16 v[6:9], v[134:137], v[222:225], 0
	v_mfma_f32_16x16x32_bf16 v[62:65], v[130:133], v[166:169], v[62:65]
	v_mfma_f32_16x16x32_bf16 v[54:57], v[146:149], v[166:169], v[54:57]
	v_mfma_f32_16x16x32_bf16 v[46:49], v[130:133], v[204:207], v[46:49]
	v_mfma_f32_16x16x32_bf16 v[38:41], v[146:149], v[204:207], v[38:41]
	v_mfma_f32_16x16x32_bf16 v[30:33], v[130:133], v[218:221], v[30:33]
	v_mfma_f32_16x16x32_bf16 v[22:25], v[146:149], v[218:221], v[22:25]
	v_mfma_f32_16x16x32_bf16 v[14:17], v[130:133], v[226:229], v[14:17]
	v_mfma_f32_16x16x32_bf16 v[6:9], v[146:149], v[226:229], v[6:9]
	s_setprio 0
	s_setprio 1
	v_mfma_f32_16x16x32_bf16 v[58:61], v[142:145], v[162:165], 0
	v_mfma_f32_16x16x32_bf16 v[50:53], v[154:157], v[162:165], 0
	v_mfma_f32_16x16x32_bf16 v[42:45], v[142:145], v[170:173], 0
	v_mfma_f32_16x16x32_bf16 v[34:37], v[154:157], v[170:173], 0
	v_mfma_f32_16x16x32_bf16 v[26:29], v[142:145], v[214:217], 0
	v_mfma_f32_16x16x32_bf16 v[18:21], v[154:157], v[214:217], 0
	v_mfma_f32_16x16x32_bf16 v[10:13], v[142:145], v[222:225], 0
	v_mfma_f32_16x16x32_bf16 v[2:5], v[154:157], v[222:225], 0
	v_mfma_f32_16x16x32_bf16 v[58:61], v[150:153], v[166:169], v[58:61]
	v_mfma_f32_16x16x32_bf16 v[50:53], v[158:161], v[166:169], v[50:53]
	v_mfma_f32_16x16x32_bf16 v[42:45], v[150:153], v[204:207], v[42:45]
	v_mfma_f32_16x16x32_bf16 v[34:37], v[158:161], v[204:207], v[34:37]
	v_mfma_f32_16x16x32_bf16 v[26:29], v[150:153], v[218:221], v[26:29]
	v_mfma_f32_16x16x32_bf16 v[18:21], v[158:161], v[218:221], v[18:21]
	v_mfma_f32_16x16x32_bf16 v[10:13], v[150:153], v[226:229], v[10:13]
	v_mfma_f32_16x16x32_bf16 v[2:5], v[158:161], v[226:229], v[2:5]
	s_setprio 0
	s_barrier
	s_branch .Lmid_3

.Lmid_3:
	ds_read_b128 v[130:133], v194
	ds_read_b128 v[134:137], v195
	ds_read_b128 v[138:141], v186
	ds_read_b128 v[142:145], v187
	ds_read_b128 v[146:149], v196
	ds_read_b128 v[150:153], v197
	ds_read_b128 v[154:157], v198
	ds_read_b128 v[158:161], v199
	s_mov_b32 m0, s52
	v_add_u32_e32 v203, s75, v180
	ds_read_b128 v[162:165], v202 offset:32768
	ds_read_b128 v[166:169], v202 offset:33792
	ds_read_b128 v[170:173], v202 offset:34816
	ds_read_b128 v[204:207], v202 offset:35840
	ds_read_b128 v[214:217], v202 offset:36864
	ds_read_b128 v[218:221], v202 offset:37888
	ds_read_b128 v[222:225], v202 offset:38912
	ds_read_b128 v[226:229], v202 offset:39936
	global_load_lds_dwordx4 v203, s[4:5]
	v_add_u32_e32 v203, s31, v203
	s_mov_b32 m0, s53
	s_nop 0
	global_load_lds_dwordx4 v203, s[4:5]
	s_waitcnt vmcnt(8)
	s_waitcnt lgkmcnt(0)
	s_barrier
	s_setprio 1
	s_waitcnt lgkmcnt(0)
	v_mfma_f32_16x16x32_bf16 v[126:129], v[138:141], v[162:165], v[126:129]
	v_mfma_f32_16x16x32_bf16 v[118:121], v[134:137], v[162:165], v[118:121]
	v_mfma_f32_16x16x32_bf16 v[110:113], v[138:141], v[170:173], v[110:113]
	v_mfma_f32_16x16x32_bf16 v[102:105], v[134:137], v[170:173], v[102:105]
	v_mfma_f32_16x16x32_bf16 v[94:97], v[138:141], v[214:217], v[94:97]
	v_mfma_f32_16x16x32_bf16 v[86:89], v[134:137], v[214:217], v[86:89]
	v_mfma_f32_16x16x32_bf16 v[78:81], v[138:141], v[222:225], v[78:81]
	v_mfma_f32_16x16x32_bf16 v[70:73], v[134:137], v[222:225], v[70:73]
	v_mfma_f32_16x16x32_bf16 v[126:129], v[130:133], v[166:169], v[126:129]
	v_mfma_f32_16x16x32_bf16 v[118:121], v[146:149], v[166:169], v[118:121]
	v_mfma_f32_16x16x32_bf16 v[110:113], v[130:133], v[204:207], v[110:113]
	v_mfma_f32_16x16x32_bf16 v[102:105], v[146:149], v[204:207], v[102:105]
	v_mfma_f32_16x16x32_bf16 v[94:97], v[130:133], v[218:221], v[94:97]
	v_mfma_f32_16x16x32_bf16 v[86:89], v[146:149], v[218:221], v[86:89]
	v_mfma_f32_16x16x32_bf16 v[78:81], v[130:133], v[226:229], v[78:81]
	v_mfma_f32_16x16x32_bf16 v[70:73], v[146:149], v[226:229], v[70:73]
	s_setprio 0
	s_setprio 1
	v_mfma_f32_16x16x32_bf16 v[122:125], v[142:145], v[162:165], v[122:125]
	v_mfma_f32_16x16x32_bf16 v[114:117], v[154:157], v[162:165], v[114:117]
	v_mfma_f32_16x16x32_bf16 v[106:109], v[142:145], v[170:173], v[106:109]
	v_mfma_f32_16x16x32_bf16 v[98:101], v[154:157], v[170:173], v[98:101]
	v_mfma_f32_16x16x32_bf16 v[90:93], v[142:145], v[214:217], v[90:93]
	v_mfma_f32_16x16x32_bf16 v[82:85], v[154:157], v[214:217], v[82:85]
	v_mfma_f32_16x16x32_bf16 v[74:77], v[142:145], v[222:225], v[74:77]
	v_mfma_f32_16x16x32_bf16 v[66:69], v[154:157], v[222:225], v[66:69]
	v_mfma_f32_16x16x32_bf16 v[122:125], v[150:153], v[166:169], v[122:125]
	v_mfma_f32_16x16x32_bf16 v[114:117], v[158:161], v[166:169], v[114:117]
	v_mfma_f32_16x16x32_bf16 v[106:109], v[150:153], v[204:207], v[106:109]
	v_mfma_f32_16x16x32_bf16 v[98:101], v[158:161], v[204:207], v[98:101]
	v_mfma_f32_16x16x32_bf16 v[90:93], v[150:153], v[218:221], v[90:93]
	v_mfma_f32_16x16x32_bf16 v[82:85], v[158:161], v[218:221], v[82:85]
	v_mfma_f32_16x16x32_bf16 v[74:77], v[150:153], v[226:229], v[74:77]
	v_mfma_f32_16x16x32_bf16 v[66:69], v[158:161], v[226:229], v[66:69]
	s_setprio 0
	s_barrier
	s_addk_i32 s81, 0x80
	s_mov_b32 m0, s55
	v_add_u32_e32 v203, s81, v178
	ds_read_b128 v[162:165], v202 offset:49152
	ds_read_b128 v[166:169], v202 offset:50176
	ds_read_b128 v[170:173], v202 offset:51200
	ds_read_b128 v[204:207], v202 offset:52224
	ds_read_b128 v[214:217], v202 offset:53248
	ds_read_b128 v[218:221], v202 offset:54272
	ds_read_b128 v[222:225], v202 offset:55296
	ds_read_b128 v[226:229], v202 offset:56320
	global_load_lds_dwordx4 v203, s[6:7]
	v_add_u32_e32 v203, s35, v203
	s_mov_b32 m0, s56
	s_nop 0
	global_load_lds_dwordx4 v203, s[6:7]
	v_add_u32_e32 v203, s81, v179
	s_mov_b32 m0, s59
	s_nop 0
	global_load_lds_dwordx4 v203, s[6:7]
	v_add_u32_e32 v203, s35, v203
	s_mov_b32 m0, s60
	s_nop 0
	global_load_lds_dwordx4 v203, s[6:7]
	v_add_u32_e32 v203, s75, v181
	s_mov_b32 m0, s57
	s_nop 0
	global_load_lds_dwordx4 v203, s[4:5]
	v_add_u32_e32 v203, s31, v203
	s_mov_b32 m0, s58
	s_nop 0
	global_load_lds_dwordx4 v203, s[4:5]
	s_waitcnt vmcnt(8)
	s_waitcnt lgkmcnt(0)
	s_barrier
	s_setprio 1
	s_waitcnt lgkmcnt(0)
	v_mfma_f32_16x16x32_bf16 v[62:65], v[138:141], v[162:165], v[62:65]
	v_mfma_f32_16x16x32_bf16 v[54:57], v[134:137], v[162:165], v[54:57]
	v_mfma_f32_16x16x32_bf16 v[46:49], v[138:141], v[170:173], v[46:49]
	v_mfma_f32_16x16x32_bf16 v[38:41], v[134:137], v[170:173], v[38:41]
	v_mfma_f32_16x16x32_bf16 v[30:33], v[138:141], v[214:217], v[30:33]
	v_mfma_f32_16x16x32_bf16 v[22:25], v[134:137], v[214:217], v[22:25]
	v_mfma_f32_16x16x32_bf16 v[14:17], v[138:141], v[222:225], v[14:17]
	v_mfma_f32_16x16x32_bf16 v[6:9], v[134:137], v[222:225], v[6:9]
	v_mfma_f32_16x16x32_bf16 v[62:65], v[130:133], v[166:169], v[62:65]
	v_mfma_f32_16x16x32_bf16 v[54:57], v[146:149], v[166:169], v[54:57]
	v_mfma_f32_16x16x32_bf16 v[46:49], v[130:133], v[204:207], v[46:49]
	v_mfma_f32_16x16x32_bf16 v[38:41], v[146:149], v[204:207], v[38:41]
	v_mfma_f32_16x16x32_bf16 v[30:33], v[130:133], v[218:221], v[30:33]
	v_mfma_f32_16x16x32_bf16 v[22:25], v[146:149], v[218:221], v[22:25]
	v_mfma_f32_16x16x32_bf16 v[14:17], v[130:133], v[226:229], v[14:17]
	v_mfma_f32_16x16x32_bf16 v[6:9], v[146:149], v[226:229], v[6:9]
	s_setprio 0
	s_setprio 1
	v_mfma_f32_16x16x32_bf16 v[58:61], v[142:145], v[162:165], v[58:61]
	v_mfma_f32_16x16x32_bf16 v[50:53], v[154:157], v[162:165], v[50:53]
	v_mfma_f32_16x16x32_bf16 v[42:45], v[142:145], v[170:173], v[42:45]
	v_mfma_f32_16x16x32_bf16 v[34:37], v[154:157], v[170:173], v[34:37]
	v_mfma_f32_16x16x32_bf16 v[26:29], v[142:145], v[214:217], v[26:29]
	v_mfma_f32_16x16x32_bf16 v[18:21], v[154:157], v[214:217], v[18:21]
	v_mfma_f32_16x16x32_bf16 v[10:13], v[142:145], v[222:225], v[10:13]
	v_mfma_f32_16x16x32_bf16 v[2:5], v[154:157], v[222:225], v[2:5]
	v_mfma_f32_16x16x32_bf16 v[58:61], v[150:153], v[166:169], v[58:61]
	v_mfma_f32_16x16x32_bf16 v[50:53], v[158:161], v[166:169], v[50:53]
	v_mfma_f32_16x16x32_bf16 v[42:45], v[150:153], v[204:207], v[42:45]
	v_mfma_f32_16x16x32_bf16 v[34:37], v[158:161], v[204:207], v[34:37]
	v_mfma_f32_16x16x32_bf16 v[26:29], v[150:153], v[218:221], v[26:29]
	v_mfma_f32_16x16x32_bf16 v[18:21], v[158:161], v[218:221], v[18:21]
	v_mfma_f32_16x16x32_bf16 v[10:13], v[150:153], v[226:229], v[10:13]
	v_mfma_f32_16x16x32_bf16 v[2:5], v[158:161], v[226:229], v[2:5]
	s_setprio 0
	s_barrier
	s_add_i32 s80, s80, 2
	s_addk_i32 s28, 0x100
	s_addk_i32 s79, 0x100
	s_cmp_ge_i32 s80, s61
	s_cbranch_scc0 .LBB0_637

.LBB0_1181:
	s_andn2_b64 vcc, exec, s[16:17]
	s_waitcnt lgkmcnt(0)
	s_cbranch_vccnz .Lzs_4
	s_add_i32 s6, s58, 0x80
	s_add_i32 s58, s59, 0x100
	s_mov_b32 s59, 0
	ds_read_b128 v[114:117], v206
	ds_read_b128 v[118:121], v207
	ds_read_b128 v[122:125], v202
	ds_read_b128 v[126:129], v203
	ds_read_b128 v[146:149], v208
	ds_read_b128 v[150:153], v209
	ds_read_b128 v[154:157], v211
	ds_read_b128 v[158:161], v213
	s_add_i32 s60, s6, 0x80
	s_cmp_eq_u32 s90, s59
	s_cselect_b32 s61, s5, s58
	s_cselect_b32 s60, s7, s60
	v_add_u32_e32 v194, s6, v221
	s_add_i32 m0, s70, 0xc000
	ds_read_b128 v[162:165], v222
	ds_read_b128 v[170:173], v222 offset:1024
	ds_read_b128 v[174:177], v222 offset:2048
	ds_read_b128 v[178:181], v222 offset:3072
	ds_read_b128 v[182:185], v222 offset:4096
	ds_read_b128 v[186:189], v222 offset:5120
	ds_read_b128 v[190:193], v222 offset:6144
	ds_read_b128 v[226:229], v222 offset:7168
	global_load_lds_dwordx4 v194, s[8:9]
	v_add_u32_e32 v194, s6, v220
	s_add_i32 m0, s70, 0xe000
	s_nop 0
	global_load_lds_dwordx4 v194, s[8:9]
	s_waitcnt vmcnt(8)
	s_waitcnt lgkmcnt(0)
	s_barrier
	s_setprio 1
	s_waitcnt lgkmcnt(0)
	v_mfma_f32_16x16x32_bf16 v[142:145], v[122:125], v[162:165], 0
	v_mfma_f32_16x16x32_bf16 v[138:141], v[118:121], v[162:165], 0
	v_mfma_f32_16x16x32_bf16 v[110:113], v[122:125], v[174:177], 0
	v_mfma_f32_16x16x32_bf16 v[106:109], v[118:121], v[174:177], 0
	v_mfma_f32_16x16x32_bf16 v[94:97], v[122:125], v[182:185], 0
	v_mfma_f32_16x16x32_bf16 v[90:93], v[118:121], v[182:185], 0
	v_mfma_f32_16x16x32_bf16 v[78:81], v[122:125], v[190:193], 0
	v_mfma_f32_16x16x32_bf16 v[74:77], v[118:121], v[190:193], 0
	v_mfma_f32_16x16x32_bf16 v[142:145], v[114:117], v[170:173], v[142:145]
	v_mfma_f32_16x16x32_bf16 v[138:141], v[146:149], v[170:173], v[138:141]
	v_mfma_f32_16x16x32_bf16 v[110:113], v[114:117], v[178:181], v[110:113]
	v_mfma_f32_16x16x32_bf16 v[106:109], v[146:149], v[178:181], v[106:109]
	v_mfma_f32_16x16x32_bf16 v[94:97], v[114:117], v[186:189], v[94:97]
	v_mfma_f32_16x16x32_bf16 v[90:93], v[146:149], v[186:189], v[90:93]
	v_mfma_f32_16x16x32_bf16 v[78:81], v[114:117], v[226:229], v[78:81]
	v_mfma_f32_16x16x32_bf16 v[74:77], v[146:149], v[226:229], v[74:77]
	s_setprio 0
	s_setprio 1
	v_mfma_f32_16x16x32_bf16 v[134:137], v[126:129], v[162:165], 0
	v_mfma_f32_16x16x32_bf16 v[130:133], v[154:157], v[162:165], 0
	v_mfma_f32_16x16x32_bf16 v[102:105], v[126:129], v[174:177], 0
	v_mfma_f32_16x16x32_bf16 v[98:101], v[154:157], v[174:177], 0
	v_mfma_f32_16x16x32_bf16 v[86:89], v[126:129], v[182:185], 0
	v_mfma_f32_16x16x32_bf16 v[82:85], v[154:157], v[182:185], 0
	v_mfma_f32_16x16x32_bf16 v[70:73], v[126:129], v[190:193], 0
	v_mfma_f32_16x16x32_bf16 v[66:69], v[154:157], v[190:193], 0
	v_mfma_f32_16x16x32_bf16 v[134:137], v[150:153], v[170:173], v[134:137]
	v_mfma_f32_16x16x32_bf16 v[130:133], v[158:161], v[170:173], v[130:133]
	v_mfma_f32_16x16x32_bf16 v[102:105], v[150:153], v[178:181], v[102:105]
	v_mfma_f32_16x16x32_bf16 v[98:101], v[158:161], v[178:181], v[98:101]
	v_mfma_f32_16x16x32_bf16 v[86:89], v[150:153], v[186:189], v[86:89]
	v_mfma_f32_16x16x32_bf16 v[82:85], v[158:161], v[186:189], v[82:85]
	v_mfma_f32_16x16x32_bf16 v[70:73], v[150:153], v[226:229], v[70:73]
	v_mfma_f32_16x16x32_bf16 v[66:69], v[158:161], v[226:229], v[66:69]
	s_setprio 0
	s_barrier
	s_mov_b32 m0, s71
	v_add_u32_e32 v194, s61, v196
	ds_read_b128 v[162:165], v222 offset:16384
	ds_read_b128 v[170:173], v222 offset:17408
	ds_read_b128 v[174:177], v222 offset:18432
	ds_read_b128 v[178:181], v222 offset:19456
	ds_read_b128 v[182:185], v222 offset:20480
	ds_read_b128 v[186:189], v222 offset:21504
	ds_read_b128 v[190:193], v222 offset:22528
	ds_read_b128 v[226:229], v222 offset:23552
	global_load_lds_dwordx4 v194, s[20:21]
	v_add_u32_e32 v194, s35, v194
	s_mov_b32 m0, s72
	s_nop 0
	global_load_lds_dwordx4 v194, s[20:21]
	v_add_u32_e32 v194, s61, v197
	s_mov_b32 m0, s73
	s_nop 0
	global_load_lds_dwordx4 v194, s[20:21]
	v_add_u32_e32 v194, s35, v194
	s_mov_b32 m0, s76
	s_nop 0
	global_load_lds_dwordx4 v194, s[20:21]
	v_add_u32_e32 v194, s60, v1
	s_mov_b32 m0, s70
	s_nop 0
	global_load_lds_dwordx4 v194, s[8:9]
	v_add_u32_e32 v194, s29, v194
	s_mov_b32 m0, s77
	s_nop 0
	global_load_lds_dwordx4 v194, s[8:9]
	s_waitcnt vmcnt(8)
	s_waitcnt lgkmcnt(0)
	s_barrier
	s_setprio 1
	s_waitcnt lgkmcnt(0)
	v_mfma_f32_16x16x32_bf16 v[62:65], v[122:125], v[162:165], 0
	v_mfma_f32_16x16x32_bf16 v[58:61], v[118:121], v[162:165], 0
	v_mfma_f32_16x16x32_bf16 v[46:49], v[122:125], v[174:177], 0
	v_mfma_f32_16x16x32_bf16 v[42:45], v[118:121], v[174:177], 0
	v_mfma_f32_16x16x32_bf16 v[30:33], v[122:125], v[182:185], 0
	v_mfma_f32_16x16x32_bf16 v[26:29], v[118:121], v[182:185], 0
	v_mfma_f32_16x16x32_bf16 v[14:17], v[122:125], v[190:193], 0
	v_mfma_f32_16x16x32_bf16 v[10:13], v[118:121], v[190:193], 0
	v_mfma_f32_16x16x32_bf16 v[62:65], v[114:117], v[170:173], v[62:65]
	v_mfma_f32_16x16x32_bf16 v[58:61], v[146:149], v[170:173], v[58:61]
	v_mfma_f32_16x16x32_bf16 v[46:49], v[114:117], v[178:181], v[46:49]
	v_mfma_f32_16x16x32_bf16 v[42:45], v[146:149], v[178:181], v[42:45]
	v_mfma_f32_16x16x32_bf16 v[30:33], v[114:117], v[186:189], v[30:33]
	v_mfma_f32_16x16x32_bf16 v[26:29], v[146:149], v[186:189], v[26:29]
	v_mfma_f32_16x16x32_bf16 v[14:17], v[114:117], v[226:229], v[14:17]
	v_mfma_f32_16x16x32_bf16 v[10:13], v[146:149], v[226:229], v[10:13]
	s_setprio 0
	s_setprio 1
	v_mfma_f32_16x16x32_bf16 v[54:57], v[126:129], v[162:165], 0
	v_mfma_f32_16x16x32_bf16 v[50:53], v[154:157], v[162:165], 0
	v_mfma_f32_16x16x32_bf16 v[38:41], v[126:129], v[174:177], 0
	v_mfma_f32_16x16x32_bf16 v[34:37], v[154:157], v[174:177], 0
	v_mfma_f32_16x16x32_bf16 v[22:25], v[126:129], v[182:185], 0
	v_mfma_f32_16x16x32_bf16 v[18:21], v[154:157], v[182:185], 0
	v_mfma_f32_16x16x32_bf16 v[6:9], v[126:129], v[190:193], 0
	v_mfma_f32_16x16x32_bf16 v[2:5], v[154:157], v[190:193], 0
	v_mfma_f32_16x16x32_bf16 v[54:57], v[150:153], v[170:173], v[54:57]
	v_mfma_f32_16x16x32_bf16 v[50:53], v[158:161], v[170:173], v[50:53]
	v_mfma_f32_16x16x32_bf16 v[38:41], v[150:153], v[178:181], v[38:41]
	v_mfma_f32_16x16x32_bf16 v[34:37], v[158:161], v[178:181], v[34:37]
	v_mfma_f32_16x16x32_bf16 v[22:25], v[150:153], v[186:189], v[22:25]
	v_mfma_f32_16x16x32_bf16 v[18:21], v[158:161], v[186:189], v[18:21]
	v_mfma_f32_16x16x32_bf16 v[6:9], v[150:153], v[226:229], v[6:9]
	v_mfma_f32_16x16x32_bf16 v[2:5], v[158:161], v[226:229], v[2:5]
	s_setprio 0
	s_barrier
	s_branch .Lmid_4

.Lmid_4:
	ds_read_b128 v[114:117], v214
	ds_read_b128 v[118:121], v215
	ds_read_b128 v[122:125], v204
	ds_read_b128 v[126:129], v205
	ds_read_b128 v[146:149], v216
	ds_read_b128 v[150:153], v217
	ds_read_b128 v[154:157], v218
	ds_read_b128 v[158:161], v219
	s_mov_b32 m0, s78
	v_add_u32_e32 v194, s60, v198
	ds_read_b128 v[162:165], v222 offset:32768
	ds_read_b128 v[170:173], v222 offset:33792
	ds_read_b128 v[174:177], v222 offset:34816
	ds_read_b128 v[178:181], v222 offset:35840
	ds_read_b128 v[182:185], v222 offset:36864
	ds_read_b128 v[186:189], v222 offset:37888
	ds_read_b128 v[190:193], v222 offset:38912
	ds_read_b128 v[226:229], v222 offset:39936
	global_load_lds_dwordx4 v194, s[8:9]
	v_add_u32_e32 v194, s29, v194
	s_mov_b32 m0, s79
	s_nop 0
	global_load_lds_dwordx4 v194, s[8:9]
	s_waitcnt vmcnt(8)
	s_waitcnt lgkmcnt(0)
	s_barrier
	s_setprio 1
	s_waitcnt lgkmcnt(0)
	v_mfma_f32_16x16x32_bf16 v[142:145], v[122:125], v[162:165], v[142:145]
	v_mfma_f32_16x16x32_bf16 v[138:141], v[118:121], v[162:165], v[138:141]
	v_mfma_f32_16x16x32_bf16 v[110:113], v[122:125], v[174:177], v[110:113]
	v_mfma_f32_16x16x32_bf16 v[106:109], v[118:121], v[174:177], v[106:109]
	v_mfma_f32_16x16x32_bf16 v[94:97], v[122:125], v[182:185], v[94:97]
	v_mfma_f32_16x16x32_bf16 v[90:93], v[118:121], v[182:185], v[90:93]
	v_mfma_f32_16x16x32_bf16 v[78:81], v[122:125], v[190:193], v[78:81]
	v_mfma_f32_16x16x32_bf16 v[74:77], v[118:121], v[190:193], v[74:77]
	v_mfma_f32_16x16x32_bf16 v[142:145], v[114:117], v[170:173], v[142:145]
	v_mfma_f32_16x16x32_bf16 v[138:141], v[146:149], v[170:173], v[138:141]
	v_mfma_f32_16x16x32_bf16 v[110:113], v[114:117], v[178:181], v[110:113]
	v_mfma_f32_16x16x32_bf16 v[106:109], v[146:149], v[178:181], v[106:109]
	v_mfma_f32_16x16x32_bf16 v[94:97], v[114:117], v[186:189], v[94:97]
	v_mfma_f32_16x16x32_bf16 v[90:93], v[146:149], v[186:189], v[90:93]
	v_mfma_f32_16x16x32_bf16 v[78:81], v[114:117], v[226:229], v[78:81]
	v_mfma_f32_16x16x32_bf16 v[74:77], v[146:149], v[226:229], v[74:77]
	s_setprio 0
	s_setprio 1
	v_mfma_f32_16x16x32_bf16 v[134:137], v[126:129], v[162:165], v[134:137]
	v_mfma_f32_16x16x32_bf16 v[130:133], v[154:157], v[162:165], v[130:133]
	v_mfma_f32_16x16x32_bf16 v[102:105], v[126:129], v[174:177], v[102:105]
	v_mfma_f32_16x16x32_bf16 v[98:101], v[154:157], v[174:177], v[98:101]
	v_mfma_f32_16x16x32_bf16 v[86:89], v[126:129], v[182:185], v[86:89]
	v_mfma_f32_16x16x32_bf16 v[82:85], v[154:157], v[182:185], v[82:85]
	v_mfma_f32_16x16x32_bf16 v[70:73], v[126:129], v[190:193], v[70:73]
	v_mfma_f32_16x16x32_bf16 v[66:69], v[154:157], v[190:193], v[66:69]
	v_mfma_f32_16x16x32_bf16 v[134:137], v[150:153], v[170:173], v[134:137]
	v_mfma_f32_16x16x32_bf16 v[130:133], v[158:161], v[170:173], v[130:133]
	v_mfma_f32_16x16x32_bf16 v[102:105], v[150:153], v[178:181], v[102:105]
	v_mfma_f32_16x16x32_bf16 v[98:101], v[158:161], v[178:181], v[98:101]
	v_mfma_f32_16x16x32_bf16 v[86:89], v[150:153], v[186:189], v[86:89]
	v_mfma_f32_16x16x32_bf16 v[82:85], v[158:161], v[186:189], v[82:85]
	v_mfma_f32_16x16x32_bf16 v[70:73], v[150:153], v[226:229], v[70:73]
	v_mfma_f32_16x16x32_bf16 v[66:69], v[158:161], v[226:229], v[66:69]
	s_setprio 0
	s_barrier
	s_addk_i32 s61, 0x80
	s_mov_b32 m0, s81
	v_add_u32_e32 v194, s61, v196
	ds_read_b128 v[162:165], v222 offset:49152
	ds_read_b128 v[170:173], v222 offset:50176
	ds_read_b128 v[174:177], v222 offset:51200
	ds_read_b128 v[178:181], v222 offset:52224
	ds_read_b128 v[182:185], v222 offset:53248
	ds_read_b128 v[186:189], v222 offset:54272
	ds_read_b128 v[190:193], v222 offset:55296
	ds_read_b128 v[226:229], v222 offset:56320
	global_load_lds_dwordx4 v194, s[20:21]
	v_add_u32_e32 v194, s35, v194
	s_mov_b32 m0, s82
	s_nop 0
	global_load_lds_dwordx4 v194, s[20:21]
	v_add_u32_e32 v194, s61, v197
	s_mov_b32 m0, s85
	s_nop 0
	global_load_lds_dwordx4 v194, s[20:21]
	v_add_u32_e32 v194, s35, v194
	s_mov_b32 m0, s86
	s_nop 0
	global_load_lds_dwordx4 v194, s[20:21]
	v_add_u32_e32 v194, s60, v201
	s_mov_b32 m0, s83
	s_nop 0
	global_load_lds_dwordx4 v194, s[8:9]
	v_add_u32_e32 v194, s29, v194
	s_mov_b32 m0, s84
	s_nop 0
	global_load_lds_dwordx4 v194, s[8:9]
	s_waitcnt vmcnt(8)
	s_waitcnt lgkmcnt(0)
	s_barrier
	s_setprio 1
	s_waitcnt lgkmcnt(0)
	v_mfma_f32_16x16x32_bf16 v[62:65], v[122:125], v[162:165], v[62:65]
	v_mfma_f32_16x16x32_bf16 v[58:61], v[118:121], v[162:165], v[58:61]
	v_mfma_f32_16x16x32_bf16 v[46:49], v[122:125], v[174:177], v[46:49]
	v_mfma_f32_16x16x32_bf16 v[42:45], v[118:121], v[174:177], v[42:45]
	v_mfma_f32_16x16x32_bf16 v[30:33], v[122:125], v[182:185], v[30:33]
	v_mfma_f32_16x16x32_bf16 v[26:29], v[118:121], v[182:185], v[26:29]
	v_mfma_f32_16x16x32_bf16 v[14:17], v[122:125], v[190:193], v[14:17]
	v_mfma_f32_16x16x32_bf16 v[10:13], v[118:121], v[190:193], v[10:13]
	v_mfma_f32_16x16x32_bf16 v[62:65], v[114:117], v[170:173], v[62:65]
	v_mfma_f32_16x16x32_bf16 v[58:61], v[146:149], v[170:173], v[58:61]
	v_mfma_f32_16x16x32_bf16 v[46:49], v[114:117], v[178:181], v[46:49]
	v_mfma_f32_16x16x32_bf16 v[42:45], v[146:149], v[178:181], v[42:45]
	v_mfma_f32_16x16x32_bf16 v[30:33], v[114:117], v[186:189], v[30:33]
	v_mfma_f32_16x16x32_bf16 v[26:29], v[146:149], v[186:189], v[26:29]
	v_mfma_f32_16x16x32_bf16 v[14:17], v[114:117], v[226:229], v[14:17]
	v_mfma_f32_16x16x32_bf16 v[10:13], v[146:149], v[226:229], v[10:13]
	s_setprio 0
	s_setprio 1
	v_mfma_f32_16x16x32_bf16 v[54:57], v[126:129], v[162:165], v[54:57]
	v_mfma_f32_16x16x32_bf16 v[50:53], v[154:157], v[162:165], v[50:53]
	v_mfma_f32_16x16x32_bf16 v[38:41], v[126:129], v[174:177], v[38:41]
	v_mfma_f32_16x16x32_bf16 v[34:37], v[154:157], v[174:177], v[34:37]
	v_mfma_f32_16x16x32_bf16 v[22:25], v[126:129], v[182:185], v[22:25]
	v_mfma_f32_16x16x32_bf16 v[18:21], v[154:157], v[182:185], v[18:21]
	v_mfma_f32_16x16x32_bf16 v[6:9], v[126:129], v[190:193], v[6:9]
	v_mfma_f32_16x16x32_bf16 v[2:5], v[154:157], v[190:193], v[2:5]
	v_mfma_f32_16x16x32_bf16 v[54:57], v[150:153], v[170:173], v[54:57]
	v_mfma_f32_16x16x32_bf16 v[50:53], v[158:161], v[170:173], v[50:53]
	v_mfma_f32_16x16x32_bf16 v[38:41], v[150:153], v[178:181], v[38:41]
	v_mfma_f32_16x16x32_bf16 v[34:37], v[158:161], v[178:181], v[34:37]
	v_mfma_f32_16x16x32_bf16 v[22:25], v[150:153], v[186:189], v[22:25]
	v_mfma_f32_16x16x32_bf16 v[18:21], v[158:161], v[186:189], v[18:21]
	v_mfma_f32_16x16x32_bf16 v[6:9], v[150:153], v[226:229], v[6:9]
	v_mfma_f32_16x16x32_bf16 v[2:5], v[158:161], v[226:229], v[2:5]
	s_setprio 0
	s_barrier
	s_add_i32 s59, s59, 2
	s_addk_i32 s6, 0x100
	s_addk_i32 s58, 0x100
	s_cmp_ge_i32 s59, s87
	s_cbranch_scc0 .LBB0_1183

.LBB0_1601:
	s_andn2_b64 vcc, exec, s[12:13]
	s_cbranch_vccnz .Lzs_6
	s_add_i32 s6, s61, 0x80
	s_add_i32 s61, s62, 0x100
	s_mov_b32 s62, 0
	ds_read_b128 v[18:21], v235
	ds_read_b128 v[22:25], v236
	ds_read_b128 v[26:29], v243
	ds_read_b128 v[30:33], v244
	s_waitcnt lgkmcnt(0)
	ds_read_b128 v[2:5], v237
	ds_read_b128 v[6:9], v238
	ds_read_b128 v[10:13], v245
	ds_read_b128 v[14:17], v246
	s_add_i32 s63, s6, 0x80
	s_cmp_eq_u32 s89, s62
	s_cselect_b32 s65, s7, s63
	s_cselect_b32 s64, s5, s61
	s_add_i32 s63, s65, 0x80
	v_mov_b32_e32 v194, v1
	ds_read_b128 v[162:165], v251
	ds_read_b128 v[166:169], v251 offset:1024
	ds_read_b128 v[170:173], v251 offset:2048
	ds_read_b128 v[174:177], v251 offset:3072
	ds_read_b128 v[178:181], v251 offset:4096
	ds_read_b128 v[182:185], v251 offset:5120
	ds_read_b128 v[186:189], v251 offset:6144
	ds_read_b128 v[190:193], v251 offset:7168
	s_add_i32 s66, s6, s86
	v_add_u32_e32 v194, s66, v194
	s_add_i32 m0, s70, 0xc000
	s_add_i32 s66, s6, s93
	global_load_lds_dwordx4 v194, s[8:9]
	v_mov_b32_e32 v194, v1
	s_add_i32 m0, s70, 0xe000
	v_add_u32_e32 v194, s66, v194
	global_load_lds_dwordx4 v194, s[8:9]
	s_waitcnt vmcnt(8)
	s_waitcnt lgkmcnt(0)
	s_barrier
	s_setprio 1
	s_waitcnt lgkmcnt(0)
	v_mfma_f32_16x16x128_f8f6f4 v[158:161], v[18:25], v[162:169], 0
	v_mfma_f32_16x16x128_f8f6f4 v[154:157], v[26:33], v[162:169], 0
	v_mfma_f32_16x16x128_f8f6f4 v[142:145], v[18:25], v[170:177], 0
	v_mfma_f32_16x16x128_f8f6f4 v[138:141], v[26:33], v[170:177], 0
	v_mfma_f32_16x16x128_f8f6f4 v[126:129], v[18:25], v[178:185], 0
	v_mfma_f32_16x16x128_f8f6f4 v[122:125], v[26:33], v[178:185], 0
	v_mfma_f32_16x16x128_f8f6f4 v[110:113], v[18:25], v[186:193], 0
	v_mfma_f32_16x16x128_f8f6f4 v[106:109], v[26:33], v[186:193], 0
	s_setprio 0
	s_setprio 1
	v_mfma_f32_16x16x128_f8f6f4 v[150:153], v[2:9], v[162:169], 0
	v_mfma_f32_16x16x128_f8f6f4 v[146:149], v[10:17], v[162:169], 0
	v_mfma_f32_16x16x128_f8f6f4 v[134:137], v[2:9], v[170:177], 0
	v_mfma_f32_16x16x128_f8f6f4 v[130:133], v[10:17], v[170:177], 0
	v_mfma_f32_16x16x128_f8f6f4 v[118:121], v[2:9], v[178:185], 0
	v_mfma_f32_16x16x128_f8f6f4 v[114:117], v[10:17], v[178:185], 0
	v_mfma_f32_16x16x128_f8f6f4 v[102:105], v[2:9], v[186:193], 0
	v_mfma_f32_16x16x128_f8f6f4 v[98:101], v[10:17], v[186:193], 0
	s_setprio 0
	s_barrier
	v_mov_b32_e32 v194, v211
	ds_read_b128 v[162:165], v251 offset:16384
	ds_read_b128 v[166:169], v251 offset:17408
	ds_read_b128 v[170:173], v251 offset:18432
	ds_read_b128 v[174:177], v251 offset:19456
	ds_read_b128 v[178:181], v251 offset:20480
	ds_read_b128 v[182:185], v251 offset:21504
	ds_read_b128 v[186:189], v251 offset:22528
	ds_read_b128 v[190:193], v251 offset:23552
	s_mov_b32 m0, s71
	v_add_u32_e32 v194, s64, v194
	global_load_lds_dwordx4 v194, s[20:21]
	v_mov_b32_e32 v194, v211
	s_add_i32 s66, s64, s35
	v_add_u32_e32 v194, s66, v194
	s_mov_b32 m0, s72
	s_add_i32 s66, s66, s35
	global_load_lds_dwordx4 v194, s[20:21]
	v_mov_b32_e32 v194, v211
	s_mov_b32 m0, s73
	v_add_u32_e32 v194, s66, v194
	global_load_lds_dwordx4 v194, s[20:21]
	v_mov_b32_e32 v194, v211
	s_add_i32 s66, s66, s35
	v_add_u32_e32 v194, s66, v194
	s_mov_b32 m0, s76
	s_nop 0
	global_load_lds_dwordx4 v194, s[20:21]
	v_mov_b32_e32 v194, v1
	s_mov_b32 m0, s70
	v_add_u32_e32 v194, s65, v194
	global_load_lds_dwordx4 v194, s[8:9]
	v_mov_b32_e32 v194, v1
	s_add_i32 s65, s65, s23
	v_add_u32_e32 v194, s65, v194
	s_mov_b32 m0, s77
	s_nop 0
	global_load_lds_dwordx4 v194, s[8:9]
	s_waitcnt vmcnt(8)
	s_waitcnt lgkmcnt(0)
	s_barrier
	s_setprio 1
	s_waitcnt lgkmcnt(0)
	v_mfma_f32_16x16x128_f8f6f4 v[94:97], v[18:25], v[162:169], 0
	v_mfma_f32_16x16x128_f8f6f4 v[90:93], v[26:33], v[162:169], 0
	v_mfma_f32_16x16x128_f8f6f4 v[78:81], v[18:25], v[170:177], 0
	v_mfma_f32_16x16x128_f8f6f4 v[74:77], v[26:33], v[170:177], 0
	v_mfma_f32_16x16x128_f8f6f4 v[62:65], v[18:25], v[178:185], 0
	v_mfma_f32_16x16x128_f8f6f4 v[58:61], v[26:33], v[178:185], 0
	v_mfma_f32_16x16x128_f8f6f4 v[46:49], v[18:25], v[186:193], 0
	v_mfma_f32_16x16x128_f8f6f4 v[42:45], v[26:33], v[186:193], 0
	s_setprio 0
	s_setprio 1
	v_mfma_f32_16x16x128_f8f6f4 v[86:89], v[2:9], v[162:169], 0
	v_mfma_f32_16x16x128_f8f6f4 v[82:85], v[10:17], v[162:169], 0
	v_mfma_f32_16x16x128_f8f6f4 v[70:73], v[2:9], v[170:177], 0
	v_mfma_f32_16x16x128_f8f6f4 v[66:69], v[10:17], v[170:177], 0
	v_mfma_f32_16x16x128_f8f6f4 v[54:57], v[2:9], v[178:185], 0
	v_mfma_f32_16x16x128_f8f6f4 v[50:53], v[10:17], v[178:185], 0
	v_mfma_f32_16x16x128_f8f6f4 v[38:41], v[2:9], v[186:193], 0
	v_mfma_f32_16x16x128_f8f6f4 v[34:37], v[10:17], v[186:193], 0
	s_setprio 0
	s_barrier
	s_branch .Lmid_5

.Lmid_5:
	ds_read_b128 v[2:5], v239
	ds_read_b128 v[6:9], v240
	ds_read_b128 v[10:13], v247
	ds_read_b128 v[14:17], v248
	ds_read_b128 v[18:21], v241
	ds_read_b128 v[22:25], v242
	ds_read_b128 v[26:29], v249
	ds_read_b128 v[30:33], v250
	v_mov_b32_e32 v194, v1
	ds_read_b128 v[162:165], v251 offset:32768
	ds_read_b128 v[166:169], v251 offset:33792
	ds_read_b128 v[170:173], v251 offset:34816
	ds_read_b128 v[174:177], v251 offset:35840
	ds_read_b128 v[178:181], v251 offset:36864
	ds_read_b128 v[182:185], v251 offset:37888
	ds_read_b128 v[186:189], v251 offset:38912
	ds_read_b128 v[190:193], v251 offset:39936
	s_add_i32 s65, s65, s23
	s_mov_b32 m0, s78
	v_add_u32_e32 v194, s65, v194
	global_load_lds_dwordx4 v194, s[8:9]
	v_mov_b32_e32 v194, v1
	s_add_i32 s65, s65, s23
	v_add_u32_e32 v194, s65, v194
	s_mov_b32 m0, s44
	s_nop 0
	global_load_lds_dwordx4 v194, s[8:9]
	s_waitcnt vmcnt(8)
	s_waitcnt lgkmcnt(0)
	s_barrier
	s_setprio 1
	s_waitcnt lgkmcnt(0)
	v_mfma_f32_16x16x128_f8f6f4 v[158:161], v[2:9], v[162:169], v[158:161]
	v_mfma_f32_16x16x128_f8f6f4 v[154:157], v[10:17], v[162:169], v[154:157]
	v_mfma_f32_16x16x128_f8f6f4 v[142:145], v[2:9], v[170:177], v[142:145]
	v_mfma_f32_16x16x128_f8f6f4 v[138:141], v[10:17], v[170:177], v[138:141]
	v_mfma_f32_16x16x128_f8f6f4 v[126:129], v[2:9], v[178:185], v[126:129]
	v_mfma_f32_16x16x128_f8f6f4 v[122:125], v[10:17], v[178:185], v[122:125]
	v_mfma_f32_16x16x128_f8f6f4 v[110:113], v[2:9], v[186:193], v[110:113]
	v_mfma_f32_16x16x128_f8f6f4 v[106:109], v[10:17], v[186:193], v[106:109]
	s_setprio 0
	s_setprio 1
	v_mfma_f32_16x16x128_f8f6f4 v[150:153], v[18:25], v[162:169], v[150:153]
	v_mfma_f32_16x16x128_f8f6f4 v[146:149], v[26:33], v[162:169], v[146:149]
	v_mfma_f32_16x16x128_f8f6f4 v[134:137], v[18:25], v[170:177], v[134:137]
	v_mfma_f32_16x16x128_f8f6f4 v[130:133], v[26:33], v[170:177], v[130:133]
	v_mfma_f32_16x16x128_f8f6f4 v[118:121], v[18:25], v[178:185], v[118:121]
	v_mfma_f32_16x16x128_f8f6f4 v[114:117], v[26:33], v[178:185], v[114:117]
	v_mfma_f32_16x16x128_f8f6f4 v[102:105], v[18:25], v[186:193], v[102:105]
	v_mfma_f32_16x16x128_f8f6f4 v[98:101], v[26:33], v[186:193], v[98:101]
	s_setprio 0
	s_barrier
	v_mov_b32_e32 v194, v211
	ds_read_b128 v[162:165], v251 offset:49152
	ds_read_b128 v[166:169], v251 offset:50176
	ds_read_b128 v[170:173], v251 offset:51200
	ds_read_b128 v[174:177], v251 offset:52224
	ds_read_b128 v[178:181], v251 offset:53248
	ds_read_b128 v[182:185], v251 offset:54272
	ds_read_b128 v[186:189], v251 offset:55296
	ds_read_b128 v[190:193], v251 offset:56320
	s_addk_i32 s64, 0x80
	s_mov_b32 m0, s79
	v_add_u32_e32 v194, s64, v194
	global_load_lds_dwordx4 v194, s[20:21]
	v_mov_b32_e32 v194, v211
	s_add_i32 s64, s64, s35
	v_add_u32_e32 v194, s64, v194
	s_mov_b32 m0, s80
	s_add_i32 s64, s64, s35
	global_load_lds_dwordx4 v194, s[20:21]
	v_mov_b32_e32 v194, v211
	s_mov_b32 m0, s83
	v_add_u32_e32 v194, s64, v194
	global_load_lds_dwordx4 v194, s[20:21]
	v_mov_b32_e32 v194, v211
	s_add_i32 s64, s64, s35
	v_add_u32_e32 v194, s64, v194
	s_mov_b32 m0, s84
	s_nop 0
	global_load_lds_dwordx4 v194, s[20:21]
	v_mov_b32_e32 v194, v1
	s_mov_b32 m0, s81
	v_add_u32_e32 v194, s63, v194
	global_load_lds_dwordx4 v194, s[8:9]
	v_mov_b32_e32 v194, v1
	s_add_i32 s63, s63, s23
	v_add_u32_e32 v194, s63, v194
	s_mov_b32 m0, s82
	s_nop 0
	global_load_lds_dwordx4 v194, s[8:9]
	s_waitcnt vmcnt(8)
	s_waitcnt lgkmcnt(0)
	s_barrier
	s_setprio 1
	s_waitcnt lgkmcnt(0)
	v_mfma_f32_16x16x128_f8f6f4 v[94:97], v[2:9], v[162:169], v[94:97]
	v_mfma_f32_16x16x128_f8f6f4 v[90:93], v[10:17], v[162:169], v[90:93]
	v_mfma_f32_16x16x128_f8f6f4 v[78:81], v[2:9], v[170:177], v[78:81]
	v_mfma_f32_16x16x128_f8f6f4 v[74:77], v[10:17], v[170:177], v[74:77]
	v_mfma_f32_16x16x128_f8f6f4 v[62:65], v[2:9], v[178:185], v[62:65]
	v_mfma_f32_16x16x128_f8f6f4 v[58:61], v[10:17], v[178:185], v[58:61]
	v_mfma_f32_16x16x128_f8f6f4 v[46:49], v[2:9], v[186:193], v[46:49]
	v_mfma_f32_16x16x128_f8f6f4 v[42:45], v[10:17], v[186:193], v[42:45]
	s_setprio 0
	s_setprio 1
	v_mfma_f32_16x16x128_f8f6f4 v[86:89], v[18:25], v[162:169], v[86:89]
	v_mfma_f32_16x16x128_f8f6f4 v[82:85], v[26:33], v[162:169], v[82:85]
	v_mfma_f32_16x16x128_f8f6f4 v[70:73], v[18:25], v[170:177], v[70:73]
	v_mfma_f32_16x16x128_f8f6f4 v[66:69], v[26:33], v[170:177], v[66:69]
	v_mfma_f32_16x16x128_f8f6f4 v[54:57], v[18:25], v[178:185], v[54:57]
	v_mfma_f32_16x16x128_f8f6f4 v[50:53], v[26:33], v[178:185], v[50:53]
	v_mfma_f32_16x16x128_f8f6f4 v[38:41], v[18:25], v[186:193], v[38:41]
	v_mfma_f32_16x16x128_f8f6f4 v[34:37], v[26:33], v[186:193], v[34:37]
	s_setprio 0
	s_barrier
	s_add_i32 s62, s62, 2
	s_addk_i32 s6, 0x100
	s_addk_i32 s61, 0x100
	s_cmp_ge_i32 s62, s85
	s_cbranch_scc0 .LBB0_1603

.LBB0_2045:
	s_andn2_b64 vcc, exec, s[16:17]
	s_cbranch_vccnz .Lzs_8
	s_add_i32 s30, s48, 0x100
	s_mov_b32 s48, 0
	ds_read_b128 v[138:141], v156
	ds_read_b128 v[142:145], v157
	ds_read_b128 v[168:171], v152
	ds_read_b128 v[172:175], v153
	ds_read_b128 v[176:179], v158
	ds_read_b128 v[180:183], v159
	ds_read_b128 v[184:187], v160
	ds_read_b128 v[188:191], v161
	s_add_i32 s49, s48, 2
	s_add_i32 s50, s73, s46
	s_cmp_eq_u32 s71, s48
	s_cselect_b32 s48, s47, s50
	s_cselect_b32 s51, s31, s30
	v_add_u32_e32 v133, s46, v132
	s_add_i32 m0, s52, 0xc000
	ds_read_b128 v[192:195], v131
	ds_read_b128 v[196:199], v131 offset:1024
	ds_read_b128 v[200:203], v131 offset:2048
	ds_read_b128 v[204:207], v131 offset:3072
	ds_read_b128 v[214:217], v131 offset:4096
	ds_read_b128 v[218:221], v131 offset:5120
	ds_read_b128 v[222:225], v131 offset:6144
	ds_read_b128 v[226:229], v131 offset:7168
	global_load_lds_dwordx4 v133, s[6:7]
	v_add_u32_e32 v133, s46, v130
	s_add_i32 m0, s52, 0xe000
	s_nop 0
	global_load_lds_dwordx4 v133, s[6:7]
	s_waitcnt vmcnt(8)
	s_waitcnt lgkmcnt(0)
	s_barrier
	s_setprio 1
	s_waitcnt lgkmcnt(0)
	v_mfma_f32_16x16x32_bf16 v[122:125], v[168:171], v[192:195], 0
	v_mfma_f32_16x16x32_bf16 v[126:129], v[142:145], v[192:195], 0
	v_mfma_f32_16x16x32_bf16 v[110:113], v[168:171], v[200:203], 0
	v_mfma_f32_16x16x32_bf16 v[106:109], v[142:145], v[200:203], 0
	v_mfma_f32_16x16x32_bf16 v[94:97], v[168:171], v[214:217], 0
	v_mfma_f32_16x16x32_bf16 v[90:93], v[142:145], v[214:217], 0
	v_mfma_f32_16x16x32_bf16 v[78:81], v[168:171], v[222:225], 0
	v_mfma_f32_16x16x32_bf16 v[74:77], v[142:145], v[222:225], 0
	v_mfma_f32_16x16x32_bf16 v[122:125], v[138:141], v[196:199], v[122:125]
	v_mfma_f32_16x16x32_bf16 v[126:129], v[176:179], v[196:199], v[126:129]
	v_mfma_f32_16x16x32_bf16 v[110:113], v[138:141], v[204:207], v[110:113]
	v_mfma_f32_16x16x32_bf16 v[106:109], v[176:179], v[204:207], v[106:109]
	v_mfma_f32_16x16x32_bf16 v[94:97], v[138:141], v[218:221], v[94:97]
	v_mfma_f32_16x16x32_bf16 v[90:93], v[176:179], v[218:221], v[90:93]
	v_mfma_f32_16x16x32_bf16 v[78:81], v[138:141], v[226:229], v[78:81]
	v_mfma_f32_16x16x32_bf16 v[74:77], v[176:179], v[226:229], v[74:77]
	s_setprio 0
	s_setprio 1
	v_mfma_f32_16x16x32_bf16 v[118:121], v[172:175], v[192:195], 0
	v_mfma_f32_16x16x32_bf16 v[114:117], v[184:187], v[192:195], 0
	v_mfma_f32_16x16x32_bf16 v[102:105], v[172:175], v[200:203], 0
	v_mfma_f32_16x16x32_bf16 v[98:101], v[184:187], v[200:203], 0
	v_mfma_f32_16x16x32_bf16 v[86:89], v[172:175], v[214:217], 0
	v_mfma_f32_16x16x32_bf16 v[82:85], v[184:187], v[214:217], 0
	v_mfma_f32_16x16x32_bf16 v[70:73], v[172:175], v[222:225], 0
	v_mfma_f32_16x16x32_bf16 v[66:69], v[184:187], v[222:225], 0
	v_mfma_f32_16x16x32_bf16 v[118:121], v[180:183], v[196:199], v[118:121]
	v_mfma_f32_16x16x32_bf16 v[114:117], v[188:191], v[196:199], v[114:117]
	v_mfma_f32_16x16x32_bf16 v[102:105], v[180:183], v[204:207], v[102:105]
	v_mfma_f32_16x16x32_bf16 v[98:101], v[188:191], v[204:207], v[98:101]
	v_mfma_f32_16x16x32_bf16 v[86:89], v[180:183], v[218:221], v[86:89]
	v_mfma_f32_16x16x32_bf16 v[82:85], v[188:191], v[218:221], v[82:85]
	v_mfma_f32_16x16x32_bf16 v[70:73], v[180:183], v[226:229], v[70:73]
	v_mfma_f32_16x16x32_bf16 v[66:69], v[188:191], v[226:229], v[66:69]
	s_setprio 0
	s_barrier
	s_mov_b32 m0, s53
	v_add_u32_e32 v133, s51, v146
	ds_read_b128 v[192:195], v131 offset:16384
	ds_read_b128 v[196:199], v131 offset:17408
	ds_read_b128 v[200:203], v131 offset:18432
	ds_read_b128 v[204:207], v131 offset:19456
	ds_read_b128 v[214:217], v131 offset:20480
	ds_read_b128 v[218:221], v131 offset:21504
	ds_read_b128 v[222:225], v131 offset:22528
	ds_read_b128 v[226:229], v131 offset:23552
	global_load_lds_dwordx4 v133, s[8:9]
	v_add_u32_e32 v133, s45, v133
	s_mov_b32 m0, s54
	s_nop 0
	global_load_lds_dwordx4 v133, s[8:9]
	v_add_u32_e32 v133, s51, v147
	s_mov_b32 m0, s55
	s_nop 0
	global_load_lds_dwordx4 v133, s[8:9]
	v_add_u32_e32 v133, s45, v133
	s_mov_b32 m0, s56
	s_nop 0
	global_load_lds_dwordx4 v133, s[8:9]
	v_add_u32_e32 v133, s48, v1
	s_mov_b32 m0, s52
	s_nop 0
	global_load_lds_dwordx4 v133, s[6:7]
	v_add_u32_e32 v133, s44, v133
	s_mov_b32 m0, s57
	s_nop 0
	global_load_lds_dwordx4 v133, s[6:7]
	s_waitcnt vmcnt(8)
	s_waitcnt lgkmcnt(0)
	s_barrier
	s_setprio 1
	s_waitcnt lgkmcnt(0)
	v_mfma_f32_16x16x32_bf16 v[62:65], v[168:171], v[192:195], 0
	v_mfma_f32_16x16x32_bf16 v[58:61], v[142:145], v[192:195], 0
	v_mfma_f32_16x16x32_bf16 v[46:49], v[168:171], v[200:203], 0
	v_mfma_f32_16x16x32_bf16 v[42:45], v[142:145], v[200:203], 0
	v_mfma_f32_16x16x32_bf16 v[30:33], v[168:171], v[214:217], 0
	v_mfma_f32_16x16x32_bf16 v[26:29], v[142:145], v[214:217], 0
	v_mfma_f32_16x16x32_bf16 v[14:17], v[168:171], v[222:225], 0
	v_mfma_f32_16x16x32_bf16 v[10:13], v[142:145], v[222:225], 0
	v_mfma_f32_16x16x32_bf16 v[62:65], v[138:141], v[196:199], v[62:65]
	v_mfma_f32_16x16x32_bf16 v[58:61], v[176:179], v[196:199], v[58:61]
	v_mfma_f32_16x16x32_bf16 v[46:49], v[138:141], v[204:207], v[46:49]
	v_mfma_f32_16x16x32_bf16 v[42:45], v[176:179], v[204:207], v[42:45]
	v_mfma_f32_16x16x32_bf16 v[30:33], v[138:141], v[218:221], v[30:33]
	v_mfma_f32_16x16x32_bf16 v[26:29], v[176:179], v[218:221], v[26:29]
	v_mfma_f32_16x16x32_bf16 v[14:17], v[138:141], v[226:229], v[14:17]
	v_mfma_f32_16x16x32_bf16 v[10:13], v[176:179], v[226:229], v[10:13]
	s_setprio 0
	s_setprio 1
	v_mfma_f32_16x16x32_bf16 v[54:57], v[172:175], v[192:195], 0
	v_mfma_f32_16x16x32_bf16 v[50:53], v[184:187], v[192:195], 0
	v_mfma_f32_16x16x32_bf16 v[38:41], v[172:175], v[200:203], 0
	v_mfma_f32_16x16x32_bf16 v[34:37], v[184:187], v[200:203], 0
	v_mfma_f32_16x16x32_bf16 v[22:25], v[172:175], v[214:217], 0
	v_mfma_f32_16x16x32_bf16 v[18:21], v[184:187], v[214:217], 0
	v_mfma_f32_16x16x32_bf16 v[6:9], v[172:175], v[222:225], 0
	v_mfma_f32_16x16x32_bf16 v[2:5], v[184:187], v[222:225], 0
	v_mfma_f32_16x16x32_bf16 v[54:57], v[180:183], v[196:199], v[54:57]
	v_mfma_f32_16x16x32_bf16 v[50:53], v[188:191], v[196:199], v[50:53]
	v_mfma_f32_16x16x32_bf16 v[38:41], v[180:183], v[204:207], v[38:41]
	v_mfma_f32_16x16x32_bf16 v[34:37], v[188:191], v[204:207], v[34:37]
	v_mfma_f32_16x16x32_bf16 v[22:25], v[180:183], v[218:221], v[22:25]
	v_mfma_f32_16x16x32_bf16 v[18:21], v[188:191], v[218:221], v[18:21]
	v_mfma_f32_16x16x32_bf16 v[6:9], v[180:183], v[226:229], v[6:9]
	v_mfma_f32_16x16x32_bf16 v[2:5], v[188:191], v[226:229], v[2:5]
	s_setprio 0
	s_barrier
	s_branch .Lmid_6

.Lmid_6:
	ds_read_b128 v[138:141], v162
	ds_read_b128 v[142:145], v163
	ds_read_b128 v[168:171], v154
	ds_read_b128 v[172:175], v155
	ds_read_b128 v[176:179], v164
	ds_read_b128 v[180:183], v165
	ds_read_b128 v[184:187], v166
	ds_read_b128 v[188:191], v167
	s_mov_b32 m0, s58
	v_add_u32_e32 v133, s48, v148
	ds_read_b128 v[192:195], v131 offset:32768
	ds_read_b128 v[196:199], v131 offset:33792
	ds_read_b128 v[200:203], v131 offset:34816
	ds_read_b128 v[204:207], v131 offset:35840
	ds_read_b128 v[214:217], v131 offset:36864
	ds_read_b128 v[218:221], v131 offset:37888
	ds_read_b128 v[222:225], v131 offset:38912
	ds_read_b128 v[226:229], v131 offset:39936
	global_load_lds_dwordx4 v133, s[6:7]
	v_add_u32_e32 v133, s44, v133
	s_mov_b32 m0, s59
	s_nop 0
	global_load_lds_dwordx4 v133, s[6:7]
	s_waitcnt vmcnt(8)
	s_waitcnt lgkmcnt(0)
	s_barrier
	s_setprio 1
	s_waitcnt lgkmcnt(0)
	v_mfma_f32_16x16x32_bf16 v[122:125], v[168:171], v[192:195], v[122:125]
	v_mfma_f32_16x16x32_bf16 v[126:129], v[142:145], v[192:195], v[126:129]
	v_mfma_f32_16x16x32_bf16 v[110:113], v[168:171], v[200:203], v[110:113]
	v_mfma_f32_16x16x32_bf16 v[106:109], v[142:145], v[200:203], v[106:109]
	v_mfma_f32_16x16x32_bf16 v[94:97], v[168:171], v[214:217], v[94:97]
	v_mfma_f32_16x16x32_bf16 v[90:93], v[142:145], v[214:217], v[90:93]
	v_mfma_f32_16x16x32_bf16 v[78:81], v[168:171], v[222:225], v[78:81]
	v_mfma_f32_16x16x32_bf16 v[74:77], v[142:145], v[222:225], v[74:77]
	v_mfma_f32_16x16x32_bf16 v[122:125], v[138:141], v[196:199], v[122:125]
	v_mfma_f32_16x16x32_bf16 v[126:129], v[176:179], v[196:199], v[126:129]
	v_mfma_f32_16x16x32_bf16 v[110:113], v[138:141], v[204:207], v[110:113]
	v_mfma_f32_16x16x32_bf16 v[106:109], v[176:179], v[204:207], v[106:109]
	v_mfma_f32_16x16x32_bf16 v[94:97], v[138:141], v[218:221], v[94:97]
	v_mfma_f32_16x16x32_bf16 v[90:93], v[176:179], v[218:221], v[90:93]
	v_mfma_f32_16x16x32_bf16 v[78:81], v[138:141], v[226:229], v[78:81]
	v_mfma_f32_16x16x32_bf16 v[74:77], v[176:179], v[226:229], v[74:77]
	s_setprio 0
	s_setprio 1
	v_mfma_f32_16x16x32_bf16 v[118:121], v[172:175], v[192:195], v[118:121]
	v_mfma_f32_16x16x32_bf16 v[114:117], v[184:187], v[192:195], v[114:117]
	v_mfma_f32_16x16x32_bf16 v[102:105], v[172:175], v[200:203], v[102:105]
	v_mfma_f32_16x16x32_bf16 v[98:101], v[184:187], v[200:203], v[98:101]
	v_mfma_f32_16x16x32_bf16 v[86:89], v[172:175], v[214:217], v[86:89]
	v_mfma_f32_16x16x32_bf16 v[82:85], v[184:187], v[214:217], v[82:85]
	v_mfma_f32_16x16x32_bf16 v[70:73], v[172:175], v[222:225], v[70:73]
	v_mfma_f32_16x16x32_bf16 v[66:69], v[184:187], v[222:225], v[66:69]
	v_mfma_f32_16x16x32_bf16 v[118:121], v[180:183], v[196:199], v[118:121]
	v_mfma_f32_16x16x32_bf16 v[114:117], v[188:191], v[196:199], v[114:117]
	v_mfma_f32_16x16x32_bf16 v[102:105], v[180:183], v[204:207], v[102:105]
	v_mfma_f32_16x16x32_bf16 v[98:101], v[188:191], v[204:207], v[98:101]
	v_mfma_f32_16x16x32_bf16 v[86:89], v[180:183], v[218:221], v[86:89]
	v_mfma_f32_16x16x32_bf16 v[82:85], v[188:191], v[218:221], v[82:85]
	v_mfma_f32_16x16x32_bf16 v[70:73], v[180:183], v[226:229], v[70:73]
	v_mfma_f32_16x16x32_bf16 v[66:69], v[188:191], v[226:229], v[66:69]
	s_setprio 0
	s_barrier
	s_addk_i32 s51, 0x80
	s_mov_b32 m0, s61
	v_add_u32_e32 v133, s51, v146
	ds_read_b128 v[192:195], v131 offset:49152
	ds_read_b128 v[196:199], v131 offset:50176
	ds_read_b128 v[200:203], v131 offset:51200
	ds_read_b128 v[204:207], v131 offset:52224
	ds_read_b128 v[214:217], v131 offset:53248
	ds_read_b128 v[218:221], v131 offset:54272
	ds_read_b128 v[222:225], v131 offset:55296
	ds_read_b128 v[226:229], v131 offset:56320
	global_load_lds_dwordx4 v133, s[8:9]
	v_add_u32_e32 v133, s45, v133
	s_mov_b32 m0, s62
	s_nop 0
	global_load_lds_dwordx4 v133, s[8:9]
	v_add_u32_e32 v133, s51, v147
	s_mov_b32 m0, s65
	s_nop 0
	global_load_lds_dwordx4 v133, s[8:9]
	v_add_u32_e32 v133, s45, v133
	s_mov_b32 m0, s66
	s_nop 0
	global_load_lds_dwordx4 v133, s[8:9]
	v_add_u32_e32 v133, s48, v149
	s_mov_b32 m0, s63
	s_nop 0
	global_load_lds_dwordx4 v133, s[6:7]
	v_add_u32_e32 v133, s44, v133
	s_mov_b32 m0, s64
	s_nop 0
	global_load_lds_dwordx4 v133, s[6:7]
	s_waitcnt vmcnt(8)
	s_waitcnt lgkmcnt(0)
	s_barrier
	s_setprio 1
	s_waitcnt lgkmcnt(0)
	v_mfma_f32_16x16x32_bf16 v[62:65], v[168:171], v[192:195], v[62:65]
	v_mfma_f32_16x16x32_bf16 v[58:61], v[142:145], v[192:195], v[58:61]
	v_mfma_f32_16x16x32_bf16 v[46:49], v[168:171], v[200:203], v[46:49]
	v_mfma_f32_16x16x32_bf16 v[42:45], v[142:145], v[200:203], v[42:45]
	v_mfma_f32_16x16x32_bf16 v[30:33], v[168:171], v[214:217], v[30:33]
	v_mfma_f32_16x16x32_bf16 v[26:29], v[142:145], v[214:217], v[26:29]
	v_mfma_f32_16x16x32_bf16 v[14:17], v[168:171], v[222:225], v[14:17]
	v_mfma_f32_16x16x32_bf16 v[10:13], v[142:145], v[222:225], v[10:13]
	v_mfma_f32_16x16x32_bf16 v[62:65], v[138:141], v[196:199], v[62:65]
	v_mfma_f32_16x16x32_bf16 v[58:61], v[176:179], v[196:199], v[58:61]
	v_mfma_f32_16x16x32_bf16 v[46:49], v[138:141], v[204:207], v[46:49]
	v_mfma_f32_16x16x32_bf16 v[42:45], v[176:179], v[204:207], v[42:45]
	v_mfma_f32_16x16x32_bf16 v[30:33], v[138:141], v[218:221], v[30:33]
	v_mfma_f32_16x16x32_bf16 v[26:29], v[176:179], v[218:221], v[26:29]
	v_mfma_f32_16x16x32_bf16 v[14:17], v[138:141], v[226:229], v[14:17]
	v_mfma_f32_16x16x32_bf16 v[10:13], v[176:179], v[226:229], v[10:13]
	s_setprio 0
	s_setprio 1
	v_mfma_f32_16x16x32_bf16 v[54:57], v[172:175], v[192:195], v[54:57]
	v_mfma_f32_16x16x32_bf16 v[50:53], v[184:187], v[192:195], v[50:53]
	v_mfma_f32_16x16x32_bf16 v[38:41], v[172:175], v[200:203], v[38:41]
	v_mfma_f32_16x16x32_bf16 v[34:37], v[184:187], v[200:203], v[34:37]
	v_mfma_f32_16x16x32_bf16 v[22:25], v[172:175], v[214:217], v[22:25]
	v_mfma_f32_16x16x32_bf16 v[18:21], v[184:187], v[214:217], v[18:21]
	v_mfma_f32_16x16x32_bf16 v[6:9], v[172:175], v[222:225], v[6:9]
	v_mfma_f32_16x16x32_bf16 v[2:5], v[184:187], v[222:225], v[2:5]
	v_mfma_f32_16x16x32_bf16 v[54:57], v[180:183], v[196:199], v[54:57]
	v_mfma_f32_16x16x32_bf16 v[50:53], v[188:191], v[196:199], v[50:53]
	v_mfma_f32_16x16x32_bf16 v[38:41], v[180:183], v[204:207], v[38:41]
	v_mfma_f32_16x16x32_bf16 v[34:37], v[188:191], v[204:207], v[34:37]
	v_mfma_f32_16x16x32_bf16 v[22:25], v[180:183], v[218:221], v[22:25]
	v_mfma_f32_16x16x32_bf16 v[18:21], v[188:191], v[218:221], v[18:21]
	v_mfma_f32_16x16x32_bf16 v[6:9], v[180:183], v[226:229], v[6:9]
	v_mfma_f32_16x16x32_bf16 v[2:5], v[188:191], v[226:229], v[2:5]
	s_setprio 0
	s_barrier
	s_addk_i32 s30, 0x100
	s_cmp_ge_i32 s49, s67
	s_mov_b32 s46, s50
	s_mov_b32 s48, s49
	s_cbranch_scc0 .LBB0_2047

.LBB0_2335:
	s_andn2_b64 vcc, exec, s[14:15]
	s_cbranch_vccnz .Lzs_9
	s_add_i32 s50, s87, 0x80
	s_add_i32 s87, s75, 0x100
	s_mov_b32 s88, 0
	ds_read_b128 v[130:133], v194
	ds_read_b128 v[134:137], v195
	ds_read_b128 v[138:141], v190
	ds_read_b128 v[142:145], v191
	ds_read_b128 v[146:149], v196
	ds_read_b128 v[150:153], v197
	ds_read_b128 v[154:157], v198
	ds_read_b128 v[158:161], v199
	s_add_i32 s75, s50, 0x80
	s_cmp_eq_u32 s70, s88
	s_cselect_b32 s89, s51, s87
	s_cselect_b32 s75, s49, s75
	v_add_u32_e32 v178, s50, v207
	s_add_i32 m0, s53, 0xc000
	ds_read_b128 v[162:165], v208
	ds_read_b128 v[166:169], v208 offset:1024
	ds_read_b128 v[170:173], v208 offset:2048
	ds_read_b128 v[180:183], v208 offset:3072
	ds_read_b128 v[214:217], v208 offset:4096
	ds_read_b128 v[218:221], v208 offset:5120
	ds_read_b128 v[222:225], v208 offset:6144
	ds_read_b128 v[226:229], v208 offset:7168
	global_load_lds_dwordx4 v178, s[4:5]
	v_add_u32_e32 v178, s50, v206
	s_add_i32 m0, s53, 0xe000
	s_nop 0
	global_load_lds_dwordx4 v178, s[4:5]
	s_waitcnt vmcnt(8)
	s_waitcnt lgkmcnt(0)
	s_barrier
	s_setprio 1
	s_waitcnt lgkmcnt(0)
	v_mfma_f32_16x16x32_bf16 v[126:129], v[138:141], v[162:165], 0
	v_mfma_f32_16x16x32_bf16 v[122:125], v[134:137], v[162:165], 0
	v_mfma_f32_16x16x32_bf16 v[110:113], v[138:141], v[170:173], 0
	v_mfma_f32_16x16x32_bf16 v[106:109], v[134:137], v[170:173], 0
	v_mfma_f32_16x16x32_bf16 v[94:97], v[138:141], v[214:217], 0
	v_mfma_f32_16x16x32_bf16 v[90:93], v[134:137], v[214:217], 0
	v_mfma_f32_16x16x32_bf16 v[78:81], v[138:141], v[222:225], 0
	v_mfma_f32_16x16x32_bf16 v[74:77], v[134:137], v[222:225], 0
	v_mfma_f32_16x16x32_bf16 v[126:129], v[130:133], v[166:169], v[126:129]
	v_mfma_f32_16x16x32_bf16 v[122:125], v[146:149], v[166:169], v[122:125]
	v_mfma_f32_16x16x32_bf16 v[110:113], v[130:133], v[180:183], v[110:113]
	v_mfma_f32_16x16x32_bf16 v[106:109], v[146:149], v[180:183], v[106:109]
	v_mfma_f32_16x16x32_bf16 v[94:97], v[130:133], v[218:221], v[94:97]
	v_mfma_f32_16x16x32_bf16 v[90:93], v[146:149], v[218:221], v[90:93]
	v_mfma_f32_16x16x32_bf16 v[78:81], v[130:133], v[226:229], v[78:81]
	v_mfma_f32_16x16x32_bf16 v[74:77], v[146:149], v[226:229], v[74:77]
	s_setprio 0
	s_setprio 1
	v_mfma_f32_16x16x32_bf16 v[118:121], v[142:145], v[162:165], 0
	v_mfma_f32_16x16x32_bf16 v[114:117], v[154:157], v[162:165], 0
	v_mfma_f32_16x16x32_bf16 v[102:105], v[142:145], v[170:173], 0
	v_mfma_f32_16x16x32_bf16 v[98:101], v[154:157], v[170:173], 0
	v_mfma_f32_16x16x32_bf16 v[86:89], v[142:145], v[214:217], 0
	v_mfma_f32_16x16x32_bf16 v[82:85], v[154:157], v[214:217], 0
	v_mfma_f32_16x16x32_bf16 v[70:73], v[142:145], v[222:225], 0
	v_mfma_f32_16x16x32_bf16 v[66:69], v[154:157], v[222:225], 0
	v_mfma_f32_16x16x32_bf16 v[118:121], v[150:153], v[166:169], v[118:121]
	v_mfma_f32_16x16x32_bf16 v[114:117], v[158:161], v[166:169], v[114:117]
	v_mfma_f32_16x16x32_bf16 v[102:105], v[150:153], v[180:183], v[102:105]
	v_mfma_f32_16x16x32_bf16 v[98:101], v[158:161], v[180:183], v[98:101]
	v_mfma_f32_16x16x32_bf16 v[86:89], v[150:153], v[218:221], v[86:89]
	v_mfma_f32_16x16x32_bf16 v[82:85], v[158:161], v[218:221], v[82:85]
	v_mfma_f32_16x16x32_bf16 v[70:73], v[150:153], v[226:229], v[70:73]
	v_mfma_f32_16x16x32_bf16 v[66:69], v[158:161], v[226:229], v[66:69]
	s_setprio 0
	s_barrier
	s_mov_b32 m0, s54
	v_add_u32_e32 v178, s89, v184
	ds_read_b128 v[162:165], v208 offset:16384
	ds_read_b128 v[166:169], v208 offset:17408
	ds_read_b128 v[170:173], v208 offset:18432
	ds_read_b128 v[180:183], v208 offset:19456
	ds_read_b128 v[214:217], v208 offset:20480
	ds_read_b128 v[218:221], v208 offset:21504
	ds_read_b128 v[222:225], v208 offset:22528
	ds_read_b128 v[226:229], v208 offset:23552
	global_load_lds_dwordx4 v178, s[6:7]
	v_add_u32_e32 v178, s52, v178
	s_mov_b32 m0, s55
	s_nop 0
	global_load_lds_dwordx4 v178, s[6:7]
	v_add_u32_e32 v178, s89, v185
	s_mov_b32 m0, s56
	s_nop 0
	global_load_lds_dwordx4 v178, s[6:7]
	v_add_u32_e32 v178, s52, v178
	s_mov_b32 m0, s57
	s_nop 0
	global_load_lds_dwordx4 v178, s[6:7]
	v_add_u32_e32 v178, s75, v1
	s_mov_b32 m0, s53
	s_nop 0
	global_load_lds_dwordx4 v178, s[4:5]
	v_add_u32_e32 v178, s45, v178
	s_mov_b32 m0, s58
	s_nop 0
	global_load_lds_dwordx4 v178, s[4:5]
	s_waitcnt vmcnt(8)
	s_waitcnt lgkmcnt(0)
	s_barrier
	s_setprio 1
	s_waitcnt lgkmcnt(0)
	v_mfma_f32_16x16x32_bf16 v[62:65], v[138:141], v[162:165], 0
	v_mfma_f32_16x16x32_bf16 v[58:61], v[134:137], v[162:165], 0
	v_mfma_f32_16x16x32_bf16 v[46:49], v[138:141], v[170:173], 0
	v_mfma_f32_16x16x32_bf16 v[42:45], v[134:137], v[170:173], 0
	v_mfma_f32_16x16x32_bf16 v[30:33], v[138:141], v[214:217], 0
	v_mfma_f32_16x16x32_bf16 v[26:29], v[134:137], v[214:217], 0
	v_mfma_f32_16x16x32_bf16 v[14:17], v[138:141], v[222:225], 0
	v_mfma_f32_16x16x32_bf16 v[10:13], v[134:137], v[222:225], 0
	v_mfma_f32_16x16x32_bf16 v[62:65], v[130:133], v[166:169], v[62:65]
	v_mfma_f32_16x16x32_bf16 v[58:61], v[146:149], v[166:169], v[58:61]
	v_mfma_f32_16x16x32_bf16 v[46:49], v[130:133], v[180:183], v[46:49]
	v_mfma_f32_16x16x32_bf16 v[42:45], v[146:149], v[180:183], v[42:45]
	v_mfma_f32_16x16x32_bf16 v[30:33], v[130:133], v[218:221], v[30:33]
	v_mfma_f32_16x16x32_bf16 v[26:29], v[146:149], v[218:221], v[26:29]
	v_mfma_f32_16x16x32_bf16 v[14:17], v[130:133], v[226:229], v[14:17]
	v_mfma_f32_16x16x32_bf16 v[10:13], v[146:149], v[226:229], v[10:13]
	s_setprio 0
	s_setprio 1
	v_mfma_f32_16x16x32_bf16 v[54:57], v[142:145], v[162:165], 0
	v_mfma_f32_16x16x32_bf16 v[50:53], v[154:157], v[162:165], 0
	v_mfma_f32_16x16x32_bf16 v[38:41], v[142:145], v[170:173], 0
	v_mfma_f32_16x16x32_bf16 v[34:37], v[154:157], v[170:173], 0
	v_mfma_f32_16x16x32_bf16 v[22:25], v[142:145], v[214:217], 0
	v_mfma_f32_16x16x32_bf16 v[18:21], v[154:157], v[214:217], 0
	v_mfma_f32_16x16x32_bf16 v[6:9], v[142:145], v[222:225], 0
	v_mfma_f32_16x16x32_bf16 v[2:5], v[154:157], v[222:225], 0
	v_mfma_f32_16x16x32_bf16 v[54:57], v[150:153], v[166:169], v[54:57]
	v_mfma_f32_16x16x32_bf16 v[50:53], v[158:161], v[166:169], v[50:53]
	v_mfma_f32_16x16x32_bf16 v[38:41], v[150:153], v[180:183], v[38:41]
	v_mfma_f32_16x16x32_bf16 v[34:37], v[158:161], v[180:183], v[34:37]
	v_mfma_f32_16x16x32_bf16 v[22:25], v[150:153], v[218:221], v[22:25]
	v_mfma_f32_16x16x32_bf16 v[18:21], v[158:161], v[218:221], v[18:21]
	v_mfma_f32_16x16x32_bf16 v[6:9], v[150:153], v[226:229], v[6:9]
	v_mfma_f32_16x16x32_bf16 v[2:5], v[158:161], v[226:229], v[2:5]
	s_setprio 0
	s_barrier
	s_branch .Lmid_7

.Lmid_7:
	ds_read_b128 v[130:133], v200
	ds_read_b128 v[134:137], v201
	ds_read_b128 v[138:141], v192
	ds_read_b128 v[142:145], v193
	ds_read_b128 v[146:149], v202
	ds_read_b128 v[150:153], v203
	ds_read_b128 v[154:157], v204
	ds_read_b128 v[158:161], v205
	s_mov_b32 m0, s59
	v_add_u32_e32 v178, s75, v186
	ds_read_b128 v[162:165], v208 offset:32768
	ds_read_b128 v[166:169], v208 offset:33792
	ds_read_b128 v[170:173], v208 offset:34816
	ds_read_b128 v[180:183], v208 offset:35840
	ds_read_b128 v[214:217], v208 offset:36864
	ds_read_b128 v[218:221], v208 offset:37888
	ds_read_b128 v[222:225], v208 offset:38912
	ds_read_b128 v[226:229], v208 offset:39936
	global_load_lds_dwordx4 v178, s[4:5]
	v_add_u32_e32 v178, s45, v178
	s_mov_b32 m0, s60
	s_nop 0
	global_load_lds_dwordx4 v178, s[4:5]
	s_waitcnt vmcnt(8)
	s_waitcnt lgkmcnt(0)
	s_barrier
	s_setprio 1
	s_waitcnt lgkmcnt(0)
	v_mfma_f32_16x16x32_bf16 v[126:129], v[138:141], v[162:165], v[126:129]
	v_mfma_f32_16x16x32_bf16 v[122:125], v[134:137], v[162:165], v[122:125]
	v_mfma_f32_16x16x32_bf16 v[110:113], v[138:141], v[170:173], v[110:113]
	v_mfma_f32_16x16x32_bf16 v[106:109], v[134:137], v[170:173], v[106:109]
	v_mfma_f32_16x16x32_bf16 v[94:97], v[138:141], v[214:217], v[94:97]
	v_mfma_f32_16x16x32_bf16 v[90:93], v[134:137], v[214:217], v[90:93]
	v_mfma_f32_16x16x32_bf16 v[78:81], v[138:141], v[222:225], v[78:81]
	v_mfma_f32_16x16x32_bf16 v[74:77], v[134:137], v[222:225], v[74:77]
	v_mfma_f32_16x16x32_bf16 v[126:129], v[130:133], v[166:169], v[126:129]
	v_mfma_f32_16x16x32_bf16 v[122:125], v[146:149], v[166:169], v[122:125]
	v_mfma_f32_16x16x32_bf16 v[110:113], v[130:133], v[180:183], v[110:113]
	v_mfma_f32_16x16x32_bf16 v[106:109], v[146:149], v[180:183], v[106:109]
	v_mfma_f32_16x16x32_bf16 v[94:97], v[130:133], v[218:221], v[94:97]
	v_mfma_f32_16x16x32_bf16 v[90:93], v[146:149], v[218:221], v[90:93]
	v_mfma_f32_16x16x32_bf16 v[78:81], v[130:133], v[226:229], v[78:81]
	v_mfma_f32_16x16x32_bf16 v[74:77], v[146:149], v[226:229], v[74:77]
	s_setprio 0
	s_setprio 1
	v_mfma_f32_16x16x32_bf16 v[118:121], v[142:145], v[162:165], v[118:121]
	v_mfma_f32_16x16x32_bf16 v[114:117], v[154:157], v[162:165], v[114:117]
	v_mfma_f32_16x16x32_bf16 v[102:105], v[142:145], v[170:173], v[102:105]
	v_mfma_f32_16x16x32_bf16 v[98:101], v[154:157], v[170:173], v[98:101]
	v_mfma_f32_16x16x32_bf16 v[86:89], v[142:145], v[214:217], v[86:89]
	v_mfma_f32_16x16x32_bf16 v[82:85], v[154:157], v[214:217], v[82:85]
	v_mfma_f32_16x16x32_bf16 v[70:73], v[142:145], v[222:225], v[70:73]
	v_mfma_f32_16x16x32_bf16 v[66:69], v[154:157], v[222:225], v[66:69]
	v_mfma_f32_16x16x32_bf16 v[118:121], v[150:153], v[166:169], v[118:121]
	v_mfma_f32_16x16x32_bf16 v[114:117], v[158:161], v[166:169], v[114:117]
	v_mfma_f32_16x16x32_bf16 v[102:105], v[150:153], v[180:183], v[102:105]
	v_mfma_f32_16x16x32_bf16 v[98:101], v[158:161], v[180:183], v[98:101]
	v_mfma_f32_16x16x32_bf16 v[86:89], v[150:153], v[218:221], v[86:89]
	v_mfma_f32_16x16x32_bf16 v[82:85], v[158:161], v[218:221], v[82:85]
	v_mfma_f32_16x16x32_bf16 v[70:73], v[150:153], v[226:229], v[70:73]
	v_mfma_f32_16x16x32_bf16 v[66:69], v[158:161], v[226:229], v[66:69]
	s_setprio 0
	s_barrier
	s_addk_i32 s89, 0x80
	s_mov_b32 m0, s63
	v_add_u32_e32 v178, s89, v184
	ds_read_b128 v[162:165], v208 offset:49152
	ds_read_b128 v[166:169], v208 offset:50176
	ds_read_b128 v[170:173], v208 offset:51200
	ds_read_b128 v[180:183], v208 offset:52224
	ds_read_b128 v[214:217], v208 offset:53248
	ds_read_b128 v[218:221], v208 offset:54272
	ds_read_b128 v[222:225], v208 offset:55296
	ds_read_b128 v[226:229], v208 offset:56320
	global_load_lds_dwordx4 v178, s[6:7]
	v_add_u32_e32 v178, s52, v178
	s_mov_b32 m0, s64
	s_nop 0
	global_load_lds_dwordx4 v178, s[6:7]
	v_add_u32_e32 v178, s89, v185
	s_mov_b32 m0, s67
	s_nop 0
	global_load_lds_dwordx4 v178, s[6:7]
	v_add_u32_e32 v178, s52, v178
	s_mov_b32 m0, s68
	s_nop 0
	global_load_lds_dwordx4 v178, s[6:7]
	v_add_u32_e32 v178, s75, v189
	s_mov_b32 m0, s65
	s_nop 0
	global_load_lds_dwordx4 v178, s[4:5]
	v_add_u32_e32 v178, s45, v178
	s_mov_b32 m0, s66
	s_nop 0
	global_load_lds_dwordx4 v178, s[4:5]
	s_waitcnt vmcnt(8)
	s_waitcnt lgkmcnt(0)
	s_barrier
	s_setprio 1
	s_waitcnt lgkmcnt(0)
	v_mfma_f32_16x16x32_bf16 v[62:65], v[138:141], v[162:165], v[62:65]
	v_mfma_f32_16x16x32_bf16 v[58:61], v[134:137], v[162:165], v[58:61]
	v_mfma_f32_16x16x32_bf16 v[46:49], v[138:141], v[170:173], v[46:49]
	v_mfma_f32_16x16x32_bf16 v[42:45], v[134:137], v[170:173], v[42:45]
	v_mfma_f32_16x16x32_bf16 v[30:33], v[138:141], v[214:217], v[30:33]
	v_mfma_f32_16x16x32_bf16 v[26:29], v[134:137], v[214:217], v[26:29]
	v_mfma_f32_16x16x32_bf16 v[14:17], v[138:141], v[222:225], v[14:17]
	v_mfma_f32_16x16x32_bf16 v[10:13], v[134:137], v[222:225], v[10:13]
	v_mfma_f32_16x16x32_bf16 v[62:65], v[130:133], v[166:169], v[62:65]
	v_mfma_f32_16x16x32_bf16 v[58:61], v[146:149], v[166:169], v[58:61]
	v_mfma_f32_16x16x32_bf16 v[46:49], v[130:133], v[180:183], v[46:49]
	v_mfma_f32_16x16x32_bf16 v[42:45], v[146:149], v[180:183], v[42:45]
	v_mfma_f32_16x16x32_bf16 v[30:33], v[130:133], v[218:221], v[30:33]
	v_mfma_f32_16x16x32_bf16 v[26:29], v[146:149], v[218:221], v[26:29]
	v_mfma_f32_16x16x32_bf16 v[14:17], v[130:133], v[226:229], v[14:17]
	v_mfma_f32_16x16x32_bf16 v[10:13], v[146:149], v[226:229], v[10:13]
	s_setprio 0
	s_setprio 1
	v_mfma_f32_16x16x32_bf16 v[54:57], v[142:145], v[162:165], v[54:57]
	v_mfma_f32_16x16x32_bf16 v[50:53], v[154:157], v[162:165], v[50:53]
	v_mfma_f32_16x16x32_bf16 v[38:41], v[142:145], v[170:173], v[38:41]
	v_mfma_f32_16x16x32_bf16 v[34:37], v[154:157], v[170:173], v[34:37]
	v_mfma_f32_16x16x32_bf16 v[22:25], v[142:145], v[214:217], v[22:25]
	v_mfma_f32_16x16x32_bf16 v[18:21], v[154:157], v[214:217], v[18:21]
	v_mfma_f32_16x16x32_bf16 v[6:9], v[142:145], v[222:225], v[6:9]
	v_mfma_f32_16x16x32_bf16 v[2:5], v[154:157], v[222:225], v[2:5]
	v_mfma_f32_16x16x32_bf16 v[54:57], v[150:153], v[166:169], v[54:57]
	v_mfma_f32_16x16x32_bf16 v[50:53], v[158:161], v[166:169], v[50:53]
	v_mfma_f32_16x16x32_bf16 v[38:41], v[150:153], v[180:183], v[38:41]
	v_mfma_f32_16x16x32_bf16 v[34:37], v[158:161], v[180:183], v[34:37]
	v_mfma_f32_16x16x32_bf16 v[22:25], v[150:153], v[218:221], v[22:25]
	v_mfma_f32_16x16x32_bf16 v[18:21], v[158:161], v[218:221], v[18:21]
	v_mfma_f32_16x16x32_bf16 v[6:9], v[150:153], v[226:229], v[6:9]
	v_mfma_f32_16x16x32_bf16 v[2:5], v[158:161], v[226:229], v[2:5]
	s_setprio 0
	s_barrier
	s_add_i32 s88, s88, 2
	s_addk_i32 s50, 0x100
	s_addk_i32 s87, 0x100
	s_cmp_ge_i32 s88, s61
	s_cbranch_scc0 .LBB0_2337

.LBB0_2519:
	s_andn2_b64 vcc, exec, s[14:15]
	s_cbranch_vccnz .Lzs_10
	s_add_i32 s56, s96, 0x80
	s_add_i32 s57, s74, 0x100
	s_mov_b32 s74, 0
	ds_read_b128 v[90:93], v160
	ds_read_b128 v[94:97], v161
	ds_read_b128 v[142:145], v156
	ds_read_b128 v[146:149], v157
	ds_read_b128 v[176:179], v162
	ds_read_b128 v[180:183], v163
	ds_read_b128 v[184:187], v164
	ds_read_b128 v[188:191], v165
	s_add_i32 s96, s56, 0x80
	s_cmp_eq_u32 s81, s74
	s_cselect_b32 vcc_lo, s55, s57
	s_cselect_b32 s96, s45, s96
	v_add_u32_e32 v175, s56, v173
	s_add_i32 m0, s60, 0xc000
	ds_read_b128 v[192:195], v174
	ds_read_b128 v[196:199], v174 offset:1024
	ds_read_b128 v[200:203], v174 offset:2048
	ds_read_b128 v[204:207], v174 offset:3072
	ds_read_b128 v[214:217], v174 offset:4096
	ds_read_b128 v[218:221], v174 offset:5120
	ds_read_b128 v[222:225], v174 offset:6144
	ds_read_b128 v[226:229], v174 offset:7168
	global_load_lds_dwordx4 v175, s[4:5]
	v_add_u32_e32 v175, s56, v172
	s_add_i32 m0, s60, 0xe000
	s_nop 0
	global_load_lds_dwordx4 v175, s[4:5]
	s_waitcnt vmcnt(8)
	s_waitcnt lgkmcnt(0)
	s_barrier
	s_setprio 1
	s_waitcnt lgkmcnt(0)
	v_mfma_f32_16x16x32_bf16 v[134:137], v[142:145], v[192:195], 0
	v_mfma_f32_16x16x32_bf16 v[130:133], v[94:97], v[192:195], 0
	v_mfma_f32_16x16x32_bf16 v[126:129], v[142:145], v[200:203], 0
	v_mfma_f32_16x16x32_bf16 v[122:125], v[94:97], v[200:203], 0
	v_mfma_f32_16x16x32_bf16 v[118:121], v[142:145], v[214:217], 0
	v_mfma_f32_16x16x32_bf16 v[114:117], v[94:97], v[214:217], 0
	v_mfma_f32_16x16x32_bf16 v[110:113], v[142:145], v[222:225], 0
	v_mfma_f32_16x16x32_bf16 v[106:109], v[94:97], v[222:225], 0
	v_mfma_f32_16x16x32_bf16 v[134:137], v[90:93], v[196:199], v[134:137]
	v_mfma_f32_16x16x32_bf16 v[130:133], v[176:179], v[196:199], v[130:133]
	v_mfma_f32_16x16x32_bf16 v[126:129], v[90:93], v[204:207], v[126:129]
	v_mfma_f32_16x16x32_bf16 v[122:125], v[176:179], v[204:207], v[122:125]
	v_mfma_f32_16x16x32_bf16 v[118:121], v[90:93], v[218:221], v[118:121]
	v_mfma_f32_16x16x32_bf16 v[114:117], v[176:179], v[218:221], v[114:117]
	v_mfma_f32_16x16x32_bf16 v[110:113], v[90:93], v[226:229], v[110:113]
	v_mfma_f32_16x16x32_bf16 v[106:109], v[176:179], v[226:229], v[106:109]
	s_setprio 0
	s_setprio 1
	v_mfma_f32_16x16x32_bf16 v[62:65], v[146:149], v[192:195], 0
	v_mfma_f32_16x16x32_bf16 v[58:61], v[184:187], v[192:195], 0
	v_mfma_f32_16x16x32_bf16 v[54:57], v[146:149], v[200:203], 0
	v_mfma_f32_16x16x32_bf16 v[50:53], v[184:187], v[200:203], 0
	v_mfma_f32_16x16x32_bf16 v[46:49], v[146:149], v[214:217], 0
	v_mfma_f32_16x16x32_bf16 v[42:45], v[184:187], v[214:217], 0
	v_mfma_f32_16x16x32_bf16 v[38:41], v[146:149], v[222:225], 0
	v_mfma_f32_16x16x32_bf16 v[34:37], v[184:187], v[222:225], 0
	v_mfma_f32_16x16x32_bf16 v[62:65], v[180:183], v[196:199], v[62:65]
	v_mfma_f32_16x16x32_bf16 v[58:61], v[188:191], v[196:199], v[58:61]
	v_mfma_f32_16x16x32_bf16 v[54:57], v[180:183], v[204:207], v[54:57]
	v_mfma_f32_16x16x32_bf16 v[50:53], v[188:191], v[204:207], v[50:53]
	v_mfma_f32_16x16x32_bf16 v[46:49], v[180:183], v[218:221], v[46:49]
	v_mfma_f32_16x16x32_bf16 v[42:45], v[188:191], v[218:221], v[42:45]
	v_mfma_f32_16x16x32_bf16 v[38:41], v[180:183], v[226:229], v[38:41]
	v_mfma_f32_16x16x32_bf16 v[34:37], v[188:191], v[226:229], v[34:37]
	s_setprio 0
	s_barrier
	s_mov_b32 m0, s61
	v_add_u32_e32 v175, vcc_lo, v150
	ds_read_b128 v[192:195], v174 offset:16384
	ds_read_b128 v[196:199], v174 offset:17408
	ds_read_b128 v[200:203], v174 offset:18432
	ds_read_b128 v[204:207], v174 offset:19456
	ds_read_b128 v[214:217], v174 offset:20480
	ds_read_b128 v[218:221], v174 offset:21504
	ds_read_b128 v[222:225], v174 offset:22528
	ds_read_b128 v[226:229], v174 offset:23552
	global_load_lds_dwordx4 v175, s[6:7]
	v_add_u32_e32 v175, s59, v175
	s_mov_b32 m0, s62
	s_nop 0
	global_load_lds_dwordx4 v175, s[6:7]
	v_add_u32_e32 v175, vcc_lo, v151
	s_mov_b32 m0, s63
	s_nop 0
	global_load_lds_dwordx4 v175, s[6:7]
	v_add_u32_e32 v175, s59, v175
	s_mov_b32 m0, s64
	s_nop 0
	global_load_lds_dwordx4 v175, s[6:7]
	v_add_u32_e32 v175, s96, v1
	s_mov_b32 m0, s60
	s_nop 0
	global_load_lds_dwordx4 v175, s[4:5]
	v_add_u32_e32 v175, s58, v175
	s_mov_b32 m0, s65
	s_nop 0
	global_load_lds_dwordx4 v175, s[4:5]
	s_waitcnt vmcnt(8)
	s_waitcnt lgkmcnt(0)
	s_barrier
	s_setprio 1
	s_waitcnt lgkmcnt(0)
	v_mfma_f32_16x16x32_bf16 v[102:105], v[142:145], v[192:195], 0
	v_mfma_f32_16x16x32_bf16 v[98:101], v[94:97], v[192:195], 0
	v_mfma_f32_16x16x32_bf16 v[86:89], v[142:145], v[200:203], 0
	v_mfma_f32_16x16x32_bf16 v[82:85], v[94:97], v[200:203], 0
	v_mfma_f32_16x16x32_bf16 v[78:81], v[142:145], v[214:217], 0
	v_mfma_f32_16x16x32_bf16 v[74:77], v[94:97], v[214:217], 0
	v_mfma_f32_16x16x32_bf16 v[70:73], v[142:145], v[222:225], 0
	v_mfma_f32_16x16x32_bf16 v[66:69], v[94:97], v[222:225], 0
	v_mfma_f32_16x16x32_bf16 v[102:105], v[90:93], v[196:199], v[102:105]
	v_mfma_f32_16x16x32_bf16 v[98:101], v[176:179], v[196:199], v[98:101]
	v_mfma_f32_16x16x32_bf16 v[86:89], v[90:93], v[204:207], v[86:89]
	v_mfma_f32_16x16x32_bf16 v[82:85], v[176:179], v[204:207], v[82:85]
	v_mfma_f32_16x16x32_bf16 v[78:81], v[90:93], v[218:221], v[78:81]
	v_mfma_f32_16x16x32_bf16 v[74:77], v[176:179], v[218:221], v[74:77]
	v_mfma_f32_16x16x32_bf16 v[70:73], v[90:93], v[226:229], v[70:73]
	v_mfma_f32_16x16x32_bf16 v[66:69], v[176:179], v[226:229], v[66:69]
	s_setprio 0
	s_setprio 1
	v_mfma_f32_16x16x32_bf16 v[30:33], v[146:149], v[192:195], 0
	v_mfma_f32_16x16x32_bf16 v[26:29], v[184:187], v[192:195], 0
	v_mfma_f32_16x16x32_bf16 v[22:25], v[146:149], v[200:203], 0
	v_mfma_f32_16x16x32_bf16 v[18:21], v[184:187], v[200:203], 0
	v_mfma_f32_16x16x32_bf16 v[14:17], v[146:149], v[214:217], 0
	v_mfma_f32_16x16x32_bf16 v[10:13], v[184:187], v[214:217], 0
	v_mfma_f32_16x16x32_bf16 v[6:9], v[146:149], v[222:225], 0
	v_mfma_f32_16x16x32_bf16 v[2:5], v[184:187], v[222:225], 0
	v_mfma_f32_16x16x32_bf16 v[30:33], v[180:183], v[196:199], v[30:33]
	v_mfma_f32_16x16x32_bf16 v[26:29], v[188:191], v[196:199], v[26:29]
	v_mfma_f32_16x16x32_bf16 v[22:25], v[180:183], v[204:207], v[22:25]
	v_mfma_f32_16x16x32_bf16 v[18:21], v[188:191], v[204:207], v[18:21]
	v_mfma_f32_16x16x32_bf16 v[14:17], v[180:183], v[218:221], v[14:17]
	v_mfma_f32_16x16x32_bf16 v[10:13], v[188:191], v[218:221], v[10:13]
	v_mfma_f32_16x16x32_bf16 v[6:9], v[180:183], v[226:229], v[6:9]
	v_mfma_f32_16x16x32_bf16 v[2:5], v[188:191], v[226:229], v[2:5]
	s_setprio 0
	s_barrier
	s_branch .Lmid_8

.Lmid_8:
	ds_read_b128 v[90:93], v166
	ds_read_b128 v[94:97], v167
	ds_read_b128 v[142:145], v158
	ds_read_b128 v[146:149], v159
	ds_read_b128 v[176:179], v168
	ds_read_b128 v[180:183], v169
	ds_read_b128 v[184:187], v170
	ds_read_b128 v[188:191], v171
	s_mov_b32 m0, s66
	v_add_u32_e32 v175, s96, v152
	ds_read_b128 v[192:195], v174 offset:32768
	ds_read_b128 v[196:199], v174 offset:33792
	ds_read_b128 v[200:203], v174 offset:34816
	ds_read_b128 v[204:207], v174 offset:35840
	ds_read_b128 v[214:217], v174 offset:36864
	ds_read_b128 v[218:221], v174 offset:37888
	ds_read_b128 v[222:225], v174 offset:38912
	ds_read_b128 v[226:229], v174 offset:39936
	global_load_lds_dwordx4 v175, s[4:5]
	v_add_u32_e32 v175, s58, v175
	s_mov_b32 m0, s67
	s_nop 0
	global_load_lds_dwordx4 v175, s[4:5]
	s_waitcnt vmcnt(8)
	s_waitcnt lgkmcnt(0)
	s_barrier
	s_setprio 1
	s_waitcnt lgkmcnt(0)
	v_mfma_f32_16x16x32_bf16 v[134:137], v[142:145], v[192:195], v[134:137]
	v_mfma_f32_16x16x32_bf16 v[130:133], v[94:97], v[192:195], v[130:133]
	v_mfma_f32_16x16x32_bf16 v[126:129], v[142:145], v[200:203], v[126:129]
	v_mfma_f32_16x16x32_bf16 v[122:125], v[94:97], v[200:203], v[122:125]
	v_mfma_f32_16x16x32_bf16 v[118:121], v[142:145], v[214:217], v[118:121]
	v_mfma_f32_16x16x32_bf16 v[114:117], v[94:97], v[214:217], v[114:117]
	v_mfma_f32_16x16x32_bf16 v[110:113], v[142:145], v[222:225], v[110:113]
	v_mfma_f32_16x16x32_bf16 v[106:109], v[94:97], v[222:225], v[106:109]
	v_mfma_f32_16x16x32_bf16 v[134:137], v[90:93], v[196:199], v[134:137]
	v_mfma_f32_16x16x32_bf16 v[130:133], v[176:179], v[196:199], v[130:133]
	v_mfma_f32_16x16x32_bf16 v[126:129], v[90:93], v[204:207], v[126:129]
	v_mfma_f32_16x16x32_bf16 v[122:125], v[176:179], v[204:207], v[122:125]
	v_mfma_f32_16x16x32_bf16 v[118:121], v[90:93], v[218:221], v[118:121]
	v_mfma_f32_16x16x32_bf16 v[114:117], v[176:179], v[218:221], v[114:117]
	v_mfma_f32_16x16x32_bf16 v[110:113], v[90:93], v[226:229], v[110:113]
	v_mfma_f32_16x16x32_bf16 v[106:109], v[176:179], v[226:229], v[106:109]
	s_setprio 0
	s_setprio 1
	v_mfma_f32_16x16x32_bf16 v[62:65], v[146:149], v[192:195], v[62:65]
	v_mfma_f32_16x16x32_bf16 v[58:61], v[184:187], v[192:195], v[58:61]
	v_mfma_f32_16x16x32_bf16 v[54:57], v[146:149], v[200:203], v[54:57]
	v_mfma_f32_16x16x32_bf16 v[50:53], v[184:187], v[200:203], v[50:53]
	v_mfma_f32_16x16x32_bf16 v[46:49], v[146:149], v[214:217], v[46:49]
	v_mfma_f32_16x16x32_bf16 v[42:45], v[184:187], v[214:217], v[42:45]
	v_mfma_f32_16x16x32_bf16 v[38:41], v[146:149], v[222:225], v[38:41]
	v_mfma_f32_16x16x32_bf16 v[34:37], v[184:187], v[222:225], v[34:37]
	v_mfma_f32_16x16x32_bf16 v[62:65], v[180:183], v[196:199], v[62:65]
	v_mfma_f32_16x16x32_bf16 v[58:61], v[188:191], v[196:199], v[58:61]
	v_mfma_f32_16x16x32_bf16 v[54:57], v[180:183], v[204:207], v[54:57]
	v_mfma_f32_16x16x32_bf16 v[50:53], v[188:191], v[204:207], v[50:53]
	v_mfma_f32_16x16x32_bf16 v[46:49], v[180:183], v[218:221], v[46:49]
	v_mfma_f32_16x16x32_bf16 v[42:45], v[188:191], v[218:221], v[42:45]
	v_mfma_f32_16x16x32_bf16 v[38:41], v[180:183], v[226:229], v[38:41]
	v_mfma_f32_16x16x32_bf16 v[34:37], v[188:191], v[226:229], v[34:37]
	s_setprio 0
	s_barrier
	s_addk_i32 vcc_lo, 0x80
	s_mov_b32 m0, s71
	v_add_u32_e32 v175, vcc_lo, v150
	ds_read_b128 v[192:195], v174 offset:49152
	ds_read_b128 v[196:199], v174 offset:50176
	ds_read_b128 v[200:203], v174 offset:51200
	ds_read_b128 v[204:207], v174 offset:52224
	ds_read_b128 v[214:217], v174 offset:53248
	ds_read_b128 v[218:221], v174 offset:54272
	ds_read_b128 v[222:225], v174 offset:55296
	ds_read_b128 v[226:229], v174 offset:56320
	global_load_lds_dwordx4 v175, s[6:7]
	v_add_u32_e32 v175, s59, v175
	s_mov_b32 m0, s72
	s_nop 0
	global_load_lds_dwordx4 v175, s[6:7]
	v_add_u32_e32 v175, vcc_lo, v151
	s_mov_b32 m0, s77
	s_nop 0
	global_load_lds_dwordx4 v175, s[6:7]
	v_add_u32_e32 v175, s59, v175
	s_mov_b32 m0, s78
	s_nop 0
	global_load_lds_dwordx4 v175, s[6:7]
	v_add_u32_e32 v175, s96, v155
	s_mov_b32 m0, s73
	s_nop 0
	global_load_lds_dwordx4 v175, s[4:5]
	v_add_u32_e32 v175, s58, v175
	s_mov_b32 m0, s76
	s_nop 0
	global_load_lds_dwordx4 v175, s[4:5]
	s_waitcnt vmcnt(8)
	s_waitcnt lgkmcnt(0)
	s_barrier
	s_setprio 1
	s_waitcnt lgkmcnt(0)
	v_mfma_f32_16x16x32_bf16 v[102:105], v[142:145], v[192:195], v[102:105]
	v_mfma_f32_16x16x32_bf16 v[98:101], v[94:97], v[192:195], v[98:101]
	v_mfma_f32_16x16x32_bf16 v[86:89], v[142:145], v[200:203], v[86:89]
	v_mfma_f32_16x16x32_bf16 v[82:85], v[94:97], v[200:203], v[82:85]
	v_mfma_f32_16x16x32_bf16 v[78:81], v[142:145], v[214:217], v[78:81]
	v_mfma_f32_16x16x32_bf16 v[74:77], v[94:97], v[214:217], v[74:77]
	v_mfma_f32_16x16x32_bf16 v[70:73], v[142:145], v[222:225], v[70:73]
	v_mfma_f32_16x16x32_bf16 v[66:69], v[94:97], v[222:225], v[66:69]
	v_mfma_f32_16x16x32_bf16 v[102:105], v[90:93], v[196:199], v[102:105]
	v_mfma_f32_16x16x32_bf16 v[98:101], v[176:179], v[196:199], v[98:101]
	v_mfma_f32_16x16x32_bf16 v[86:89], v[90:93], v[204:207], v[86:89]
	v_mfma_f32_16x16x32_bf16 v[82:85], v[176:179], v[204:207], v[82:85]
	v_mfma_f32_16x16x32_bf16 v[78:81], v[90:93], v[218:221], v[78:81]
	v_mfma_f32_16x16x32_bf16 v[74:77], v[176:179], v[218:221], v[74:77]
	v_mfma_f32_16x16x32_bf16 v[70:73], v[90:93], v[226:229], v[70:73]
	v_mfma_f32_16x16x32_bf16 v[66:69], v[176:179], v[226:229], v[66:69]
	s_setprio 0
	s_setprio 1
	v_mfma_f32_16x16x32_bf16 v[30:33], v[146:149], v[192:195], v[30:33]
	v_mfma_f32_16x16x32_bf16 v[26:29], v[184:187], v[192:195], v[26:29]
	v_mfma_f32_16x16x32_bf16 v[22:25], v[146:149], v[200:203], v[22:25]
	v_mfma_f32_16x16x32_bf16 v[18:21], v[184:187], v[200:203], v[18:21]
	v_mfma_f32_16x16x32_bf16 v[14:17], v[146:149], v[214:217], v[14:17]
	v_mfma_f32_16x16x32_bf16 v[10:13], v[184:187], v[214:217], v[10:13]
	v_mfma_f32_16x16x32_bf16 v[6:9], v[146:149], v[222:225], v[6:9]
	v_mfma_f32_16x16x32_bf16 v[2:5], v[184:187], v[222:225], v[2:5]
	v_mfma_f32_16x16x32_bf16 v[30:33], v[180:183], v[196:199], v[30:33]
	v_mfma_f32_16x16x32_bf16 v[26:29], v[188:191], v[196:199], v[26:29]
	v_mfma_f32_16x16x32_bf16 v[22:25], v[180:183], v[204:207], v[22:25]
	v_mfma_f32_16x16x32_bf16 v[18:21], v[188:191], v[204:207], v[18:21]
	v_mfma_f32_16x16x32_bf16 v[14:17], v[180:183], v[218:221], v[14:17]
	v_mfma_f32_16x16x32_bf16 v[10:13], v[188:191], v[218:221], v[10:13]
	v_mfma_f32_16x16x32_bf16 v[6:9], v[180:183], v[226:229], v[6:9]
	v_mfma_f32_16x16x32_bf16 v[2:5], v[188:191], v[226:229], v[2:5]
	s_setprio 0
	s_barrier
	s_add_i32 s74, s74, 2
	s_addk_i32 s56, 0x100
	s_addk_i32 s57, 0x100
	s_cmp_ge_i32 s74, s69
	s_cbranch_scc0 .LBB0_2521

.LBB0_2595:
	s_andn2_b64 vcc, exec, s[12:13]
	s_cbranch_vccnz .Lzs_11
	s_add_i32 s60, s64, 0x80
	s_addk_i32 s63, 0x100
	s_mov_b32 s64, 0
	ds_read_b128 v[130:133], v206
	ds_read_b128 v[134:137], v207
	ds_read_b128 v[138:141], v202
	ds_read_b128 v[142:145], v203
	ds_read_b128 v[146:149], v208
	ds_read_b128 v[150:153], v209
	ds_read_b128 v[154:157], v211
	ds_read_b128 v[158:161], v213
	s_add_i32 s65, s60, 0x80
	s_cmp_eq_u32 s84, s64
	s_cselect_b32 s75, s61, s63
	s_cselect_b32 s65, s5, s65
	v_add_u32_e32 v194, s60, v221
	s_add_i32 m0, s45, 0xc000
	ds_read_b128 v[162:165], v222
	ds_read_b128 v[166:169], v222 offset:1024
	ds_read_b128 v[170:173], v222 offset:2048
	ds_read_b128 v[174:177], v222 offset:3072
	ds_read_b128 v[182:185], v222 offset:4096
	ds_read_b128 v[186:189], v222 offset:5120
	ds_read_b128 v[190:193], v222 offset:6144
	ds_read_b128 v[224:227], v222 offset:7168
	global_load_lds_dwordx4 v194, s[6:7]
	v_add_u32_e32 v194, s60, v220
	s_add_i32 m0, s45, 0xe000
	s_nop 0
	global_load_lds_dwordx4 v194, s[6:7]
	s_waitcnt vmcnt(8)
	s_waitcnt lgkmcnt(0)
	s_barrier
	s_setprio 1
	s_waitcnt lgkmcnt(0)
	v_mfma_f32_16x16x32_bf16 v[126:129], v[138:141], v[162:165], 0
	v_mfma_f32_16x16x32_bf16 v[122:125], v[134:137], v[162:165], 0
	v_mfma_f32_16x16x32_bf16 v[110:113], v[138:141], v[170:173], 0
	v_mfma_f32_16x16x32_bf16 v[106:109], v[134:137], v[170:173], 0
	v_mfma_f32_16x16x32_bf16 v[94:97], v[138:141], v[182:185], 0
	v_mfma_f32_16x16x32_bf16 v[90:93], v[134:137], v[182:185], 0
	v_mfma_f32_16x16x32_bf16 v[78:81], v[138:141], v[190:193], 0
	v_mfma_f32_16x16x32_bf16 v[74:77], v[134:137], v[190:193], 0
	v_mfma_f32_16x16x32_bf16 v[126:129], v[130:133], v[166:169], v[126:129]
	v_mfma_f32_16x16x32_bf16 v[122:125], v[146:149], v[166:169], v[122:125]
	v_mfma_f32_16x16x32_bf16 v[110:113], v[130:133], v[174:177], v[110:113]
	v_mfma_f32_16x16x32_bf16 v[106:109], v[146:149], v[174:177], v[106:109]
	v_mfma_f32_16x16x32_bf16 v[94:97], v[130:133], v[186:189], v[94:97]
	v_mfma_f32_16x16x32_bf16 v[90:93], v[146:149], v[186:189], v[90:93]
	v_mfma_f32_16x16x32_bf16 v[78:81], v[130:133], v[224:227], v[78:81]
	v_mfma_f32_16x16x32_bf16 v[74:77], v[146:149], v[224:227], v[74:77]
	s_setprio 0
	s_setprio 1
	v_mfma_f32_16x16x32_bf16 v[118:121], v[142:145], v[162:165], 0
	v_mfma_f32_16x16x32_bf16 v[114:117], v[154:157], v[162:165], 0
	v_mfma_f32_16x16x32_bf16 v[102:105], v[142:145], v[170:173], 0
	v_mfma_f32_16x16x32_bf16 v[98:101], v[154:157], v[170:173], 0
	v_mfma_f32_16x16x32_bf16 v[86:89], v[142:145], v[182:185], 0
	v_mfma_f32_16x16x32_bf16 v[82:85], v[154:157], v[182:185], 0
	v_mfma_f32_16x16x32_bf16 v[70:73], v[142:145], v[190:193], 0
	v_mfma_f32_16x16x32_bf16 v[66:69], v[154:157], v[190:193], 0
	v_mfma_f32_16x16x32_bf16 v[118:121], v[150:153], v[166:169], v[118:121]
	v_mfma_f32_16x16x32_bf16 v[114:117], v[158:161], v[166:169], v[114:117]
	v_mfma_f32_16x16x32_bf16 v[102:105], v[150:153], v[174:177], v[102:105]
	v_mfma_f32_16x16x32_bf16 v[98:101], v[158:161], v[174:177], v[98:101]
	v_mfma_f32_16x16x32_bf16 v[86:89], v[150:153], v[186:189], v[86:89]
	v_mfma_f32_16x16x32_bf16 v[82:85], v[158:161], v[186:189], v[82:85]
	v_mfma_f32_16x16x32_bf16 v[70:73], v[150:153], v[224:227], v[70:73]
	v_mfma_f32_16x16x32_bf16 v[66:69], v[158:161], v[224:227], v[66:69]
	s_setprio 0
	s_barrier
	s_mov_b32 m0, s66
	v_add_u32_e32 v194, s75, v196
	ds_read_b128 v[162:165], v222 offset:16384
	ds_read_b128 v[166:169], v222 offset:17408
	ds_read_b128 v[170:173], v222 offset:18432
	ds_read_b128 v[174:177], v222 offset:19456
	ds_read_b128 v[182:185], v222 offset:20480
	ds_read_b128 v[186:189], v222 offset:21504
	ds_read_b128 v[190:193], v222 offset:22528
	ds_read_b128 v[224:227], v222 offset:23552
	global_load_lds_dwordx4 v194, s[8:9]
	v_add_u32_e32 v194, s44, v194
	s_mov_b32 m0, s67
	s_nop 0
	global_load_lds_dwordx4 v194, s[8:9]
	v_add_u32_e32 v194, s75, v197
	s_mov_b32 m0, s68
	s_nop 0
	global_load_lds_dwordx4 v194, s[8:9]
	v_add_u32_e32 v194, s44, v194
	s_mov_b32 m0, s69
	s_nop 0
	global_load_lds_dwordx4 v194, s[8:9]
	v_add_u32_e32 v194, s65, v1
	s_mov_b32 m0, s45
	s_nop 0
	global_load_lds_dwordx4 v194, s[6:7]
	v_add_u32_e32 v194, s35, v194
	s_mov_b32 m0, s70
	s_nop 0
	global_load_lds_dwordx4 v194, s[6:7]
	s_waitcnt vmcnt(8)
	s_waitcnt lgkmcnt(0)
	s_barrier
	s_setprio 1
	s_waitcnt lgkmcnt(0)
	v_mfma_f32_16x16x32_bf16 v[62:65], v[138:141], v[162:165], 0
	v_mfma_f32_16x16x32_bf16 v[58:61], v[134:137], v[162:165], 0
	v_mfma_f32_16x16x32_bf16 v[46:49], v[138:141], v[170:173], 0
	v_mfma_f32_16x16x32_bf16 v[42:45], v[134:137], v[170:173], 0
	v_mfma_f32_16x16x32_bf16 v[30:33], v[138:141], v[182:185], 0
	v_mfma_f32_16x16x32_bf16 v[26:29], v[134:137], v[182:185], 0
	v_mfma_f32_16x16x32_bf16 v[14:17], v[138:141], v[190:193], 0
	v_mfma_f32_16x16x32_bf16 v[10:13], v[134:137], v[190:193], 0
	v_mfma_f32_16x16x32_bf16 v[62:65], v[130:133], v[166:169], v[62:65]
	v_mfma_f32_16x16x32_bf16 v[58:61], v[146:149], v[166:169], v[58:61]
	v_mfma_f32_16x16x32_bf16 v[46:49], v[130:133], v[174:177], v[46:49]
	v_mfma_f32_16x16x32_bf16 v[42:45], v[146:149], v[174:177], v[42:45]
	v_mfma_f32_16x16x32_bf16 v[30:33], v[130:133], v[186:189], v[30:33]
	v_mfma_f32_16x16x32_bf16 v[26:29], v[146:149], v[186:189], v[26:29]
	v_mfma_f32_16x16x32_bf16 v[14:17], v[130:133], v[224:227], v[14:17]
	v_mfma_f32_16x16x32_bf16 v[10:13], v[146:149], v[224:227], v[10:13]
	s_setprio 0
	s_setprio 1
	v_mfma_f32_16x16x32_bf16 v[54:57], v[142:145], v[162:165], 0
	v_mfma_f32_16x16x32_bf16 v[50:53], v[154:157], v[162:165], 0
	v_mfma_f32_16x16x32_bf16 v[38:41], v[142:145], v[170:173], 0
	v_mfma_f32_16x16x32_bf16 v[34:37], v[154:157], v[170:173], 0
	v_mfma_f32_16x16x32_bf16 v[22:25], v[142:145], v[182:185], 0
	v_mfma_f32_16x16x32_bf16 v[18:21], v[154:157], v[182:185], 0
	v_mfma_f32_16x16x32_bf16 v[6:9], v[142:145], v[190:193], 0
	v_mfma_f32_16x16x32_bf16 v[2:5], v[154:157], v[190:193], 0
	v_mfma_f32_16x16x32_bf16 v[54:57], v[150:153], v[166:169], v[54:57]
	v_mfma_f32_16x16x32_bf16 v[50:53], v[158:161], v[166:169], v[50:53]
	v_mfma_f32_16x16x32_bf16 v[38:41], v[150:153], v[174:177], v[38:41]
	v_mfma_f32_16x16x32_bf16 v[34:37], v[158:161], v[174:177], v[34:37]
	v_mfma_f32_16x16x32_bf16 v[22:25], v[150:153], v[186:189], v[22:25]
	v_mfma_f32_16x16x32_bf16 v[18:21], v[158:161], v[186:189], v[18:21]
	v_mfma_f32_16x16x32_bf16 v[6:9], v[150:153], v[224:227], v[6:9]
	v_mfma_f32_16x16x32_bf16 v[2:5], v[158:161], v[224:227], v[2:5]
	s_setprio 0
	s_barrier
	s_branch .Lmid_9

.Lmid_9:
	ds_read_b128 v[130:133], v214
	ds_read_b128 v[134:137], v215
	ds_read_b128 v[138:141], v204
	ds_read_b128 v[142:145], v205
	ds_read_b128 v[146:149], v216
	ds_read_b128 v[150:153], v217
	ds_read_b128 v[154:157], v218
	ds_read_b128 v[158:161], v219
	s_mov_b32 m0, s71
	v_add_u32_e32 v194, s65, v198
	ds_read_b128 v[162:165], v222 offset:32768
	ds_read_b128 v[166:169], v222 offset:33792
	ds_read_b128 v[170:173], v222 offset:34816
	ds_read_b128 v[174:177], v222 offset:35840
	ds_read_b128 v[182:185], v222 offset:36864
	ds_read_b128 v[186:189], v222 offset:37888
	ds_read_b128 v[190:193], v222 offset:38912
	ds_read_b128 v[224:227], v222 offset:39936
	global_load_lds_dwordx4 v194, s[6:7]
	v_add_u32_e32 v194, s35, v194
	s_mov_b32 m0, s72
	s_nop 0
	global_load_lds_dwordx4 v194, s[6:7]
	s_waitcnt vmcnt(8)
	s_waitcnt lgkmcnt(0)
	s_barrier
	s_setprio 1
	s_waitcnt lgkmcnt(0)
	v_mfma_f32_16x16x32_bf16 v[126:129], v[138:141], v[162:165], v[126:129]
	v_mfma_f32_16x16x32_bf16 v[122:125], v[134:137], v[162:165], v[122:125]
	v_mfma_f32_16x16x32_bf16 v[110:113], v[138:141], v[170:173], v[110:113]
	v_mfma_f32_16x16x32_bf16 v[106:109], v[134:137], v[170:173], v[106:109]
	v_mfma_f32_16x16x32_bf16 v[94:97], v[138:141], v[182:185], v[94:97]
	v_mfma_f32_16x16x32_bf16 v[90:93], v[134:137], v[182:185], v[90:93]
	v_mfma_f32_16x16x32_bf16 v[78:81], v[138:141], v[190:193], v[78:81]
	v_mfma_f32_16x16x32_bf16 v[74:77], v[134:137], v[190:193], v[74:77]
	v_mfma_f32_16x16x32_bf16 v[126:129], v[130:133], v[166:169], v[126:129]
	v_mfma_f32_16x16x32_bf16 v[122:125], v[146:149], v[166:169], v[122:125]
	v_mfma_f32_16x16x32_bf16 v[110:113], v[130:133], v[174:177], v[110:113]
	v_mfma_f32_16x16x32_bf16 v[106:109], v[146:149], v[174:177], v[106:109]
	v_mfma_f32_16x16x32_bf16 v[94:97], v[130:133], v[186:189], v[94:97]
	v_mfma_f32_16x16x32_bf16 v[90:93], v[146:149], v[186:189], v[90:93]
	v_mfma_f32_16x16x32_bf16 v[78:81], v[130:133], v[224:227], v[78:81]
	v_mfma_f32_16x16x32_bf16 v[74:77], v[146:149], v[224:227], v[74:77]
	s_setprio 0
	s_setprio 1
	v_mfma_f32_16x16x32_bf16 v[118:121], v[142:145], v[162:165], v[118:121]
	v_mfma_f32_16x16x32_bf16 v[114:117], v[154:157], v[162:165], v[114:117]
	v_mfma_f32_16x16x32_bf16 v[102:105], v[142:145], v[170:173], v[102:105]
	v_mfma_f32_16x16x32_bf16 v[98:101], v[154:157], v[170:173], v[98:101]
	v_mfma_f32_16x16x32_bf16 v[86:89], v[142:145], v[182:185], v[86:89]
	v_mfma_f32_16x16x32_bf16 v[82:85], v[154:157], v[182:185], v[82:85]
	v_mfma_f32_16x16x32_bf16 v[70:73], v[142:145], v[190:193], v[70:73]
	v_mfma_f32_16x16x32_bf16 v[66:69], v[154:157], v[190:193], v[66:69]
	v_mfma_f32_16x16x32_bf16 v[118:121], v[150:153], v[166:169], v[118:121]
	v_mfma_f32_16x16x32_bf16 v[114:117], v[158:161], v[166:169], v[114:117]
	v_mfma_f32_16x16x32_bf16 v[102:105], v[150:153], v[174:177], v[102:105]
	v_mfma_f32_16x16x32_bf16 v[98:101], v[158:161], v[174:177], v[98:101]
	v_mfma_f32_16x16x32_bf16 v[86:89], v[150:153], v[186:189], v[86:89]
	v_mfma_f32_16x16x32_bf16 v[82:85], v[158:161], v[186:189], v[82:85]
	v_mfma_f32_16x16x32_bf16 v[70:73], v[150:153], v[224:227], v[70:73]
	v_mfma_f32_16x16x32_bf16 v[66:69], v[158:161], v[224:227], v[66:69]
	s_setprio 0
	s_barrier
	s_addk_i32 s75, 0x80
	s_mov_b32 m0, s77
	v_add_u32_e32 v194, s75, v196
	ds_read_b128 v[162:165], v222 offset:49152
	ds_read_b128 v[166:169], v222 offset:50176
	ds_read_b128 v[170:173], v222 offset:51200
	ds_read_b128 v[174:177], v222 offset:52224
	ds_read_b128 v[182:185], v222 offset:53248
	ds_read_b128 v[186:189], v222 offset:54272
	ds_read_b128 v[190:193], v222 offset:55296
	ds_read_b128 v[224:227], v222 offset:56320
	global_load_lds_dwordx4 v194, s[8:9]
	v_add_u32_e32 v194, s44, v194
	s_mov_b32 m0, s78
	s_nop 0
	global_load_lds_dwordx4 v194, s[8:9]
	v_add_u32_e32 v194, s75, v197
	s_mov_b32 m0, s81
	s_nop 0
	global_load_lds_dwordx4 v194, s[8:9]
	v_add_u32_e32 v194, s44, v194
	s_mov_b32 m0, s82
	s_nop 0
	global_load_lds_dwordx4 v194, s[8:9]
	v_add_u32_e32 v194, s65, v201
	s_mov_b32 m0, s79
	s_nop 0
	global_load_lds_dwordx4 v194, s[6:7]
	v_add_u32_e32 v194, s35, v194
	s_mov_b32 m0, s80
	s_nop 0
	global_load_lds_dwordx4 v194, s[6:7]
	s_waitcnt vmcnt(8)
	s_waitcnt lgkmcnt(0)
	s_barrier
	s_setprio 1
	s_waitcnt lgkmcnt(0)
	v_mfma_f32_16x16x32_bf16 v[62:65], v[138:141], v[162:165], v[62:65]
	v_mfma_f32_16x16x32_bf16 v[58:61], v[134:137], v[162:165], v[58:61]
	v_mfma_f32_16x16x32_bf16 v[46:49], v[138:141], v[170:173], v[46:49]
	v_mfma_f32_16x16x32_bf16 v[42:45], v[134:137], v[170:173], v[42:45]
	v_mfma_f32_16x16x32_bf16 v[30:33], v[138:141], v[182:185], v[30:33]
	v_mfma_f32_16x16x32_bf16 v[26:29], v[134:137], v[182:185], v[26:29]
	v_mfma_f32_16x16x32_bf16 v[14:17], v[138:141], v[190:193], v[14:17]
	v_mfma_f32_16x16x32_bf16 v[10:13], v[134:137], v[190:193], v[10:13]
	v_mfma_f32_16x16x32_bf16 v[62:65], v[130:133], v[166:169], v[62:65]
	v_mfma_f32_16x16x32_bf16 v[58:61], v[146:149], v[166:169], v[58:61]
	v_mfma_f32_16x16x32_bf16 v[46:49], v[130:133], v[174:177], v[46:49]
	v_mfma_f32_16x16x32_bf16 v[42:45], v[146:149], v[174:177], v[42:45]
	v_mfma_f32_16x16x32_bf16 v[30:33], v[130:133], v[186:189], v[30:33]
	v_mfma_f32_16x16x32_bf16 v[26:29], v[146:149], v[186:189], v[26:29]
	v_mfma_f32_16x16x32_bf16 v[14:17], v[130:133], v[224:227], v[14:17]
	v_mfma_f32_16x16x32_bf16 v[10:13], v[146:149], v[224:227], v[10:13]
	s_setprio 0
	s_setprio 1
	v_mfma_f32_16x16x32_bf16 v[54:57], v[142:145], v[162:165], v[54:57]
	v_mfma_f32_16x16x32_bf16 v[50:53], v[154:157], v[162:165], v[50:53]
	v_mfma_f32_16x16x32_bf16 v[38:41], v[142:145], v[170:173], v[38:41]
	v_mfma_f32_16x16x32_bf16 v[34:37], v[154:157], v[170:173], v[34:37]
	v_mfma_f32_16x16x32_bf16 v[22:25], v[142:145], v[182:185], v[22:25]
	v_mfma_f32_16x16x32_bf16 v[18:21], v[154:157], v[182:185], v[18:21]
	v_mfma_f32_16x16x32_bf16 v[6:9], v[142:145], v[190:193], v[6:9]
	v_mfma_f32_16x16x32_bf16 v[2:5], v[154:157], v[190:193], v[2:5]
	v_mfma_f32_16x16x32_bf16 v[54:57], v[150:153], v[166:169], v[54:57]
	v_mfma_f32_16x16x32_bf16 v[50:53], v[158:161], v[166:169], v[50:53]
	v_mfma_f32_16x16x32_bf16 v[38:41], v[150:153], v[174:177], v[38:41]
	v_mfma_f32_16x16x32_bf16 v[34:37], v[158:161], v[174:177], v[34:37]
	v_mfma_f32_16x16x32_bf16 v[22:25], v[150:153], v[186:189], v[22:25]
	v_mfma_f32_16x16x32_bf16 v[18:21], v[158:161], v[186:189], v[18:21]
	v_mfma_f32_16x16x32_bf16 v[6:9], v[150:153], v[224:227], v[6:9]
	v_mfma_f32_16x16x32_bf16 v[2:5], v[158:161], v[224:227], v[2:5]
	s_setprio 0
	s_barrier
	s_add_i32 s64, s64, 2
	s_addk_i32 s60, 0x100
	s_addk_i32 s63, 0x100
	s_cmp_ge_i32 s64, s74
	s_cbranch_scc0 .LBB0_2597

.LBB0_2935:
	s_andn2_b64 vcc, exec, s[14:15]
	v_mov_b64_e32 v[2:3], 0
	v_mov_b64_e32 v[4:5], 0
	v_mov_b64_e32 v[6:7], 0
	v_mov_b64_e32 v[8:9], 0
	v_mov_b64_e32 v[10:11], 0
	v_mov_b64_e32 v[12:13], 0
	v_mov_b64_e32 v[14:15], 0
	v_mov_b64_e32 v[16:17], 0
	v_mov_b64_e32 v[18:19], 0
	v_mov_b64_e32 v[20:21], 0
	v_mov_b64_e32 v[22:23], 0
	v_mov_b64_e32 v[24:25], 0
	v_mov_b64_e32 v[26:27], 0
	v_mov_b64_e32 v[28:29], 0
	v_mov_b64_e32 v[30:31], 0
	v_mov_b64_e32 v[32:33], 0
	v_mov_b64_e32 v[164:165], 0
	v_mov_b64_e32 v[166:167], 0
	v_mov_b64_e32 v[168:169], 0
	v_mov_b64_e32 v[170:171], 0
	v_mov_b64_e32 v[172:173], 0
	v_mov_b64_e32 v[174:175], 0
	s_cbranch_vccnz .Lzs_12
	s_add_i32 s28, s82, 0x80
	s_add_i32 s82, s83, 0x100
	s_mov_b32 s83, 0
	ds_read_b128 v[18:21], v180
	ds_read_b128 v[22:25], v181
	ds_read_b128 v[26:29], v188
	ds_read_b128 v[30:33], v189
	ds_read_b128 v[2:5], v182
	ds_read_b128 v[6:9], v183
	ds_read_b128 v[10:13], v190
	ds_read_b128 v[14:17], v191
	s_add_i32 s84, s28, 0x80
	s_cmp_eq_u32 s67, s83
	s_cselect_b32 s86, s25, s84
	s_cselect_b32 s87, s29, s82
	s_add_i32 s84, s86, 0x80
	s_add_i32 s85, s87, 0x80
	v_mov_b32_e32 v172, v176
	ds_read_b128 v[164:167], v196
	ds_read_b128 v[168:171], v196 offset:1024
	ds_read_b128 v[198:201], v196 offset:2048
	ds_read_b128 v[202:205], v196 offset:3072
	ds_read_b128 v[214:217], v196 offset:4096
	ds_read_b128 v[218:221], v196 offset:5120
	ds_read_b128 v[222:225], v196 offset:6144
	ds_read_b128 v[226:229], v196 offset:7168
	s_add_i32 s88, s28, s65
	v_add_u32_e32 v172, s88, v172
	s_add_i32 m0, s49, 0xc000
	s_add_i32 s88, s28, s70
	global_load_lds_dwordx4 v172, s[4:5]
	v_mov_b32_e32 v172, v176
	s_add_i32 m0, s49, 0xe000
	v_add_u32_e32 v172, s88, v172
	global_load_lds_dwordx4 v172, s[4:5]
	s_waitcnt vmcnt(8)
	s_waitcnt lgkmcnt(0)
	s_barrier
	s_setprio 1
	s_waitcnt lgkmcnt(0)
	v_mfma_f32_16x16x128_f8f6f4 v[158:161], v[18:25], v[164:171], 0
	v_mfma_f32_16x16x128_f8f6f4 v[154:157], v[26:33], v[164:171], 0
	v_mfma_f32_16x16x128_f8f6f4 v[150:153], v[18:25], v[198:205], 0
	v_mfma_f32_16x16x128_f8f6f4 v[146:149], v[26:33], v[198:205], 0
	v_mfma_f32_16x16x128_f8f6f4 v[138:141], v[18:25], v[214:221], 0
	v_mfma_f32_16x16x128_f8f6f4 v[130:133], v[26:33], v[214:221], 0
	v_mfma_f32_16x16x128_f8f6f4 v[122:125], v[18:25], v[222:229], 0
	v_mfma_f32_16x16x128_f8f6f4 v[114:117], v[26:33], v[222:229], 0
	s_setprio 0
	s_setprio 1
	v_mfma_f32_16x16x128_f8f6f4 v[142:145], v[2:9], v[164:171], 0
	v_mfma_f32_16x16x128_f8f6f4 v[134:137], v[10:17], v[164:171], 0
	v_mfma_f32_16x16x128_f8f6f4 v[126:129], v[2:9], v[198:205], 0
	v_mfma_f32_16x16x128_f8f6f4 v[118:121], v[10:17], v[198:205], 0
	v_mfma_f32_16x16x128_f8f6f4 v[110:113], v[2:9], v[214:221], 0
	v_mfma_f32_16x16x128_f8f6f4 v[106:109], v[10:17], v[214:221], 0
	v_mfma_f32_16x16x128_f8f6f4 v[102:105], v[2:9], v[222:229], 0
	v_mfma_f32_16x16x128_f8f6f4 v[98:101], v[10:17], v[222:229], 0
	s_setprio 0
	s_barrier
	v_mov_b32_e32 v172, v177
	ds_read_b128 v[164:167], v196 offset:16384
	ds_read_b128 v[168:171], v196 offset:17408
	ds_read_b128 v[198:201], v196 offset:18432
	ds_read_b128 v[202:205], v196 offset:19456
	ds_read_b128 v[214:217], v196 offset:20480
	ds_read_b128 v[218:221], v196 offset:21504
	ds_read_b128 v[222:225], v196 offset:22528
	ds_read_b128 v[226:229], v196 offset:23552
	s_mov_b32 m0, s50
	v_add_u32_e32 v172, s87, v172
	global_load_lds_dwordx4 v172, s[6:7]
	v_mov_b32_e32 v172, v177
	s_add_i32 s87, s87, s48
	v_add_u32_e32 v172, s87, v172
	s_mov_b32 m0, s51
	s_add_i32 s87, s87, s48
	global_load_lds_dwordx4 v172, s[6:7]
	v_mov_b32_e32 v172, v177
	s_mov_b32 m0, s52
	v_add_u32_e32 v172, s87, v172
	global_load_lds_dwordx4 v172, s[6:7]
	v_mov_b32_e32 v172, v177
	s_add_i32 s87, s87, s48
	v_add_u32_e32 v172, s87, v172
	s_mov_b32 m0, s53
	s_nop 0
	global_load_lds_dwordx4 v172, s[6:7]
	v_mov_b32_e32 v172, v176
	s_mov_b32 m0, s49
	v_add_u32_e32 v172, s86, v172
	global_load_lds_dwordx4 v172, s[4:5]
	v_mov_b32_e32 v172, v176
	s_add_i32 s86, s86, s47
	v_add_u32_e32 v172, s86, v172
	s_mov_b32 m0, s54
	s_nop 0
	global_load_lds_dwordx4 v172, s[4:5]
	s_waitcnt vmcnt(8)
	s_waitcnt lgkmcnt(0)
	s_barrier
	s_setprio 1
	s_waitcnt lgkmcnt(0)
	v_mfma_f32_16x16x128_f8f6f4 v[94:97], v[18:25], v[164:171], 0
	v_mfma_f32_16x16x128_f8f6f4 v[90:93], v[26:33], v[164:171], 0
	v_mfma_f32_16x16x128_f8f6f4 v[86:89], v[18:25], v[198:205], 0
	v_mfma_f32_16x16x128_f8f6f4 v[82:85], v[26:33], v[198:205], 0
	v_mfma_f32_16x16x128_f8f6f4 v[74:77], v[18:25], v[214:221], 0
	v_mfma_f32_16x16x128_f8f6f4 v[66:69], v[26:33], v[214:221], 0
	v_mfma_f32_16x16x128_f8f6f4 v[58:61], v[18:25], v[222:229], 0
	v_mfma_f32_16x16x128_f8f6f4 v[50:53], v[26:33], v[222:229], 0
	s_setprio 0
	s_setprio 1
	v_mfma_f32_16x16x128_f8f6f4 v[78:81], v[2:9], v[164:171], 0
	v_mfma_f32_16x16x128_f8f6f4 v[70:73], v[10:17], v[164:171], 0
	v_mfma_f32_16x16x128_f8f6f4 v[62:65], v[2:9], v[198:205], 0
	v_mfma_f32_16x16x128_f8f6f4 v[54:57], v[10:17], v[198:205], 0
	v_mfma_f32_16x16x128_f8f6f4 v[46:49], v[2:9], v[214:221], 0
	v_mfma_f32_16x16x128_f8f6f4 v[42:45], v[10:17], v[214:221], 0
	v_mfma_f32_16x16x128_f8f6f4 v[38:41], v[2:9], v[222:229], 0
	v_mfma_f32_16x16x128_f8f6f4 v[34:37], v[10:17], v[222:229], 0
	s_setprio 0
	s_barrier
	s_branch .Lmid_10

.Lmid_10:
	s_cmp_lg_u64 s[2:3], 0
	s_cbranch_scc0 .Ltx23_skip
	v_readfirstlane_b32 s23, v230
	s_mul_i32 s23, s23, 44
	s_add_i32 s23, s23, s79
	s_lshl_b32 s23, s23, 19
	s_mov_b32 s29, s23

.LBB0_3005:
	s_andn2_b64 vcc, exec, s[12:13]
	v_mov_b64_e32 v[2:3], 0
	v_mov_b64_e32 v[4:5], 0
	v_mov_b64_e32 v[6:7], 0
	v_mov_b64_e32 v[8:9], 0
	v_mov_b64_e32 v[10:11], 0
	v_mov_b64_e32 v[12:13], 0
	v_mov_b64_e32 v[14:15], 0
	v_mov_b64_e32 v[16:17], 0
	v_mov_b64_e32 v[18:19], 0
	v_mov_b64_e32 v[20:21], 0
	v_mov_b64_e32 v[22:23], 0
	v_mov_b64_e32 v[24:25], 0
	v_mov_b64_e32 v[26:27], 0
	v_mov_b64_e32 v[28:29], 0
	v_mov_b64_e32 v[30:31], 0
	v_mov_b64_e32 v[32:33], 0
	s_cbranch_vccnz .Lzs_13
	s_add_i32 s20, s74, 0x80
	s_add_i32 s74, s75, 0x100
	s_mov_b32 s75, 0
	ds_read_b128 v[18:21], v168
	ds_read_b128 v[22:25], v169
	ds_read_b128 v[26:29], v176
	ds_read_b128 v[30:33], v177
	ds_read_b128 v[2:5], v170
	ds_read_b128 v[6:9], v171
	ds_read_b128 v[10:13], v178
	ds_read_b128 v[14:17], v179
	s_add_i32 s76, s20, 0x80
	s_cmp_eq_u32 s61, s75
	s_cselect_b32 s78, s11, s76
	s_cselect_b32 s77, s21, s74
	s_add_i32 s76, s78, 0x80
	v_mov_b32_e32 v185, v164
	ds_read_b128 v[186:189], v184
	ds_read_b128 v[190:193], v184 offset:1024
	ds_read_b128 v[194:197], v184 offset:2048
	ds_read_b128 v[198:201], v184 offset:3072
	ds_read_b128 v[202:205], v184 offset:4096
	ds_read_b128 v[206:209], v184 offset:5120
	ds_read_b128 v[214:217], v184 offset:6144
	ds_read_b128 v[218:221], v184 offset:7168
	s_add_i32 s79, s20, s59
	v_add_u32_e32 v185, s79, v185
	s_add_i32 m0, s30, 0xc000
	s_add_i32 s79, s20, s66
	global_load_lds_dwordx4 v185, s[4:5]
	v_mov_b32_e32 v185, v164
	s_add_i32 m0, s30, 0xe000
	v_add_u32_e32 v185, s79, v185
	global_load_lds_dwordx4 v185, s[4:5]
	s_waitcnt vmcnt(8)
	s_waitcnt lgkmcnt(0)
	s_barrier
	s_setprio 1
	s_waitcnt lgkmcnt(0)
	v_mfma_f32_16x16x128_f8f6f4 v[158:161], v[18:25], v[186:193], 0
	v_mfma_f32_16x16x128_f8f6f4 v[154:157], v[26:33], v[186:193], 0
	v_mfma_f32_16x16x128_f8f6f4 v[150:153], v[18:25], v[194:201], 0
	v_mfma_f32_16x16x128_f8f6f4 v[146:149], v[26:33], v[194:201], 0
	v_mfma_f32_16x16x128_f8f6f4 v[138:141], v[18:25], v[202:209], 0
	v_mfma_f32_16x16x128_f8f6f4 v[130:133], v[26:33], v[202:209], 0
	v_mfma_f32_16x16x128_f8f6f4 v[122:125], v[18:25], v[214:221], 0
	v_mfma_f32_16x16x128_f8f6f4 v[114:117], v[26:33], v[214:221], 0
	s_setprio 0
	s_setprio 1
	v_mfma_f32_16x16x128_f8f6f4 v[142:145], v[2:9], v[186:193], 0
	v_mfma_f32_16x16x128_f8f6f4 v[134:137], v[10:17], v[186:193], 0
	v_mfma_f32_16x16x128_f8f6f4 v[126:129], v[2:9], v[194:201], 0
	v_mfma_f32_16x16x128_f8f6f4 v[118:121], v[10:17], v[194:201], 0
	v_mfma_f32_16x16x128_f8f6f4 v[110:113], v[2:9], v[202:209], 0
	v_mfma_f32_16x16x128_f8f6f4 v[106:109], v[10:17], v[202:209], 0
	v_mfma_f32_16x16x128_f8f6f4 v[102:105], v[2:9], v[214:221], 0
	v_mfma_f32_16x16x128_f8f6f4 v[98:101], v[10:17], v[214:221], 0
	s_setprio 0
	s_barrier
	v_mov_b32_e32 v185, v165
	ds_read_b128 v[186:189], v184 offset:16384
	ds_read_b128 v[190:193], v184 offset:17408
	ds_read_b128 v[194:197], v184 offset:18432
	ds_read_b128 v[198:201], v184 offset:19456
	ds_read_b128 v[202:205], v184 offset:20480
	ds_read_b128 v[206:209], v184 offset:21504
	ds_read_b128 v[214:217], v184 offset:22528
	ds_read_b128 v[218:221], v184 offset:23552
	s_mov_b32 m0, s31
	v_add_u32_e32 v185, s77, v185
	global_load_lds_dwordx4 v185, s[6:7]
	v_mov_b32_e32 v185, v165
	s_add_i32 s79, s77, s25
	v_add_u32_e32 v185, s79, v185
	s_mov_b32 m0, s35
	s_add_i32 s79, s79, s25
	global_load_lds_dwordx4 v185, s[6:7]
	v_mov_b32_e32 v185, v165
	s_mov_b32 m0, s44
	v_add_u32_e32 v185, s79, v185
	global_load_lds_dwordx4 v185, s[6:7]
	v_mov_b32_e32 v185, v165
	s_add_i32 s79, s79, s25
	v_add_u32_e32 v185, s79, v185
	s_mov_b32 m0, s45
	s_nop 0
	global_load_lds_dwordx4 v185, s[6:7]
	v_mov_b32_e32 v185, v164
	s_mov_b32 m0, s30
	v_add_u32_e32 v185, s78, v185
	global_load_lds_dwordx4 v185, s[4:5]
	v_mov_b32_e32 v185, v164
	s_add_i32 s78, s78, s24
	v_add_u32_e32 v185, s78, v185
	s_mov_b32 m0, s46
	s_nop 0
	global_load_lds_dwordx4 v185, s[4:5]
	s_waitcnt vmcnt(8)
	s_waitcnt lgkmcnt(0)
	s_barrier
	s_setprio 1
	s_waitcnt lgkmcnt(0)
	v_mfma_f32_16x16x128_f8f6f4 v[94:97], v[18:25], v[186:193], 0
	v_mfma_f32_16x16x128_f8f6f4 v[90:93], v[26:33], v[186:193], 0
	v_mfma_f32_16x16x128_f8f6f4 v[86:89], v[18:25], v[194:201], 0
	v_mfma_f32_16x16x128_f8f6f4 v[82:85], v[26:33], v[194:201], 0
	v_mfma_f32_16x16x128_f8f6f4 v[74:77], v[18:25], v[202:209], 0
	v_mfma_f32_16x16x128_f8f6f4 v[66:69], v[26:33], v[202:209], 0
	v_mfma_f32_16x16x128_f8f6f4 v[58:61], v[18:25], v[214:221], 0
	v_mfma_f32_16x16x128_f8f6f4 v[50:53], v[26:33], v[214:221], 0
	s_setprio 0
	s_setprio 1
	v_mfma_f32_16x16x128_f8f6f4 v[78:81], v[2:9], v[186:193], 0
	v_mfma_f32_16x16x128_f8f6f4 v[70:73], v[10:17], v[186:193], 0
	v_mfma_f32_16x16x128_f8f6f4 v[62:65], v[2:9], v[194:201], 0
	v_mfma_f32_16x16x128_f8f6f4 v[54:57], v[10:17], v[194:201], 0
	v_mfma_f32_16x16x128_f8f6f4 v[46:49], v[2:9], v[202:209], 0
	v_mfma_f32_16x16x128_f8f6f4 v[42:45], v[10:17], v[202:209], 0
	v_mfma_f32_16x16x128_f8f6f4 v[38:41], v[2:9], v[214:221], 0
	v_mfma_f32_16x16x128_f8f6f4 v[34:37], v[10:17], v[214:221], 0
	s_setprio 0
	s_barrier
	s_branch .Lmid_11

.Lmid_11:
	s_cmp_lg_u64 s[2:3], 0
	s_cbranch_scc0 .Ltx24_skip
	v_readfirstlane_b32 s19, v230
	s_lshl_b32 s19, s19, 3
	s_add_i32 s19, s19, s72
	s_mul_i32 s21, s19, 0x160000
	s_mov_b32 s19, s21
